# SGU/conv/pool row reductions: serialised ds_bpermute butterflies replaced by DPP/permlane all-reduce
# speedup vs baseline: 1.0072x; 1.0060x over previous
.LBB0_488:
	s_or_b64 exec, exec, s[20:21]
	s_lshl_b64 s[4:5], s[52:53], 2
	s_add_u32 s13, s18, s4
	s_addc_u32 s21, s19, s5
	v_readlane_b32 s4, v255, 23
	v_readlane_b32 s5, v255, 24
	s_lshl_b64 s[4:5], s[4:5], 2
	s_add_u32 s16, s16, s4
	s_addc_u32 s17, s17, s5
	s_add_u32 s18, s10, 0x27c20000
	s_mul_i32 s4, s12, 0x4400
	s_addc_u32 s19, s11, 0
	s_add_i32 s20, s4, 0
	s_lshl_b64 s[4:5], s[6:7], 2
	v_lshlrev_b32_e32 v2, 3, v144
	s_add_u32 s4, s13, s4
	s_addc_u32 s5, s21, s5
	v_lshlrev_b32_e32 v6, 2, v2
	s_waitcnt lgkmcnt(0)
	s_barrier
	global_load_dwordx4 v[2:5], v6, s[4:5] offset:16
	s_nop 0
	global_load_dwordx4 v[6:9], v6, s[4:5]
	s_add_i32 s7, 0, 0x22000
	v_lshl_add_u32 v161, v0, 5, s7
	ds_read_b128 v[162:165], v161
	ds_read_b128 v[166:169], v161 offset:16
	v_and_b32_e32 v103, 63, v87
	v_and_b32_e32 v105, 31, v87
	v_or_b32_e32 v160, 8, v0
	s_waitcnt lgkmcnt(1)
	v_add_f32_e32 v161, v162, v163
	v_add_f32_e32 v162, v164, v165
	v_add_f32_e32 v161, v161, v162
	s_waitcnt lgkmcnt(0)
	v_add_f32_e32 v162, v166, v167
	v_add_f32_e32 v161, v161, v162
	v_add_f32_e32 v162, v168, v169
	v_add_f32_e32 v161, v162, v161
	v_fmamk_f32 v161, v161, 0x3b000000, v235
	v_rsq_f32_e32 v161, v161
	v_or_b32_e32 v159, 16, v0
	v_or_b32_e32 v150, 24, v0
	v_or_b32_e32 v149, 32, v0
	v_mul_f32_e32 v151, v161, v151
	v_or_b32_e32 v148, 40, v0
	v_or_b32_e32 v147, 48, v0
	v_or_b32_e32 v146, 56, v0
	v_or_b32_e32 v145, 64, v0
	v_or_b32_e32 v143, 0x48, v0
	v_or_b32_e32 v134, 0x50, v0
	v_or_b32_e32 v133, 0x58, v0
	v_or_b32_e32 v132, 0x60, v0
	v_or_b32_e32 v128, 0x68, v0
	v_or_b32_e32 v87, 0x70, v0
	v_or_b32_e32 v49, 0x78, v0
	v_mul_f32_e32 v152, v161, v152
	v_mul_f32_e32 v154, v161, v154
	v_mul_f32_e32 v153, v161, v153
	v_mul_f32_e32 v156, v161, v156
	v_mul_f32_e32 v155, v161, v155
	v_mul_f32_e32 v158, v161, v158
	v_mul_f32_e32 v157, v161, v157
	v_lshlrev_b32_e32 v161, 1, v0
	v_mul_u32_u24_e32 v0, 0x880, v144
	v_add3_u32 v144, s20, v161, v0
	s_ashr_i32 s13, s12, 31
	s_lshl_b64 s[4:5], s[12:13], 15
	v_lshrrev_b32_e32 v106, 5, v103
	s_add_u32 s4, s10, s4
	s_addc_u32 s5, s11, s5
	s_lshl_b32 s23, s12, 4
	s_waitcnt vmcnt(1)
	v_mul_f32_e32 v156, v2, v156
	s_waitcnt vmcnt(0)
	v_mul_f32_e32 v151, v7, v151
	v_mul_f32_e32 v154, v8, v154
	v_cvt_pk_bf16_f32 v151, v151, s0
	v_mul_f32_e32 v153, v9, v153
	ds_write_b16 v144, v151 offset:272
	v_cvt_pk_bf16_f32 v151, v154, s0
	ds_write_b16 v144, v151 offset:544
	v_cvt_pk_bf16_f32 v151, v153, s0
	v_mul_f32_e32 v155, v3, v155
	ds_write_b16 v144, v151 offset:816
	v_cvt_pk_bf16_f32 v151, v156, s0
	v_mul_f32_e32 v158, v4, v158
	ds_write_b16 v144, v151 offset:1088
	v_cvt_pk_bf16_f32 v151, v155, s0
	v_mul_f32_e32 v152, v6, v152
	v_mul_f32_e32 v157, v5, v157
	ds_write_b16 v144, v151 offset:1360
	v_cvt_pk_bf16_f32 v151, v158, s0
	v_cvt_pk_bf16_f32 v152, v152, s0
	ds_write_b16 v144, v151 offset:1632
	v_cvt_pk_bf16_f32 v151, v157, s0
	ds_write_b16 v144, v152
	ds_write_b16 v144, v151 offset:1904
	v_lshl_add_u32 v144, v160, 5, s7
	ds_read_b128 v[152:155], v144
	ds_read_b128 v[162:165], v144 offset:16
	s_waitcnt lgkmcnt(1)
	v_add_f32_e32 v144, v152, v153
	v_add_f32_e32 v151, v154, v155
	v_add_f32_e32 v144, v144, v151
	s_waitcnt lgkmcnt(0)
	v_add_f32_e32 v151, v162, v163
	v_add_f32_e32 v144, v144, v151
	v_add_f32_e32 v151, v164, v165
	v_add_f32_e32 v144, v151, v144
	v_fmamk_f32 v144, v144, 0x3b000000, v235
	v_rsq_f32_e32 v144, v144
	s_nop 0
	v_mul_f32_e32 v135, v144, v135
	v_mul_f32_e32 v136, v144, v136
	v_mul_f32_e32 v135, v7, v135
	v_mul_f32_e32 v138, v144, v138
	v_mul_f32_e32 v137, v144, v137
	v_mul_f32_e32 v140, v144, v140
	v_mul_f32_e32 v139, v144, v139
	v_mul_f32_e32 v142, v144, v142
	v_mul_f32_e32 v141, v144, v141
	v_lshlrev_b32_e32 v144, 1, v160
	v_mul_f32_e32 v138, v8, v138
	v_add3_u32 v144, s20, v144, v0
	v_cvt_pk_bf16_f32 v135, v135, s0
	v_mul_f32_e32 v137, v9, v137
	ds_write_b16 v144, v135 offset:272
	v_cvt_pk_bf16_f32 v135, v138, s0
	v_mul_f32_e32 v140, v2, v140
	ds_write_b16 v144, v135 offset:544
	v_cvt_pk_bf16_f32 v135, v137, s0
	v_mul_f32_e32 v139, v3, v139
	ds_write_b16 v144, v135 offset:816
	v_cvt_pk_bf16_f32 v135, v140, s0
	v_mul_f32_e32 v142, v4, v142
	ds_write_b16 v144, v135 offset:1088
	v_cvt_pk_bf16_f32 v135, v139, s0
	v_mul_f32_e32 v136, v6, v136
	v_mul_f32_e32 v141, v5, v141
	ds_write_b16 v144, v135 offset:1360
	v_cvt_pk_bf16_f32 v135, v142, s0
	v_cvt_pk_bf16_f32 v136, v136, s0
	ds_write_b16 v144, v135 offset:1632
	v_cvt_pk_bf16_f32 v135, v141, s0
	ds_write_b16 v144, v136
	ds_write_b16 v144, v135 offset:1904
	v_lshl_add_u32 v135, v159, 5, s7
	ds_read_b128 v[136:139], v135
	ds_read_b128 v[152:155], v135 offset:16
	s_waitcnt lgkmcnt(1)
	v_add_f32_e32 v135, v136, v137
	v_add_f32_e32 v136, v138, v139
	v_add_f32_e32 v135, v135, v136
	s_waitcnt lgkmcnt(0)
	v_add_f32_e32 v136, v152, v153
	v_add_f32_e32 v135, v135, v136
	v_add_f32_e32 v136, v154, v155
	v_add_f32_e32 v135, v136, v135
	v_fmamk_f32 v135, v135, 0x3b000000, v235
	v_rsq_f32_e32 v135, v135
	s_nop 0
	v_mul_f32_e32 v123, v135, v123
	v_mul_f32_e32 v124, v135, v124
	v_mul_f32_e32 v123, v7, v123
	v_mul_f32_e32 v126, v135, v126
	v_mul_f32_e32 v125, v135, v125
	v_mul_f32_e32 v129, v135, v129
	v_mul_f32_e32 v127, v135, v127
	v_mul_f32_e32 v131, v135, v131
	v_mul_f32_e32 v130, v135, v130
	v_lshlrev_b32_e32 v135, 1, v159
	v_mul_f32_e32 v126, v8, v126
	v_add3_u32 v135, s20, v135, v0
	v_cvt_pk_bf16_f32 v123, v123, s0
	v_mul_f32_e32 v125, v9, v125
	ds_write_b16 v135, v123 offset:272
	v_cvt_pk_bf16_f32 v123, v126, s0
	v_mul_f32_e32 v129, v2, v129
	ds_write_b16 v135, v123 offset:544
	v_cvt_pk_bf16_f32 v123, v125, s0
	v_mul_f32_e32 v127, v3, v127
	ds_write_b16 v135, v123 offset:816
	v_cvt_pk_bf16_f32 v123, v129, s0
	v_mul_f32_e32 v131, v4, v131
	ds_write_b16 v135, v123 offset:1088
	v_cvt_pk_bf16_f32 v123, v127, s0
	v_mul_f32_e32 v124, v6, v124
	v_mul_f32_e32 v130, v5, v130
	ds_write_b16 v135, v123 offset:1360
	v_cvt_pk_bf16_f32 v123, v131, s0
	v_cvt_pk_bf16_f32 v124, v124, s0
	ds_write_b16 v135, v123 offset:1632
	v_cvt_pk_bf16_f32 v123, v130, s0
	ds_write_b16 v135, v124
	ds_write_b16 v135, v123 offset:1904
	v_lshl_add_u32 v123, v150, 5, s7
	ds_read_b128 v[124:127], v123
	ds_read_b128 v[136:139], v123 offset:16
	s_waitcnt lgkmcnt(1)
	v_add_f32_e32 v123, v124, v125
	v_add_f32_e32 v124, v126, v127
	v_add_f32_e32 v123, v123, v124
	s_waitcnt lgkmcnt(0)
	v_add_f32_e32 v124, v136, v137
	v_add_f32_e32 v123, v123, v124
	v_add_f32_e32 v124, v138, v139
	v_add_f32_e32 v123, v124, v123
	v_fmamk_f32 v123, v123, 0x3b000000, v235
	v_rsq_f32_e32 v123, v123
	s_nop 0
	v_mul_f32_e32 v115, v123, v115
	v_mul_f32_e32 v116, v123, v116
	v_mul_f32_e32 v115, v7, v115
	v_mul_f32_e32 v118, v123, v118
	v_mul_f32_e32 v117, v123, v117
	v_mul_f32_e32 v120, v123, v120
	v_mul_f32_e32 v119, v123, v119
	v_mul_f32_e32 v122, v123, v122
	v_mul_f32_e32 v121, v123, v121
	v_lshlrev_b32_e32 v123, 1, v150
	v_mul_f32_e32 v118, v8, v118
	v_add3_u32 v123, s20, v123, v0
	v_cvt_pk_bf16_f32 v115, v115, s0
	v_mul_f32_e32 v117, v9, v117
	ds_write_b16 v123, v115 offset:272
	v_cvt_pk_bf16_f32 v115, v118, s0
	v_mul_f32_e32 v120, v2, v120
	ds_write_b16 v123, v115 offset:544
	v_cvt_pk_bf16_f32 v115, v117, s0
	v_mul_f32_e32 v119, v3, v119
	ds_write_b16 v123, v115 offset:816
	v_cvt_pk_bf16_f32 v115, v120, s0
	v_mul_f32_e32 v122, v4, v122
	ds_write_b16 v123, v115 offset:1088
	v_cvt_pk_bf16_f32 v115, v119, s0
	v_mul_f32_e32 v116, v6, v116
	v_mul_f32_e32 v121, v5, v121
	ds_write_b16 v123, v115 offset:1360
	v_cvt_pk_bf16_f32 v115, v122, s0
	v_cvt_pk_bf16_f32 v116, v116, s0
	ds_write_b16 v123, v115 offset:1632
	v_cvt_pk_bf16_f32 v115, v121, s0
	ds_write_b16 v123, v116
	ds_write_b16 v123, v115 offset:1904
	v_lshl_add_u32 v115, v149, 5, s7
	ds_read_b128 v[116:119], v115
	ds_read_b128 v[120:123], v115 offset:16
	s_waitcnt lgkmcnt(1)
	v_add_f32_e32 v115, v116, v117
	v_add_f32_e32 v116, v118, v119
	v_add_f32_e32 v115, v115, v116
	s_waitcnt lgkmcnt(0)
	v_add_f32_e32 v116, v120, v121
	v_add_f32_e32 v115, v115, v116
	v_add_f32_e32 v116, v122, v123
	v_add_f32_e32 v115, v116, v115
	v_fmamk_f32 v115, v115, 0x3b000000, v235
	v_rsq_f32_e32 v115, v115
	s_nop 0
	v_mul_f32_e32 v107, v115, v107
	v_mul_f32_e32 v108, v115, v108
	v_mul_f32_e32 v107, v7, v107
	v_mul_f32_e32 v110, v115, v110
	v_mul_f32_e32 v109, v115, v109
	v_mul_f32_e32 v112, v115, v112
	v_mul_f32_e32 v111, v115, v111
	v_mul_f32_e32 v114, v115, v114
	v_mul_f32_e32 v113, v115, v113
	v_lshlrev_b32_e32 v115, 1, v149
	v_mul_f32_e32 v110, v8, v110
	v_add3_u32 v115, s20, v115, v0
	v_cvt_pk_bf16_f32 v107, v107, s0
	v_mul_f32_e32 v109, v9, v109
	ds_write_b16 v115, v107 offset:272
	v_cvt_pk_bf16_f32 v107, v110, s0
	v_mul_f32_e32 v112, v2, v112
	ds_write_b16 v115, v107 offset:544
	v_cvt_pk_bf16_f32 v107, v109, s0
	v_mul_f32_e32 v111, v3, v111
	ds_write_b16 v115, v107 offset:816
	v_cvt_pk_bf16_f32 v107, v112, s0
	v_mul_f32_e32 v114, v4, v114
	ds_write_b16 v115, v107 offset:1088
	v_cvt_pk_bf16_f32 v107, v111, s0
	v_mul_f32_e32 v108, v6, v108
	v_mul_f32_e32 v113, v5, v113
	ds_write_b16 v115, v107 offset:1360
	v_cvt_pk_bf16_f32 v107, v114, s0
	v_cvt_pk_bf16_f32 v108, v108, s0
	ds_write_b16 v115, v107 offset:1632
	v_cvt_pk_bf16_f32 v107, v113, s0
	ds_write_b16 v115, v108
	ds_write_b16 v115, v107 offset:1904
	v_lshl_add_u32 v107, v148, 5, s7
	ds_read_b128 v[108:111], v107
	ds_read_b128 v[112:115], v107 offset:16
	s_waitcnt lgkmcnt(1)
	v_add_f32_e32 v107, v108, v109
	v_add_f32_e32 v108, v110, v111
	v_add_f32_e32 v107, v107, v108
	s_waitcnt lgkmcnt(0)
	v_add_f32_e32 v108, v112, v113
	v_add_f32_e32 v107, v107, v108
	v_add_f32_e32 v108, v114, v115
	v_add_f32_e32 v107, v108, v107
	v_fmamk_f32 v107, v107, 0x3b000000, v235
	v_rsq_f32_e32 v107, v107
	s_nop 0
	v_mul_f32_e32 v92, v107, v92
	v_mul_f32_e32 v93, v107, v93
	v_mul_f32_e32 v92, v7, v92
	v_mul_f32_e32 v95, v107, v95
	v_mul_f32_e32 v94, v107, v94
	v_mul_f32_e32 v97, v107, v97
	v_mul_f32_e32 v96, v107, v96
	v_mul_f32_e32 v99, v107, v99
	v_mul_f32_e32 v98, v107, v98
	v_lshlrev_b32_e32 v107, 1, v148
	v_mul_f32_e32 v95, v8, v95
	v_add3_u32 v107, s20, v107, v0
	v_cvt_pk_bf16_f32 v92, v92, s0
	v_mul_f32_e32 v94, v9, v94
	ds_write_b16 v107, v92 offset:272
	v_cvt_pk_bf16_f32 v92, v95, s0
	v_mul_f32_e32 v97, v2, v97
	ds_write_b16 v107, v92 offset:544
	v_cvt_pk_bf16_f32 v92, v94, s0
	v_mul_f32_e32 v96, v3, v96
	ds_write_b16 v107, v92 offset:816
	v_cvt_pk_bf16_f32 v92, v97, s0
	v_mul_f32_e32 v99, v4, v99
	ds_write_b16 v107, v92 offset:1088
	v_cvt_pk_bf16_f32 v92, v96, s0
	v_mul_f32_e32 v93, v6, v93
	v_mul_f32_e32 v98, v5, v98
	ds_write_b16 v107, v92 offset:1360
	v_cvt_pk_bf16_f32 v92, v99, s0
	v_cvt_pk_bf16_f32 v93, v93, s0
	ds_write_b16 v107, v92 offset:1632
	v_cvt_pk_bf16_f32 v92, v98, s0
	ds_write_b16 v107, v93
	ds_write_b16 v107, v92 offset:1904
	v_lshl_add_u32 v96, v147, 5, s7
	ds_read_b128 v[92:95], v96
	ds_read_b128 v[96:99], v96 offset:16
	s_waitcnt lgkmcnt(1)
	v_add_f32_e32 v92, v92, v93
	v_add_f32_e32 v93, v94, v95
	v_add_f32_e32 v92, v92, v93
	s_waitcnt lgkmcnt(0)
	v_add_f32_e32 v93, v96, v97
	v_add_f32_e32 v92, v92, v93
	v_add_f32_e32 v93, v98, v99
	v_add_f32_e32 v92, v93, v92
	v_fmamk_f32 v92, v92, 0x3b000000, v235
	v_rsq_f32_e32 v92, v92
	s_nop 0
	v_mul_f32_e32 v83, v92, v83
	v_mul_f32_e32 v84, v92, v84
	v_mul_f32_e32 v83, v7, v83
	v_mul_f32_e32 v86, v92, v86
	v_mul_f32_e32 v85, v92, v85
	v_mul_f32_e32 v89, v92, v89
	v_mul_f32_e32 v88, v92, v88
	v_mul_f32_e32 v91, v92, v91
	v_mul_f32_e32 v90, v92, v90
	v_lshlrev_b32_e32 v92, 1, v147
	v_mul_f32_e32 v86, v8, v86
	v_add3_u32 v92, s20, v92, v0
	v_cvt_pk_bf16_f32 v83, v83, s0
	v_mul_f32_e32 v85, v9, v85
	ds_write_b16 v92, v83 offset:272
	v_cvt_pk_bf16_f32 v83, v86, s0
	v_mul_f32_e32 v89, v2, v89
	ds_write_b16 v92, v83 offset:544
	v_cvt_pk_bf16_f32 v83, v85, s0
	v_mul_f32_e32 v88, v3, v88
	ds_write_b16 v92, v83 offset:816
	v_cvt_pk_bf16_f32 v83, v89, s0
	v_mul_f32_e32 v91, v4, v91
	ds_write_b16 v92, v83 offset:1088
	v_cvt_pk_bf16_f32 v83, v88, s0
	v_mul_f32_e32 v84, v6, v84
	v_mul_f32_e32 v90, v5, v90
	ds_write_b16 v92, v83 offset:1360
	v_cvt_pk_bf16_f32 v83, v91, s0
	v_cvt_pk_bf16_f32 v84, v84, s0
	ds_write_b16 v92, v83 offset:1632
	v_cvt_pk_bf16_f32 v83, v90, s0
	ds_write_b16 v92, v84
	ds_write_b16 v92, v83 offset:1904
	v_lshl_add_u32 v83, v146, 5, s7
	ds_read_b128 v[88:91], v83
	ds_read_b128 v[92:95], v83 offset:16
	s_waitcnt lgkmcnt(1)
	v_add_f32_e32 v83, v88, v89
	v_add_f32_e32 v84, v90, v91
	v_add_f32_e32 v83, v83, v84
	s_waitcnt lgkmcnt(0)
	v_add_f32_e32 v84, v92, v93
	v_add_f32_e32 v83, v83, v84
	v_add_f32_e32 v84, v94, v95
	v_add_f32_e32 v83, v84, v83
	v_fmamk_f32 v83, v83, 0x3b000000, v235
	v_rsq_f32_e32 v83, v83
	s_nop 0
	v_mul_f32_e32 v75, v83, v75
	v_mul_f32_e32 v76, v83, v76
	v_mul_f32_e32 v75, v7, v75
	v_mul_f32_e32 v78, v83, v78
	v_mul_f32_e32 v77, v83, v77
	v_mul_f32_e32 v80, v83, v80
	v_mul_f32_e32 v79, v83, v79
	v_mul_f32_e32 v82, v83, v82
	v_mul_f32_e32 v81, v83, v81
	v_lshlrev_b32_e32 v83, 1, v146
	v_mul_f32_e32 v78, v8, v78
	v_add3_u32 v83, s20, v83, v0
	v_cvt_pk_bf16_f32 v75, v75, s0
	v_mul_f32_e32 v77, v9, v77
	ds_write_b16 v83, v75 offset:272
	v_cvt_pk_bf16_f32 v75, v78, s0
	v_mul_f32_e32 v80, v2, v80
	ds_write_b16 v83, v75 offset:544
	v_cvt_pk_bf16_f32 v75, v77, s0
	v_mul_f32_e32 v79, v3, v79
	ds_write_b16 v83, v75 offset:816
	v_cvt_pk_bf16_f32 v75, v80, s0
	v_mul_f32_e32 v82, v4, v82
	ds_write_b16 v83, v75 offset:1088
	v_cvt_pk_bf16_f32 v75, v79, s0
	v_mul_f32_e32 v76, v6, v76
	v_mul_f32_e32 v81, v5, v81
	ds_write_b16 v83, v75 offset:1360
	v_cvt_pk_bf16_f32 v75, v82, s0
	v_cvt_pk_bf16_f32 v76, v76, s0
	ds_write_b16 v83, v75 offset:1632
	v_cvt_pk_bf16_f32 v75, v81, s0
	ds_write_b16 v83, v76
	ds_write_b16 v83, v75 offset:1904
	v_lshl_add_u32 v75, v145, 5, s7
	ds_read_b128 v[76:79], v75
	ds_read_b128 v[80:83], v75 offset:16
	s_waitcnt lgkmcnt(1)
	v_add_f32_e32 v75, v76, v77
	v_add_f32_e32 v76, v78, v79
	v_add_f32_e32 v75, v75, v76
	s_waitcnt lgkmcnt(0)
	v_add_f32_e32 v76, v80, v81
	v_add_f32_e32 v75, v75, v76
	v_add_f32_e32 v76, v82, v83
	v_add_f32_e32 v75, v76, v75
	v_fmamk_f32 v75, v75, 0x3b000000, v235
	v_rsq_f32_e32 v75, v75
	s_nop 0
	v_mul_f32_e32 v67, v75, v67
	v_mul_f32_e32 v68, v75, v68
	v_mul_f32_e32 v67, v7, v67
	v_mul_f32_e32 v70, v75, v70
	v_mul_f32_e32 v69, v75, v69
	v_mul_f32_e32 v72, v75, v72
	v_mul_f32_e32 v71, v75, v71
	v_mul_f32_e32 v74, v75, v74
	v_mul_f32_e32 v73, v75, v73
	v_lshlrev_b32_e32 v75, 1, v145
	v_mul_f32_e32 v70, v8, v70
	v_add3_u32 v75, s20, v75, v0
	v_cvt_pk_bf16_f32 v67, v67, s0
	v_mul_f32_e32 v69, v9, v69
	ds_write_b16 v75, v67 offset:272
	v_cvt_pk_bf16_f32 v67, v70, s0
	v_mul_f32_e32 v72, v2, v72
	ds_write_b16 v75, v67 offset:544
	v_cvt_pk_bf16_f32 v67, v69, s0
	v_mul_f32_e32 v71, v3, v71
	ds_write_b16 v75, v67 offset:816
	v_cvt_pk_bf16_f32 v67, v72, s0
	v_mul_f32_e32 v74, v4, v74
	ds_write_b16 v75, v67 offset:1088
	v_cvt_pk_bf16_f32 v67, v71, s0
	v_mul_f32_e32 v68, v6, v68
	v_mul_f32_e32 v73, v5, v73
	ds_write_b16 v75, v67 offset:1360
	v_cvt_pk_bf16_f32 v67, v74, s0
	v_cvt_pk_bf16_f32 v68, v68, s0
	ds_write_b16 v75, v67 offset:1632
	v_cvt_pk_bf16_f32 v67, v73, s0
	ds_write_b16 v75, v68
	ds_write_b16 v75, v67 offset:1904
	v_lshl_add_u32 v67, v143, 5, s7
	ds_read_b128 v[68:71], v67
	ds_read_b128 v[72:75], v67 offset:16
	s_waitcnt lgkmcnt(1)
	v_add_f32_e32 v67, v68, v69
	v_add_f32_e32 v68, v70, v71
	v_add_f32_e32 v67, v67, v68
	s_waitcnt lgkmcnt(0)
	v_add_f32_e32 v68, v72, v73
	v_add_f32_e32 v67, v67, v68
	v_add_f32_e32 v68, v74, v75
	v_add_f32_e32 v67, v68, v67
	v_fmamk_f32 v67, v67, 0x3b000000, v235
	v_rsq_f32_e32 v67, v67
	s_nop 0
	v_mul_f32_e32 v59, v67, v59
	v_mul_f32_e32 v60, v67, v60
	v_mul_f32_e32 v59, v7, v59
	v_mul_f32_e32 v62, v67, v62
	v_mul_f32_e32 v61, v67, v61
	v_mul_f32_e32 v64, v67, v64
	v_mul_f32_e32 v63, v67, v63
	v_mul_f32_e32 v66, v67, v66
	v_mul_f32_e32 v65, v67, v65
	v_lshlrev_b32_e32 v67, 1, v143
	v_mul_f32_e32 v62, v8, v62
	v_add3_u32 v67, s20, v67, v0
	v_cvt_pk_bf16_f32 v59, v59, s0
	v_mul_f32_e32 v61, v9, v61
	ds_write_b16 v67, v59 offset:272
	v_cvt_pk_bf16_f32 v59, v62, s0
	v_mul_f32_e32 v64, v2, v64
	ds_write_b16 v67, v59 offset:544
	v_cvt_pk_bf16_f32 v59, v61, s0
	v_mul_f32_e32 v63, v3, v63
	ds_write_b16 v67, v59 offset:816
	v_cvt_pk_bf16_f32 v59, v64, s0
	v_mul_f32_e32 v66, v4, v66
	ds_write_b16 v67, v59 offset:1088
	v_cvt_pk_bf16_f32 v59, v63, s0
	v_mul_f32_e32 v60, v6, v60
	v_mul_f32_e32 v65, v5, v65
	ds_write_b16 v67, v59 offset:1360
	v_cvt_pk_bf16_f32 v59, v66, s0
	v_cvt_pk_bf16_f32 v60, v60, s0
	ds_write_b16 v67, v59 offset:1632
	v_cvt_pk_bf16_f32 v59, v65, s0
	ds_write_b16 v67, v60
	ds_write_b16 v67, v59 offset:1904
	v_lshl_add_u32 v59, v134, 5, s7
	ds_read_b128 v[60:63], v59
	ds_read_b128 v[64:67], v59 offset:16
	s_waitcnt lgkmcnt(1)
	v_add_f32_e32 v59, v60, v61
	v_add_f32_e32 v60, v62, v63
	v_add_f32_e32 v59, v59, v60
	s_waitcnt lgkmcnt(0)
	v_add_f32_e32 v60, v64, v65
	v_add_f32_e32 v59, v59, v60
	v_add_f32_e32 v60, v66, v67
	v_add_f32_e32 v59, v60, v59
	v_fmamk_f32 v59, v59, 0x3b000000, v235
	v_rsq_f32_e32 v59, v59
	s_nop 0
	v_mul_f32_e32 v51, v59, v51
	v_mul_f32_e32 v52, v59, v52
	v_mul_f32_e32 v51, v7, v51
	v_mul_f32_e32 v54, v59, v54
	v_mul_f32_e32 v53, v59, v53
	v_mul_f32_e32 v56, v59, v56
	v_mul_f32_e32 v55, v59, v55
	v_mul_f32_e32 v58, v59, v58
	v_mul_f32_e32 v57, v59, v57
	v_lshlrev_b32_e32 v59, 1, v134
	v_mul_f32_e32 v54, v8, v54
	v_add3_u32 v59, s20, v59, v0
	v_cvt_pk_bf16_f32 v51, v51, s0
	v_mul_f32_e32 v53, v9, v53
	ds_write_b16 v59, v51 offset:272
	v_cvt_pk_bf16_f32 v51, v54, s0
	v_mul_f32_e32 v56, v2, v56
	ds_write_b16 v59, v51 offset:544
	v_cvt_pk_bf16_f32 v51, v53, s0
	v_mul_f32_e32 v55, v3, v55
	ds_write_b16 v59, v51 offset:816
	v_cvt_pk_bf16_f32 v51, v56, s0
	v_mul_f32_e32 v58, v4, v58
	ds_write_b16 v59, v51 offset:1088
	v_cvt_pk_bf16_f32 v51, v55, s0
	v_mul_f32_e32 v52, v6, v52
	v_mul_f32_e32 v57, v5, v57
	ds_write_b16 v59, v51 offset:1360
	v_cvt_pk_bf16_f32 v51, v58, s0
	v_cvt_pk_bf16_f32 v52, v52, s0
	ds_write_b16 v59, v51 offset:1632
	v_cvt_pk_bf16_f32 v51, v57, s0
	ds_write_b16 v59, v52
	ds_write_b16 v59, v51 offset:1904
	v_lshl_add_u32 v51, v133, 5, s7
	ds_read_b128 v[52:55], v51
	ds_read_b128 v[56:59], v51 offset:16
	s_waitcnt lgkmcnt(1)
	v_add_f32_e32 v51, v52, v53
	v_add_f32_e32 v52, v54, v55
	v_add_f32_e32 v51, v51, v52
	s_waitcnt lgkmcnt(0)
	v_add_f32_e32 v52, v56, v57
	v_add_f32_e32 v51, v51, v52
	v_add_f32_e32 v52, v58, v59
	v_add_f32_e32 v51, v52, v51
	v_fmamk_f32 v51, v51, 0x3b000000, v235
	v_rsq_f32_e32 v51, v51
	s_nop 0
	v_mul_f32_e32 v42, v51, v42
	v_mul_f32_e32 v43, v51, v43
	v_mul_f32_e32 v42, v7, v42
	v_mul_f32_e32 v45, v51, v45
	v_mul_f32_e32 v44, v51, v44
	v_mul_f32_e32 v47, v51, v47
	v_mul_f32_e32 v46, v51, v46
	v_mul_f32_e32 v50, v51, v50
	v_mul_f32_e32 v48, v51, v48
	v_lshlrev_b32_e32 v51, 1, v133
	v_mul_f32_e32 v45, v8, v45
	v_add3_u32 v51, s20, v51, v0
	v_cvt_pk_bf16_f32 v42, v42, s0
	v_mul_f32_e32 v44, v9, v44
	ds_write_b16 v51, v42 offset:272
	v_cvt_pk_bf16_f32 v42, v45, s0
	v_mul_f32_e32 v47, v2, v47
	ds_write_b16 v51, v42 offset:544
	v_cvt_pk_bf16_f32 v42, v44, s0
	v_mul_f32_e32 v46, v3, v46
	ds_write_b16 v51, v42 offset:816
	v_cvt_pk_bf16_f32 v42, v47, s0
	v_mul_f32_e32 v50, v4, v50
	ds_write_b16 v51, v42 offset:1088
	v_cvt_pk_bf16_f32 v42, v46, s0
	v_mul_f32_e32 v43, v6, v43
	v_mul_f32_e32 v48, v5, v48
	ds_write_b16 v51, v42 offset:1360
	v_cvt_pk_bf16_f32 v42, v50, s0
	v_cvt_pk_bf16_f32 v43, v43, s0
	ds_write_b16 v51, v42 offset:1632
	v_cvt_pk_bf16_f32 v42, v48, s0
	ds_write_b16 v51, v43
	ds_write_b16 v51, v42 offset:1904
	v_lshl_add_u32 v46, v132, 5, s7
	ds_read_b128 v[42:45], v46
	ds_read_b128 v[50:53], v46 offset:16
	s_waitcnt lgkmcnt(1)
	v_add_f32_e32 v42, v42, v43
	v_add_f32_e32 v43, v44, v45
	v_add_f32_e32 v42, v42, v43
	s_waitcnt lgkmcnt(0)
	v_add_f32_e32 v43, v50, v51
	v_add_f32_e32 v42, v42, v43
	v_add_f32_e32 v43, v52, v53
	v_add_f32_e32 v42, v43, v42
	v_fmamk_f32 v42, v42, 0x3b000000, v235
	v_rsq_f32_e32 v42, v42
	s_nop 0
	v_mul_f32_e32 v34, v42, v34
	v_mul_f32_e32 v35, v42, v35
	v_mul_f32_e32 v34, v7, v34
	v_mul_f32_e32 v37, v42, v37
	v_mul_f32_e32 v36, v42, v36
	v_mul_f32_e32 v39, v42, v39
	v_mul_f32_e32 v38, v42, v38
	v_mul_f32_e32 v41, v42, v41
	v_mul_f32_e32 v40, v42, v40
	v_lshlrev_b32_e32 v42, 1, v132
	v_mul_f32_e32 v37, v8, v37
	v_add3_u32 v42, s20, v42, v0
	v_cvt_pk_bf16_f32 v34, v34, s0
	v_mul_f32_e32 v36, v9, v36
	ds_write_b16 v42, v34 offset:272
	v_cvt_pk_bf16_f32 v34, v37, s0
	v_mul_f32_e32 v39, v2, v39
	ds_write_b16 v42, v34 offset:544
	v_cvt_pk_bf16_f32 v34, v36, s0
	v_mul_f32_e32 v38, v3, v38
	ds_write_b16 v42, v34 offset:816
	v_cvt_pk_bf16_f32 v34, v39, s0
	v_mul_f32_e32 v41, v4, v41
	ds_write_b16 v42, v34 offset:1088
	v_cvt_pk_bf16_f32 v34, v38, s0
	v_mul_f32_e32 v35, v6, v35
	v_mul_f32_e32 v40, v5, v40
	ds_write_b16 v42, v34 offset:1360
	v_cvt_pk_bf16_f32 v34, v41, s0
	v_cvt_pk_bf16_f32 v35, v35, s0
	ds_write_b16 v42, v34 offset:1632
	v_cvt_pk_bf16_f32 v34, v40, s0
	ds_write_b16 v42, v35
	ds_write_b16 v42, v34 offset:1904
	v_lshl_add_u32 v38, v128, 5, s7
	ds_read_b128 v[34:37], v38
	ds_read_b128 v[38:41], v38 offset:16
	s_waitcnt lgkmcnt(1)
	v_add_f32_e32 v34, v34, v35
	v_add_f32_e32 v35, v36, v37
	v_add_f32_e32 v34, v34, v35
	s_waitcnt lgkmcnt(0)
	v_add_f32_e32 v35, v38, v39
	v_add_f32_e32 v34, v34, v35
	v_add_f32_e32 v35, v40, v41
	v_add_f32_e32 v34, v35, v34
	v_fmamk_f32 v34, v34, 0x3b000000, v235
	v_rsq_f32_e32 v34, v34
	s_nop 0
	v_mul_f32_e32 v26, v34, v26
	v_mul_f32_e32 v27, v34, v27
	v_mul_f32_e32 v26, v7, v26
	v_mul_f32_e32 v29, v34, v29
	v_mul_f32_e32 v28, v34, v28
	v_mul_f32_e32 v31, v34, v31
	v_mul_f32_e32 v30, v34, v30
	v_mul_f32_e32 v33, v34, v33
	v_mul_f32_e32 v32, v34, v32
	v_lshlrev_b32_e32 v34, 1, v128
	v_mul_f32_e32 v29, v8, v29
	v_add3_u32 v34, s20, v34, v0
	v_cvt_pk_bf16_f32 v26, v26, s0
	v_mul_f32_e32 v28, v9, v28
	ds_write_b16 v34, v26 offset:272
	v_cvt_pk_bf16_f32 v26, v29, s0
	v_mul_f32_e32 v31, v2, v31
	ds_write_b16 v34, v26 offset:544
	v_cvt_pk_bf16_f32 v26, v28, s0
	v_mul_f32_e32 v30, v3, v30
	ds_write_b16 v34, v26 offset:816
	v_cvt_pk_bf16_f32 v26, v31, s0
	v_mul_f32_e32 v33, v4, v33
	ds_write_b16 v34, v26 offset:1088
	v_cvt_pk_bf16_f32 v26, v30, s0
	v_mul_f32_e32 v27, v6, v27
	v_mul_f32_e32 v32, v5, v32
	ds_write_b16 v34, v26 offset:1360
	v_cvt_pk_bf16_f32 v26, v33, s0
	v_cvt_pk_bf16_f32 v27, v27, s0
	ds_write_b16 v34, v26 offset:1632
	v_cvt_pk_bf16_f32 v26, v32, s0
	ds_write_b16 v34, v27
	ds_write_b16 v34, v26 offset:1904
	v_lshl_add_u32 v30, v87, 5, s7
	ds_read_b128 v[26:29], v30
	ds_read_b128 v[30:33], v30 offset:16
	s_waitcnt lgkmcnt(1)
	v_add_f32_e32 v26, v26, v27
	v_add_f32_e32 v27, v28, v29
	v_add_f32_e32 v26, v26, v27
	s_waitcnt lgkmcnt(0)
	v_add_f32_e32 v27, v30, v31
	v_add_f32_e32 v26, v26, v27
	v_add_f32_e32 v27, v32, v33
	v_add_f32_e32 v26, v27, v26
	v_fmamk_f32 v26, v26, 0x3b000000, v235
	v_rsq_f32_e32 v26, v26
	s_nop 0
	v_mul_f32_e32 v18, v26, v18
	v_mul_f32_e32 v19, v26, v19
	v_mul_f32_e32 v18, v7, v18
	v_mul_f32_e32 v21, v26, v21
	v_mul_f32_e32 v20, v26, v20
	v_mul_f32_e32 v23, v26, v23
	v_mul_f32_e32 v22, v26, v22
	v_mul_f32_e32 v25, v26, v25
	v_mul_f32_e32 v24, v26, v24
	v_lshlrev_b32_e32 v26, 1, v87
	v_mul_f32_e32 v21, v8, v21
	v_add3_u32 v26, s20, v26, v0
	v_cvt_pk_bf16_f32 v18, v18, s0
	v_mul_f32_e32 v20, v9, v20
	ds_write_b16 v26, v18 offset:272
	v_cvt_pk_bf16_f32 v18, v21, s0
	v_mul_f32_e32 v23, v2, v23
	ds_write_b16 v26, v18 offset:544
	v_cvt_pk_bf16_f32 v18, v20, s0
	v_mul_f32_e32 v22, v3, v22
	ds_write_b16 v26, v18 offset:816
	v_cvt_pk_bf16_f32 v18, v23, s0
	v_mul_f32_e32 v25, v4, v25
	ds_write_b16 v26, v18 offset:1088
	v_cvt_pk_bf16_f32 v18, v22, s0
	v_mul_f32_e32 v19, v6, v19
	v_mul_f32_e32 v24, v5, v24
	ds_write_b16 v26, v18 offset:1360
	v_cvt_pk_bf16_f32 v18, v25, s0
	v_cvt_pk_bf16_f32 v19, v19, s0
	ds_write_b16 v26, v18 offset:1632
	v_cvt_pk_bf16_f32 v18, v24, s0
	ds_write_b16 v26, v19
	ds_write_b16 v26, v18 offset:1904
	v_lshl_add_u32 v22, v49, 5, s7
	ds_read_b128 v[18:21], v22
	ds_read_b128 v[22:25], v22 offset:16
	s_waitcnt lgkmcnt(1)
	v_add_f32_e32 v18, v18, v19
	v_add_f32_e32 v19, v20, v21
	v_add_f32_e32 v18, v18, v19
	s_waitcnt lgkmcnt(0)
	v_add_f32_e32 v19, v22, v23
	v_add_f32_e32 v18, v18, v19
	v_add_f32_e32 v19, v24, v25
	v_add_f32_e32 v18, v19, v18
	v_fmamk_f32 v18, v18, 0x3b000000, v235
	v_rsq_f32_e32 v18, v18
	s_nop 0
	v_mul_f32_e32 v10, v18, v10
	v_mul_f32_e32 v7, v7, v10
	v_mul_f32_e32 v10, v18, v13
	v_mul_f32_e32 v8, v8, v10
	v_mul_f32_e32 v10, v18, v12
	v_mul_f32_e32 v9, v9, v10
	v_mul_f32_e32 v10, v18, v15
	v_mul_f32_e32 v2, v2, v10
	v_mul_f32_e32 v10, v18, v14
	v_mul_f32_e32 v3, v3, v10
	v_mul_f32_e32 v10, v18, v17
	v_mul_f32_e32 v11, v18, v11
	v_mul_f32_e32 v4, v4, v10
	v_mul_f32_e32 v10, v18, v16
	v_mul_f32_e32 v6, v6, v11
	v_mul_f32_e32 v5, v5, v10
	v_lshlrev_b32_e32 v10, 1, v49
	v_cvt_pk_bf16_f32 v6, v6, s0
	v_add3_u32 v0, s20, v10, v0
	v_cvt_pk_bf16_f32 v2, v2, s0
	ds_write_b16 v0, v6
	v_cvt_pk_bf16_f32 v6, v7, s0
	ds_write_b16 v0, v2 offset:1088
	v_cvt_pk_bf16_f32 v2, v3, s0
	ds_write_b16 v0, v6 offset:272
	v_cvt_pk_bf16_f32 v6, v8, s0
	ds_write_b16 v0, v2 offset:1360
	v_cvt_pk_bf16_f32 v2, v4, s0
	ds_write_b16 v0, v6 offset:544
	v_cvt_pk_bf16_f32 v6, v9, s0
	ds_write_b16 v0, v2 offset:1632
	v_cvt_pk_bf16_f32 v2, v5, s0
	ds_write_b16 v0, v6 offset:816
	ds_write_b16 v0, v2 offset:1904
	v_lshlrev_b32_e32 v0, 4, v106
	v_lshlrev_b32_e32 v4, 2, v106
	v_lshl_add_u64 v[2:3], s[4:5], 0, v[0:1]
	v_lshl_or_b32 v54, s12, 7, v4
	v_lshlrev_b32_e32 v4, 8, v105
	v_mov_b32_e32 v5, v1
	v_lshl_add_u64 v[82:83], v[2:3], 0, v[4:5]
	s_mov_b64 s[4:5], 0x1620000
	v_lshl_add_u64 v[6:7], v[82:83], 0, s[4:5]
	s_mov_b32 s4, 0x1620000
	v_add_co_u32_e32 v2, vcc, s4, v82
	s_waitcnt lgkmcnt(0)
	s_nop 0
	v_addc_co_u32_e32 v3, vcc, 0, v83, vcc
	s_barrier
	global_load_dwordx4 v[2:5], v[2:3], off
	s_nop 0
	global_load_dwordx4 v[50:53], v[6:7], off offset:32
	v_mul_u32_u24_e32 v8, 0x110, v105
	v_add3_u32 v0, s20, v8, v0
	ds_read_b128 v[42:45], v0 offset:8704
	ds_read_b128 v[46:49], v0
	ds_read_b128 v[38:41], v0 offset:32
	s_waitcnt vmcnt(1) lgkmcnt(1)
	v_mfma_f32_32x32x16_bf16 v[18:33], v[2:5], v[46:49], 0
	ds_read_b128 v[34:37], v0 offset:8736
	v_ashrrev_i32_e32 v55, 31, v54
	v_lshl_add_u64 v[98:99], v[54:55], 2, s[16:17]
	s_mov_b32 s4, 0x1622000
	v_mfma_f32_32x32x16_bf16 v[2:17], v[2:5], v[42:45], 0
	s_waitcnt vmcnt(0) lgkmcnt(1)
	v_mfma_f32_32x32x16_bf16 v[18:33], v[50:53], v[38:41], v[18:33]
	s_waitcnt lgkmcnt(0)
	v_mfma_f32_32x32x16_bf16 v[2:17], v[50:53], v[34:37], v[2:17]
	global_load_dwordx4 v[50:53], v[98:99], off
	global_load_dwordx4 v[54:57], v[98:99], off offset:32
	global_load_dwordx4 v[58:61], v[98:99], off offset:64
	global_load_dwordx4 v[62:65], v[98:99], off offset:96
	s_nop 5
	v_mov_b32_e32 v66, v18
	s_nop 0
	v_mov_b32_e32 v67, v2
	v_mov_b32_e32 v2, v19
	s_waitcnt vmcnt(3)
	v_pk_add_f32 v[2:3], v[2:3], v[50:51] op_sel:[0,1]
	s_nop 0
	v_cvt_pk_bf16_f32 v108, v2, v3
	v_mov_b32_e32 v2, v20
	v_mov_b32_e32 v3, v4
	v_pk_add_f32 v[2:3], v[2:3], v[52:53] op_sel_hi:[1,0]
	v_mov_b32_e32 v4, v21
	v_cvt_pk_bf16_f32 v109, v2, v3
	v_mov_b32_e32 v2, v53
	v_pk_add_f32 v[2:3], v[4:5], v[2:3] op_sel_hi:[1,0]
	v_pk_add_f32 v[66:67], v[66:67], v[50:51] op_sel_hi:[1,0]
	v_cvt_pk_bf16_f32 v110, v2, v3
	v_mov_b32_e32 v2, v22
	v_mov_b32_e32 v3, v6
	s_waitcnt vmcnt(2)
	v_pk_add_f32 v[2:3], v[2:3], v[54:55] op_sel_hi:[1,0]
	v_mov_b32_e32 v6, v23
	v_cvt_pk_bf16_f32 v111, v2, v3
	v_pk_add_f32 v[2:3], v[6:7], v[54:55] op_sel:[0,1]
	v_add_co_u32_e32 v6, vcc, s4, v82
	v_cvt_pk_bf16_f32 v112, v2, v3
	v_mov_b32_e32 v2, v24
	v_mov_b32_e32 v3, v8
	v_pk_add_f32 v[2:3], v[2:3], v[56:57] op_sel_hi:[1,0]
	v_mov_b32_e32 v8, v25
	v_cvt_pk_bf16_f32 v113, v2, v3
	v_mov_b32_e32 v2, v57
	v_pk_add_f32 v[2:3], v[8:9], v[2:3] op_sel_hi:[1,0]
	v_addc_co_u32_e32 v7, vcc, 0, v83, vcc
	v_cvt_pk_bf16_f32 v114, v2, v3
	v_mov_b32_e32 v2, v26
	v_mov_b32_e32 v3, v10
	s_waitcnt vmcnt(1)
	v_pk_add_f32 v[2:3], v[2:3], v[58:59] op_sel_hi:[1,0]
	v_mov_b32_e32 v10, v27
	v_cvt_pk_bf16_f32 v115, v2, v3
	v_pk_add_f32 v[2:3], v[10:11], v[58:59] op_sel:[0,1]
	v_cvt_pk_bf16_f32 v107, v66, v67
	v_cvt_pk_bf16_f32 v116, v2, v3
	v_mov_b32_e32 v2, v28
	v_mov_b32_e32 v3, v12
	v_pk_add_f32 v[2:3], v[2:3], v[60:61] op_sel_hi:[1,0]
	v_mov_b32_e32 v12, v29
	v_cvt_pk_bf16_f32 v117, v2, v3
	v_mov_b32_e32 v2, v61
	v_pk_add_f32 v[2:3], v[12:13], v[2:3] op_sel_hi:[1,0]
	s_mov_b32 s4, 0x1624000
	v_cvt_pk_bf16_f32 v118, v2, v3
	v_mov_b32_e32 v2, v30
	v_mov_b32_e32 v3, v14
	s_waitcnt vmcnt(0)
	v_pk_add_f32 v[2:3], v[2:3], v[62:63] op_sel_hi:[1,0]
	v_mov_b32_e32 v14, v31
	v_cvt_pk_bf16_f32 v119, v2, v3
	v_pk_add_f32 v[2:3], v[14:15], v[62:63] op_sel:[0,1]
	s_nop 0
	v_cvt_pk_bf16_f32 v120, v2, v3
	v_mov_b32_e32 v2, v32
	v_mov_b32_e32 v3, v16
	v_pk_add_f32 v[2:3], v[2:3], v[64:65] op_sel_hi:[1,0]
	v_mov_b32_e32 v16, v33
	v_cvt_pk_bf16_f32 v121, v2, v3
	v_mov_b32_e32 v2, v65
	v_pk_add_f32 v[2:3], v[16:17], v[2:3] op_sel_hi:[1,0]
	s_nop 0
	v_cvt_pk_bf16_f32 v122, v2, v3
	global_load_dwordx4 v[2:5], v[6:7], off
	global_load_dwordx4 v[50:53], v[6:7], off offset:32
	global_load_dwordx4 v[54:57], v[6:7], off offset:64
	global_load_dwordx4 v[66:69], v[6:7], off offset:96
	s_waitcnt vmcnt(3)
	v_mfma_f32_32x32x16_bf16 v[18:33], v[2:5], v[46:49], 0
	ds_read_b128 v[62:65], v0 offset:64
	ds_read_b128 v[58:61], v0 offset:8768
	v_mfma_f32_32x32x16_bf16 v[2:17], v[2:5], v[42:45], 0
	s_waitcnt vmcnt(2)
	v_mfma_f32_32x32x16_bf16 v[18:33], v[50:53], v[38:41], v[18:33]
	v_mfma_f32_32x32x16_bf16 v[2:17], v[50:53], v[34:37], v[2:17]
	s_waitcnt vmcnt(1) lgkmcnt(1)
	v_mfma_f32_32x32x16_bf16 v[18:33], v[54:57], v[62:65], v[18:33]
	s_waitcnt lgkmcnt(0)
	v_mfma_f32_32x32x16_bf16 v[2:17], v[54:57], v[58:61], v[2:17]
	ds_read_b128 v[50:53], v0 offset:96
	ds_read_b128 v[54:57], v0 offset:8800
	s_waitcnt vmcnt(0) lgkmcnt(1)
	v_mfma_f32_32x32x16_bf16 v[18:33], v[66:69], v[50:53], v[18:33]
	s_waitcnt lgkmcnt(0)
	v_mfma_f32_32x32x16_bf16 v[2:17], v[66:69], v[54:57], v[2:17]
	global_load_dwordx4 v[66:69], v[98:99], off offset:128
	global_load_dwordx4 v[70:73], v[98:99], off offset:160
	global_load_dwordx4 v[74:77], v[98:99], off offset:192
	global_load_dwordx4 v[78:81], v[98:99], off offset:224
	s_nop 5
	v_mov_b32_e32 v84, v18
	s_nop 0
	v_mov_b32_e32 v85, v2
	v_mov_b32_e32 v2, v19
	s_waitcnt vmcnt(3)
	v_pk_add_f32 v[2:3], v[2:3], v[66:67] op_sel:[0,1]
	s_nop 0
	v_cvt_pk_bf16_f32 v124, v2, v3
	v_mov_b32_e32 v2, v20
	v_mov_b32_e32 v3, v4
	v_pk_add_f32 v[2:3], v[2:3], v[68:69] op_sel_hi:[1,0]
	v_mov_b32_e32 v4, v21
	v_cvt_pk_bf16_f32 v125, v2, v3
	v_mov_b32_e32 v2, v69
	v_pk_add_f32 v[2:3], v[4:5], v[2:3] op_sel_hi:[1,0]
	v_pk_add_f32 v[84:85], v[84:85], v[66:67] op_sel_hi:[1,0]
	v_cvt_pk_bf16_f32 v126, v2, v3
	v_mov_b32_e32 v2, v22
	v_mov_b32_e32 v3, v6
	s_waitcnt vmcnt(2)
	v_pk_add_f32 v[2:3], v[2:3], v[70:71] op_sel_hi:[1,0]
	v_mov_b32_e32 v6, v23
	v_cvt_pk_bf16_f32 v127, v2, v3
	v_pk_add_f32 v[2:3], v[6:7], v[70:71] op_sel:[0,1]
	v_cvt_pk_bf16_f32 v123, v84, v85
	v_cvt_pk_bf16_f32 v128, v2, v3
	v_mov_b32_e32 v2, v24
	v_mov_b32_e32 v3, v8
	v_pk_add_f32 v[2:3], v[2:3], v[72:73] op_sel_hi:[1,0]
	v_mov_b32_e32 v8, v25
	v_cvt_pk_bf16_f32 v129, v2, v3
	v_mov_b32_e32 v2, v73
	v_pk_add_f32 v[2:3], v[8:9], v[2:3] op_sel_hi:[1,0]
	s_nop 0
	v_cvt_pk_bf16_f32 v130, v2, v3
	v_mov_b32_e32 v2, v26
	v_mov_b32_e32 v3, v10
	s_waitcnt vmcnt(1)
	v_pk_add_f32 v[2:3], v[2:3], v[74:75] op_sel_hi:[1,0]
	v_mov_b32_e32 v10, v27
	v_cvt_pk_bf16_f32 v131, v2, v3
	v_pk_add_f32 v[2:3], v[10:11], v[74:75] op_sel:[0,1]
	s_nop 0
	v_cvt_pk_bf16_f32 v132, v2, v3
	v_mov_b32_e32 v2, v28
	v_mov_b32_e32 v3, v12
	v_pk_add_f32 v[2:3], v[2:3], v[76:77] op_sel_hi:[1,0]
	v_mov_b32_e32 v12, v29
	v_cvt_pk_bf16_f32 v133, v2, v3
	v_mov_b32_e32 v2, v77
	v_pk_add_f32 v[2:3], v[12:13], v[2:3] op_sel_hi:[1,0]
	s_nop 0
	v_cvt_pk_bf16_f32 v134, v2, v3
	v_mov_b32_e32 v2, v30
	v_mov_b32_e32 v3, v14
	s_waitcnt vmcnt(0)
	v_pk_add_f32 v[2:3], v[2:3], v[78:79] op_sel_hi:[1,0]
	v_mov_b32_e32 v14, v31
	v_cvt_pk_bf16_f32 v135, v2, v3
	v_pk_add_f32 v[2:3], v[14:15], v[78:79] op_sel:[0,1]
	s_nop 0
	v_cvt_pk_bf16_f32 v136, v2, v3
	v_mov_b32_e32 v2, v32
	v_mov_b32_e32 v3, v16
	v_pk_add_f32 v[2:3], v[2:3], v[80:81] op_sel_hi:[1,0]
	v_mov_b32_e32 v16, v33
	v_cvt_pk_bf16_f32 v137, v2, v3
	v_mov_b32_e32 v2, v81
	v_pk_add_f32 v[2:3], v[16:17], v[2:3] op_sel_hi:[1,0]
	s_nop 0
	v_cvt_pk_bf16_f32 v138, v2, v3
	v_add_co_u32_e32 v2, vcc, s4, v82
	s_mov_b32 s4, 0x1626000
	s_nop 0
	v_addc_co_u32_e32 v3, vcc, 0, v83, vcc
	global_load_dwordx4 v[18:21], v[2:3], off
	global_load_dwordx4 v[66:69], v[2:3], off offset:32
	global_load_dwordx4 v[70:73], v[2:3], off offset:64
	global_load_dwordx4 v[74:77], v[2:3], off offset:96
	global_load_dwordx4 v[78:81], v[2:3], off offset:128
	global_load_dwordx4 v[84:87], v[2:3], off offset:160
	s_waitcnt vmcnt(5)
	v_mfma_f32_32x32x16_bf16 v[2:17], v[18:21], v[46:49], 0
	v_mfma_f32_32x32x16_bf16 v[18:33], v[18:21], v[42:45], 0
	s_waitcnt vmcnt(4)
	v_mfma_f32_32x32x16_bf16 v[2:17], v[66:69], v[38:41], v[2:17]
	v_mfma_f32_32x32x16_bf16 v[18:33], v[66:69], v[34:37], v[18:33]
	s_waitcnt vmcnt(3)
	v_mfma_f32_32x32x16_bf16 v[2:17], v[70:73], v[62:65], v[2:17]
	v_mfma_f32_32x32x16_bf16 v[18:33], v[70:73], v[58:61], v[18:33]
	ds_read_b128 v[66:69], v0 offset:128
	ds_read_b128 v[70:73], v0 offset:8832
	s_waitcnt vmcnt(2)
	v_mfma_f32_32x32x16_bf16 v[2:17], v[74:77], v[50:53], v[2:17]
	v_mfma_f32_32x32x16_bf16 v[18:33], v[74:77], v[54:57], v[18:33]
	s_waitcnt vmcnt(1) lgkmcnt(1)
	v_mfma_f32_32x32x16_bf16 v[2:17], v[78:81], v[66:69], v[2:17]
	s_waitcnt lgkmcnt(0)
	v_mfma_f32_32x32x16_bf16 v[18:33], v[78:81], v[70:73], v[18:33]
	ds_read_b128 v[74:77], v0 offset:160
	ds_read_b128 v[78:81], v0 offset:8864
	s_waitcnt vmcnt(0) lgkmcnt(1)
	v_mfma_f32_32x32x16_bf16 v[2:17], v[84:87], v[74:77], v[2:17]
	s_waitcnt lgkmcnt(0)
	v_mfma_f32_32x32x16_bf16 v[18:33], v[84:87], v[78:81], v[18:33]
	global_load_dwordx4 v[84:87], v[98:99], off offset:256
	global_load_dwordx4 v[88:91], v[98:99], off offset:288
	global_load_dwordx4 v[92:95], v[98:99], off offset:320
	global_load_dwordx4 v[156:159], v[98:99], off offset:352
	s_nop 5
	v_mov_b32_e32 v96, v2
	s_nop 0
	v_mov_b32_e32 v97, v18
	v_mov_b32_e32 v18, v3
	s_waitcnt vmcnt(3)
	v_pk_add_f32 v[2:3], v[18:19], v[84:85] op_sel:[0,1]
	s_nop 0
	v_cvt_pk_bf16_f32 v150, v2, v3
	v_mov_b32_e32 v2, v4
	v_mov_b32_e32 v3, v20
	v_pk_add_f32 v[2:3], v[2:3], v[86:87] op_sel_hi:[1,0]
	v_mov_b32_e32 v20, v5
	v_cvt_pk_bf16_f32 v151, v2, v3
	v_mov_b32_e32 v2, v87
	v_pk_add_f32 v[2:3], v[20:21], v[2:3] op_sel_hi:[1,0]
	v_pk_add_f32 v[96:97], v[96:97], v[84:85] op_sel_hi:[1,0]
	v_cvt_pk_bf16_f32 v152, v2, v3
	v_mov_b32_e32 v2, v6
	v_mov_b32_e32 v3, v22
	s_waitcnt vmcnt(2)
	v_pk_add_f32 v[2:3], v[2:3], v[88:89] op_sel_hi:[1,0]
	v_mov_b32_e32 v22, v7
	v_cvt_pk_bf16_f32 v153, v2, v3
	v_pk_add_f32 v[2:3], v[22:23], v[88:89] op_sel:[0,1]
	v_cvt_pk_bf16_f32 v154, v96, v97
	v_cvt_pk_bf16_f32 v146, v2, v3
	v_mov_b32_e32 v2, v8
	v_mov_b32_e32 v3, v24
	v_pk_add_f32 v[2:3], v[2:3], v[90:91] op_sel_hi:[1,0]
	v_mov_b32_e32 v24, v9
	v_cvt_pk_bf16_f32 v147, v2, v3
	v_mov_b32_e32 v2, v91
	v_pk_add_f32 v[2:3], v[24:25], v[2:3] op_sel_hi:[1,0]
	s_nop 0
	v_cvt_pk_bf16_f32 v148, v2, v3
	v_mov_b32_e32 v2, v10
	v_mov_b32_e32 v3, v26
	s_waitcnt vmcnt(1)
	v_pk_add_f32 v[2:3], v[2:3], v[92:93] op_sel_hi:[1,0]
	v_mov_b32_e32 v26, v11
	v_cvt_pk_bf16_f32 v149, v2, v3
	v_pk_add_f32 v[2:3], v[26:27], v[92:93] op_sel:[0,1]
	s_nop 0
	v_cvt_pk_bf16_f32 v142, v2, v3
	v_mov_b32_e32 v2, v12
	v_mov_b32_e32 v3, v28
	v_pk_add_f32 v[2:3], v[2:3], v[94:95] op_sel_hi:[1,0]
	v_mov_b32_e32 v28, v13
	v_cvt_pk_bf16_f32 v143, v2, v3
	v_mov_b32_e32 v2, v95
	v_pk_add_f32 v[2:3], v[28:29], v[2:3] op_sel_hi:[1,0]
	s_nop 0
	v_cvt_pk_bf16_f32 v144, v2, v3
	v_mov_b32_e32 v2, v14
	v_mov_b32_e32 v3, v30
	s_waitcnt vmcnt(0)
	v_pk_add_f32 v[2:3], v[2:3], v[156:157] op_sel_hi:[1,0]
	v_mov_b32_e32 v30, v15
	v_cvt_pk_bf16_f32 v145, v2, v3
	v_pk_add_f32 v[2:3], v[30:31], v[156:157] op_sel:[0,1]
	s_nop 0
	v_cvt_pk_bf16_f32 v139, v2, v3
	v_mov_b32_e32 v2, v16
	v_mov_b32_e32 v3, v32
	v_pk_add_f32 v[2:3], v[2:3], v[158:159] op_sel_hi:[1,0]
	v_mov_b32_e32 v32, v17
	v_cvt_pk_bf16_f32 v140, v2, v3
	v_mov_b32_e32 v2, v159
	v_pk_add_f32 v[2:3], v[32:33], v[2:3] op_sel_hi:[1,0]
	s_nop 0
	v_cvt_pk_bf16_f32 v141, v2, v3
	v_add_co_u32_e32 v2, vcc, s4, v82
	s_ashr_i32 s4, s23, 31
	s_nop 0
	v_addc_co_u32_e32 v3, vcc, 0, v83, vcc
	global_load_dwordx4 v[18:21], v[2:3], off
	global_load_dwordx4 v[82:85], v[2:3], off offset:32
	global_load_dwordx4 v[86:89], v[2:3], off offset:64
	global_load_dwordx4 v[90:93], v[2:3], off offset:96
	global_load_dwordx4 v[94:97], v[2:3], off offset:128
	global_load_dwordx4 v[156:159], v[2:3], off offset:160
	global_load_dwordx4 v[160:163], v[2:3], off offset:192
	global_load_dwordx4 v[164:167], v[2:3], off offset:224
	s_waitcnt vmcnt(7)
	v_mfma_f32_32x32x16_bf16 v[2:17], v[18:21], v[46:49], 0
	s_add_u32 s20, s8, s23
	s_addc_u32 s21, s9, s4
	s_add_u32 s16, s20, 0xffffff88
	s_addc_u32 s17, s21, -1
	s_lshl_b64 s[4:5], s[16:17], 11
	v_mfma_f32_32x32x16_bf16 v[18:33], v[18:21], v[42:45], 0
	s_waitcnt vmcnt(6)
	v_mfma_f32_32x32x16_bf16 v[2:17], v[82:85], v[38:41], v[2:17]
	v_mfma_f32_32x32x16_bf16 v[18:33], v[82:85], v[34:37], v[18:33]
	ds_read_b128 v[34:37], v0 offset:192
	ds_read_b128 v[38:41], v0 offset:8896
	v_or_b32_e32 v82, s6, v105
	v_lshlrev_b32_e32 v82, 1, v82
	v_mul_u32_u24_e32 v83, 0x1040, v106
	v_add3_u32 v82, 0, v82, v83
	v_add_u32_e32 v83, 0x10400, v82
	v_cmp_eq_u32_e64 s[6:7], 0, v103
	s_waitcnt vmcnt(5)
	v_mfma_f32_32x32x16_bf16 v[2:17], v[86:89], v[62:65], v[2:17]
	v_mfma_f32_32x32x16_bf16 v[18:33], v[86:89], v[58:61], v[18:33]
	s_waitcnt vmcnt(4)
	v_mfma_f32_32x32x16_bf16 v[2:17], v[90:93], v[50:53], v[2:17]
	v_mfma_f32_32x32x16_bf16 v[18:33], v[90:93], v[54:57], v[18:33]
	s_waitcnt vmcnt(3)
	v_mfma_f32_32x32x16_bf16 v[2:17], v[94:97], v[66:69], v[2:17]
	v_mfma_f32_32x32x16_bf16 v[18:33], v[94:97], v[70:73], v[18:33]
	s_waitcnt vmcnt(2)
	v_mfma_f32_32x32x16_bf16 v[2:17], v[156:159], v[74:77], v[2:17]
	v_mfma_f32_32x32x16_bf16 v[18:33], v[156:159], v[78:81], v[18:33]
	s_waitcnt vmcnt(1) lgkmcnt(1)
	v_mfma_f32_32x32x16_bf16 v[2:17], v[160:163], v[34:37], v[2:17]
	s_waitcnt lgkmcnt(0)
	v_mfma_f32_32x32x16_bf16 v[18:33], v[160:163], v[38:41], v[18:33]
	ds_read_b128 v[34:37], v0 offset:224
	ds_read_b128 v[38:41], v0 offset:8928
	s_waitcnt vmcnt(0) lgkmcnt(1)
	v_mfma_f32_32x32x16_bf16 v[2:17], v[164:167], v[34:37], v[2:17]
	s_waitcnt lgkmcnt(0)
	v_mfma_f32_32x32x16_bf16 v[18:33], v[164:167], v[38:41], v[18:33]
	global_load_dwordx4 v[34:37], v[98:99], off offset:384
	global_load_dwordx4 v[38:41], v[98:99], off offset:416
	global_load_dwordx4 v[42:45], v[98:99], off offset:448
	global_load_dwordx4 v[46:49], v[98:99], off offset:480
	s_nop 5
	v_mov_b32_e32 v50, v2
	s_nop 0
	v_mov_b32_e32 v51, v18
	v_mov_b32_e32 v18, v3
	s_waitcnt vmcnt(3)
	v_pk_add_f32 v[2:3], v[18:19], v[34:35] op_sel:[0,1]
	s_nop 0
	v_cvt_pk_bf16_f32 v67, v2, v3
	v_mov_b32_e32 v2, v4
	v_mov_b32_e32 v3, v20
	v_pk_add_f32 v[2:3], v[2:3], v[36:37] op_sel_hi:[1,0]
	v_mov_b32_e32 v20, v5
	v_mov_b32_e32 v0, v37
	v_cvt_pk_bf16_f32 v68, v2, v3
	v_pk_add_f32 v[2:3], v[20:21], v[0:1] op_sel_hi:[1,0]
	s_waitcnt vmcnt(2)
	v_mov_b32_e32 v0, v41
	v_cvt_pk_bf16_f32 v69, v2, v3
	v_mov_b32_e32 v2, v6
	v_mov_b32_e32 v3, v22
	v_pk_add_f32 v[2:3], v[2:3], v[38:39] op_sel_hi:[1,0]
	v_mov_b32_e32 v22, v7
	v_cvt_pk_bf16_f32 v70, v2, v3
	v_pk_add_f32 v[2:3], v[22:23], v[38:39] op_sel:[0,1]
	v_pk_add_f32 v[50:51], v[50:51], v[34:35] op_sel_hi:[1,0]
	v_cvt_pk_bf16_f32 v71, v2, v3
	v_mov_b32_e32 v2, v8
	v_mov_b32_e32 v3, v24
	v_pk_add_f32 v[2:3], v[2:3], v[40:41] op_sel_hi:[1,0]
	v_mov_b32_e32 v24, v9
	v_cvt_pk_bf16_f32 v72, v2, v3
	v_pk_add_f32 v[2:3], v[24:25], v[0:1] op_sel_hi:[1,0]
	s_waitcnt vmcnt(1)
	v_mov_b32_e32 v0, v45
	v_cvt_pk_bf16_f32 v73, v2, v3
	v_mov_b32_e32 v2, v10
	v_mov_b32_e32 v3, v26
	v_pk_add_f32 v[2:3], v[2:3], v[42:43] op_sel_hi:[1,0]
	v_mov_b32_e32 v26, v11
	v_cvt_pk_bf16_f32 v74, v2, v3
	v_pk_add_f32 v[2:3], v[26:27], v[42:43] op_sel:[0,1]
	v_cvt_pk_bf16_f32 v66, v50, v51
	v_cvt_pk_bf16_f32 v75, v2, v3
	v_mov_b32_e32 v2, v12
	v_mov_b32_e32 v3, v28
	v_pk_add_f32 v[2:3], v[2:3], v[44:45] op_sel_hi:[1,0]
	v_mov_b32_e32 v28, v13
	v_cvt_pk_bf16_f32 v76, v2, v3
	v_pk_add_f32 v[2:3], v[28:29], v[0:1] op_sel_hi:[1,0]
	s_waitcnt vmcnt(0)
	v_mov_b32_e32 v0, v49
	v_cvt_pk_bf16_f32 v77, v2, v3
	v_mov_b32_e32 v2, v14
	v_mov_b32_e32 v3, v30
	v_pk_add_f32 v[2:3], v[2:3], v[46:47] op_sel_hi:[1,0]
	v_mov_b32_e32 v30, v15
	v_cvt_pk_bf16_f32 v78, v2, v3
	v_pk_add_f32 v[2:3], v[30:31], v[46:47] op_sel:[0,1]
	s_nop 0
	v_cvt_pk_bf16_f32 v79, v2, v3
	v_mov_b32_e32 v2, v16
	v_mov_b32_e32 v3, v32
	v_pk_add_f32 v[2:3], v[2:3], v[48:49] op_sel_hi:[1,0]
	v_mov_b32_e32 v32, v17
	v_cvt_pk_bf16_f32 v80, v2, v3
	v_pk_add_f32 v[2:3], v[32:33], v[0:1] op_sel_hi:[1,0]
	v_lshlrev_b32_e32 v0, 4, v103
	v_cvt_pk_bf16_f32 v81, v2, v3
	v_lshl_add_u64 v[2:3], s[14:15], 0, v[0:1]
	v_lshl_add_u64 v[2:3], v[2:3], 0, s[4:5]
	v_add_co_u32_e32 v4, vcc, s74, v2
	s_movk_i32 s4, 0x2000
	s_nop 0
	v_addc_co_u32_e32 v5, vcc, 0, v3, vcc
	v_add_co_u32_e32 v6, vcc, s4, v2
	global_load_dwordx4 v[62:65], v[2:3], off
	global_load_dwordx4 v[58:61], v[2:3], off offset:2048
	v_addc_co_u32_e32 v7, vcc, 0, v3, vcc
	s_movk_i32 s4, 0x3000
	global_load_dwordx4 v[54:57], v[6:7], off offset:-4096
	global_load_dwordx4 v[50:53], v[4:5], off offset:2048
	global_load_dwordx4 v[46:49], v[6:7], off
	global_load_dwordx4 v[42:45], v[6:7], off offset:2048
	v_add_co_u32_e32 v4, vcc, s4, v2
	s_movk_i32 s4, 0x4000
	s_nop 0
	v_addc_co_u32_e32 v5, vcc, 0, v3, vcc
	v_add_co_u32_e32 v6, vcc, s4, v2
	s_movk_i32 s4, 0x5000
	s_nop 0
	v_addc_co_u32_e32 v7, vcc, 0, v3, vcc
	global_load_dwordx4 v[38:41], v[6:7], off offset:-4096
	global_load_dwordx4 v[34:37], v[4:5], off offset:2048
	global_load_dwordx4 v[30:33], v[6:7], off
	global_load_dwordx4 v[26:29], v[6:7], off offset:2048
	v_add_co_u32_e32 v4, vcc, s4, v2
	s_movk_i32 s4, 0x6000
	s_nop 0
	v_addc_co_u32_e32 v5, vcc, 0, v3, vcc
	v_add_co_u32_e32 v6, vcc, s4, v2
	s_movk_i32 s4, 0x7000
	s_nop 0
	v_addc_co_u32_e32 v7, vcc, 0, v3, vcc
	v_add_co_u32_e32 v2, vcc, s4, v2
	global_load_dwordx4 v[22:25], v[6:7], off offset:-4096
	global_load_dwordx4 v[18:21], v[4:5], off offset:2048
	global_load_dwordx4 v[14:17], v[6:7], off
	global_load_dwordx4 v[10:13], v[6:7], off offset:2048
	v_addc_co_u32_e32 v3, vcc, 0, v3, vcc
	global_load_dwordx4 v[6:9], v[2:3], off
	s_nop 0
	global_load_dwordx4 v[2:5], v[2:3], off offset:2048
	s_barrier
	ds_write_b16 v82, v107
	ds_write_b16_d16_hi v82, v107 offset:64
	ds_write_b16 v82, v108 offset:1040
	ds_write_b16_d16_hi v82, v108 offset:1104
	ds_write_b16 v82, v109 offset:2080
	ds_write_b16_d16_hi v82, v109 offset:2144
	ds_write_b16 v82, v110 offset:3120
	ds_write_b16_d16_hi v82, v110 offset:3184
	ds_write_b16 v82, v111 offset:8320
	ds_write_b16_d16_hi v82, v111 offset:8384
	ds_write_b16 v82, v112 offset:9360
	ds_write_b16_d16_hi v82, v112 offset:9424
	ds_write_b16 v82, v113 offset:10400
	ds_write_b16_d16_hi v82, v113 offset:10464
	ds_write_b16 v82, v114 offset:11440
	ds_write_b16_d16_hi v82, v114 offset:11504
	ds_write_b16 v82, v115 offset:16640
	ds_write_b16_d16_hi v82, v115 offset:16704
	ds_write_b16 v82, v116 offset:17680
	ds_write_b16_d16_hi v82, v116 offset:17744
	ds_write_b16 v82, v117 offset:18720
	ds_write_b16_d16_hi v82, v117 offset:18784
	ds_write_b16 v82, v118 offset:19760
	ds_write_b16_d16_hi v82, v118 offset:19824
	ds_write_b16 v82, v119 offset:24960
	ds_write_b16_d16_hi v82, v119 offset:25024
	ds_write_b16 v82, v120 offset:26000
	ds_write_b16_d16_hi v82, v120 offset:26064
	ds_write_b16 v82, v121 offset:27040
	ds_write_b16_d16_hi v82, v121 offset:27104
	ds_write_b16 v82, v122 offset:28080
	ds_write_b16_d16_hi v82, v122 offset:28144
	ds_write_b16 v82, v123 offset:33280
	ds_write_b16_d16_hi v82, v123 offset:33344
	ds_write_b16 v82, v124 offset:34320
	ds_write_b16_d16_hi v82, v124 offset:34384
	ds_write_b16 v82, v125 offset:35360
	ds_write_b16_d16_hi v82, v125 offset:35424
	ds_write_b16 v82, v126 offset:36400
	ds_write_b16_d16_hi v82, v126 offset:36464
	ds_write_b16 v82, v127 offset:41600
	ds_write_b16_d16_hi v82, v127 offset:41664
	ds_write_b16 v82, v128 offset:42640
	ds_write_b16_d16_hi v82, v128 offset:42704
	ds_write_b16 v82, v129 offset:43680
	ds_write_b16_d16_hi v82, v129 offset:43744
	ds_write_b16 v82, v130 offset:44720
	ds_write_b16_d16_hi v82, v130 offset:44784
	ds_write_b16 v82, v131 offset:49920
	ds_write_b16_d16_hi v82, v131 offset:49984
	ds_write_b16 v82, v132 offset:50960
	ds_write_b16_d16_hi v82, v132 offset:51024
	ds_write_b16 v82, v133 offset:52000
	ds_write_b16_d16_hi v82, v133 offset:52064
	ds_write_b16 v82, v134 offset:53040
	ds_write_b16_d16_hi v82, v134 offset:53104
	ds_write_b16 v82, v135 offset:58240
	ds_write_b16_d16_hi v82, v135 offset:58304
	ds_write_b16 v82, v136 offset:59280
	ds_write_b16_d16_hi v82, v136 offset:59344
	ds_write_b16 v82, v137 offset:60320
	ds_write_b16_d16_hi v82, v137 offset:60384
	ds_write_b16 v82, v138 offset:61360
	ds_write_b16_d16_hi v82, v138 offset:61424
	ds_write_b16 v83, v154
	v_add_u32_e32 v83, 0x10440, v82
	ds_write_b16_d16_hi v83, v154
	v_add_u32_e32 v83, 0x10810, v82
	ds_write_b16 v83, v150
	v_add_u32_e32 v83, 0x10850, v82
	ds_write_b16_d16_hi v83, v150
	v_add_u32_e32 v83, 0x10c20, v82
	ds_write_b16 v83, v151
	v_add_u32_e32 v83, 0x10c60, v82
	ds_write_b16_d16_hi v83, v151
	v_add_u32_e32 v83, 0x11030, v82
	ds_write_b16 v83, v152
	v_add_u32_e32 v83, 0x11070, v82
	ds_write_b16_d16_hi v83, v152
	v_add_u32_e32 v83, 0x12480, v82
	ds_write_b16 v83, v153
	v_add_u32_e32 v83, 0x124c0, v82
	ds_write_b16_d16_hi v83, v153
	v_add_u32_e32 v83, 0x12890, v82
	ds_write_b16 v83, v146
	v_add_u32_e32 v83, 0x128d0, v82
	ds_write_b16_d16_hi v83, v146
	v_add_u32_e32 v83, 0x12ca0, v82
	ds_write_b16 v83, v147
	v_add_u32_e32 v83, 0x12ce0, v82
	ds_write_b16_d16_hi v83, v147
	v_add_u32_e32 v83, 0x130b0, v82
	ds_write_b16 v83, v148
	v_add_u32_e32 v83, 0x130f0, v82
	ds_write_b16_d16_hi v83, v148
	v_add_u32_e32 v83, 0x14500, v82
	ds_write_b16 v83, v149
	v_add_u32_e32 v83, 0x14540, v82
	ds_write_b16_d16_hi v83, v149
	v_add_u32_e32 v83, 0x14910, v82
	ds_write_b16 v83, v142
	v_add_u32_e32 v83, 0x14950, v82
	ds_write_b16_d16_hi v83, v142
	v_add_u32_e32 v83, 0x14d20, v82
	ds_write_b16 v83, v143
	v_add_u32_e32 v83, 0x14d60, v82
	ds_write_b16_d16_hi v83, v143
	v_add_u32_e32 v83, 0x15130, v82
	ds_write_b16 v83, v144
	v_add_u32_e32 v83, 0x15170, v82
	ds_write_b16_d16_hi v83, v144
	v_add_u32_e32 v83, 0x16580, v82
	ds_write_b16 v83, v145
	v_add_u32_e32 v83, 0x165c0, v82
	ds_write_b16_d16_hi v83, v145
	v_add_u32_e32 v83, 0x16990, v82
	ds_write_b16 v83, v139
	v_add_u32_e32 v83, 0x169d0, v82
	ds_write_b16_d16_hi v83, v139
	v_add_u32_e32 v83, 0x16da0, v82
	ds_write_b16 v83, v140
	v_add_u32_e32 v83, 0x16de0, v82
	ds_write_b16_d16_hi v83, v140
	v_add_u32_e32 v83, 0x171b0, v82
	ds_write_b16 v83, v141
	v_add_u32_e32 v83, 0x171f0, v82
	ds_write_b16_d16_hi v83, v141
	v_add_u32_e32 v83, 0x18600, v82
	ds_write_b16 v83, v66
	v_add_u32_e32 v83, 0x18640, v82
	ds_write_b16_d16_hi v83, v66
	v_add_u32_e32 v66, 0x18a10, v82
	ds_write_b16 v66, v67
	v_add_u32_e32 v66, 0x18a50, v82
	ds_write_b16_d16_hi v66, v67
	v_add_u32_e32 v66, 0x18e20, v82
	ds_write_b16 v66, v68
	v_add_u32_e32 v66, 0x18e60, v82
	ds_write_b16_d16_hi v66, v68
	v_add_u32_e32 v66, 0x19230, v82
	ds_write_b16 v66, v69
	v_add_u32_e32 v66, 0x19270, v82
	ds_write_b16_d16_hi v66, v69
	v_add_u32_e32 v66, 0x1a680, v82
	ds_write_b16 v66, v70
	v_add_u32_e32 v66, 0x1a6c0, v82
	ds_write_b16_d16_hi v66, v70
	v_add_u32_e32 v66, 0x1aa90, v82
	ds_write_b16 v66, v71
	v_add_u32_e32 v66, 0x1aad0, v82
	ds_write_b16_d16_hi v66, v71
	v_add_u32_e32 v66, 0x1aea0, v82
	ds_write_b16 v66, v72
	v_add_u32_e32 v66, 0x1aee0, v82
	ds_write_b16_d16_hi v66, v72
	v_add_u32_e32 v66, 0x1b2b0, v82
	ds_write_b16 v66, v73
	v_add_u32_e32 v66, 0x1b2f0, v82
	ds_write_b16_d16_hi v66, v73
	v_add_u32_e32 v66, 0x1c700, v82
	ds_write_b16 v66, v74
	v_add_u32_e32 v66, 0x1c740, v82
	ds_write_b16_d16_hi v66, v74
	v_add_u32_e32 v66, 0x1cb10, v82
	ds_write_b16 v66, v75
	v_add_u32_e32 v66, 0x1cb50, v82
	ds_write_b16_d16_hi v66, v75
	v_add_u32_e32 v66, 0x1cf20, v82
	ds_write_b16 v66, v76
	v_add_u32_e32 v66, 0x1cf60, v82
	ds_write_b16_d16_hi v66, v76
	v_add_u32_e32 v66, 0x1d330, v82
	ds_write_b16 v66, v77
	v_add_u32_e32 v66, 0x1d370, v82
	ds_write_b16_d16_hi v66, v77
	v_add_u32_e32 v66, 0x1e780, v82
	ds_write_b16 v66, v78
	v_add_u32_e32 v66, 0x1e7c0, v82
	ds_write_b16_d16_hi v66, v78
	v_add_u32_e32 v66, 0x1eb90, v82
	ds_write_b16 v66, v79
	v_add_u32_e32 v66, 0x1ebd0, v82
	ds_write_b16_d16_hi v66, v79
	v_add_u32_e32 v66, 0x1efa0, v82
	v_add_u32_e32 v70, 0, v0
	v_xor_b32_e32 v0, 8, v234
	ds_write_b16 v66, v80
	v_add_u32_e32 v66, 0x1efe0, v82
	v_cmp_lt_i32_e32 vcc, v0, v104
	ds_write_b16_d16_hi v66, v80
	v_add_u32_e32 v66, 0x1f3b0, v82
	v_cndmask_b32_e32 v0, v234, v0, vcc
	s_mul_i32 s4, s12, 0x4100
	ds_write_b16 v66, v81
	v_add_u32_e32 v66, 0x1f3f0, v82
	v_lshlrev_b32_e32 v68, 2, v0
	v_xor_b32_e32 v0, 16, v234
	v_add_u32_e32 v69, s4, v70
	ds_write_b16_d16_hi v66, v81
	s_waitcnt lgkmcnt(0)
	s_barrier
	v_cmp_lt_i32_e32 vcc, v0, v104
	ds_read_b128 v[74:77], v69
	ds_read_b128 v[82:85], v69 offset:1040
	v_cndmask_b32_e32 v0, v234, v0, vcc
	v_lshlrev_b32_e32 v67, 2, v0
	v_xor_b32_e32 v0, 32, v234
	v_cmp_lt_i32_e32 vcc, v0, v104
	s_waitcnt vmcnt(15)
	v_lshlrev_b32_e32 v71, 16, v62
	v_and_b32_e32 v62, 0xffff0000, v62
	v_cndmask_b32_e32 v0, v234, v0, vcc
	v_lshlrev_b32_e32 v66, 2, v0
	s_waitcnt lgkmcnt(1)
	v_lshlrev_b32_e32 v0, 16, v74
	v_mul_f32_e32 v71, v71, v0
	v_and_b32_e32 v0, 0xffff0000, v74
	v_mul_f32_e32 v72, v62, v0
	v_lshlrev_b32_e32 v0, 16, v75
	v_lshlrev_b32_e32 v62, 16, v63
	v_mul_f32_e32 v73, v62, v0
	v_and_b32_e32 v0, 0xffff0000, v75
	v_and_b32_e32 v62, 0xffff0000, v63
	v_mul_f32_e32 v74, v62, v0
	v_lshlrev_b32_e32 v0, 16, v76
	v_lshlrev_b32_e32 v62, 16, v64
	v_mul_f32_e32 v62, v62, v0
	v_and_b32_e32 v0, 0xffff0000, v76
	v_and_b32_e32 v63, 0xffff0000, v64
	v_mul_f32_e32 v63, v63, v0
	v_lshlrev_b32_e32 v0, 16, v77
	v_lshlrev_b32_e32 v64, 16, v65
	v_mul_f32_e32 v64, v64, v0
	v_and_b32_e32 v0, 0xffff0000, v77
	v_and_b32_e32 v65, 0xffff0000, v65
	v_mul_f32_e32 v65, v65, v0
	s_waitcnt lgkmcnt(0)
	v_lshlrev_b32_e32 v0, 16, v82
	s_waitcnt vmcnt(14)
	v_lshlrev_b32_e32 v75, 16, v58
	v_mul_f32_e32 v79, v75, v0
	v_and_b32_e32 v0, 0xffff0000, v82
	v_and_b32_e32 v58, 0xffff0000, v58
	v_mul_f32_e32 v80, v58, v0
	v_lshlrev_b32_e32 v0, 16, v83
	v_lshlrev_b32_e32 v58, 16, v59
	v_mul_f32_e32 v81, v58, v0
	v_and_b32_e32 v0, 0xffff0000, v83
	v_and_b32_e32 v58, 0xffff0000, v59
	v_mul_f32_e32 v82, v58, v0
	v_lshlrev_b32_e32 v0, 16, v84
	v_lshlrev_b32_e32 v58, 16, v60
	v_mul_f32_e32 v75, v58, v0
	v_and_b32_e32 v0, 0xffff0000, v84
	v_and_b32_e32 v58, 0xffff0000, v60
	v_mul_f32_e32 v76, v58, v0
	v_lshlrev_b32_e32 v0, 16, v85
	v_lshlrev_b32_e32 v58, 16, v61
	v_mul_f32_e32 v77, v58, v0
	v_and_b32_e32 v0, 0xffff0000, v85
	ds_read_b128 v[84:87], v69 offset:2080
	ds_read_b128 v[90:93], v69 offset:3120
	v_and_b32_e32 v58, 0xffff0000, v61
	v_mul_f32_e32 v78, v58, v0
	s_waitcnt vmcnt(13)
	v_lshlrev_b32_e32 v58, 16, v54
	s_waitcnt lgkmcnt(1)
	v_lshlrev_b32_e32 v0, 16, v84
	v_mul_f32_e32 v58, v58, v0
	v_and_b32_e32 v0, 0xffff0000, v84
	v_and_b32_e32 v54, 0xffff0000, v54
	v_mul_f32_e32 v59, v54, v0
	v_lshlrev_b32_e32 v0, 16, v85
	v_lshlrev_b32_e32 v54, 16, v55
	v_mul_f32_e32 v60, v54, v0
	v_and_b32_e32 v0, 0xffff0000, v85
	v_and_b32_e32 v54, 0xffff0000, v55
	v_mul_f32_e32 v61, v54, v0
	v_lshlrev_b32_e32 v0, 16, v86
	v_lshlrev_b32_e32 v54, 16, v56
	v_mul_f32_e32 v54, v54, v0
	v_and_b32_e32 v0, 0xffff0000, v86
	v_and_b32_e32 v55, 0xffff0000, v56
	v_mul_f32_e32 v55, v55, v0
	v_lshlrev_b32_e32 v0, 16, v87
	v_lshlrev_b32_e32 v56, 16, v57
	v_mul_f32_e32 v56, v56, v0
	v_and_b32_e32 v0, 0xffff0000, v87
	v_and_b32_e32 v57, 0xffff0000, v57
	v_mul_f32_e32 v57, v57, v0
	s_waitcnt lgkmcnt(0)
	v_lshlrev_b32_e32 v0, 16, v90
	s_waitcnt vmcnt(12)
	v_lshlrev_b32_e32 v83, 16, v50
	v_mul_f32_e32 v87, v83, v0
	v_and_b32_e32 v0, 0xffff0000, v90
	v_and_b32_e32 v50, 0xffff0000, v50
	v_mul_f32_e32 v88, v50, v0
	v_lshlrev_b32_e32 v0, 16, v91
	v_lshlrev_b32_e32 v50, 16, v51
	v_mul_f32_e32 v89, v50, v0
	v_and_b32_e32 v0, 0xffff0000, v91
	v_and_b32_e32 v50, 0xffff0000, v51
	v_mul_f32_e32 v90, v50, v0
	v_lshlrev_b32_e32 v0, 16, v92
	v_lshlrev_b32_e32 v50, 16, v52
	v_mul_f32_e32 v83, v50, v0
	v_and_b32_e32 v0, 0xffff0000, v92
	v_and_b32_e32 v50, 0xffff0000, v52
	v_mul_f32_e32 v84, v50, v0
	v_lshlrev_b32_e32 v0, 16, v93
	v_lshlrev_b32_e32 v50, 16, v53
	v_mul_f32_e32 v85, v50, v0
	v_and_b32_e32 v0, 0xffff0000, v93
	ds_read_b128 v[92:95], v69 offset:4160
	ds_read_b128 v[104:107], v69 offset:5200
	v_and_b32_e32 v50, 0xffff0000, v53
	v_mul_f32_e32 v86, v50, v0
	s_waitcnt vmcnt(11)
	v_lshlrev_b32_e32 v50, 16, v46
	s_waitcnt lgkmcnt(1)
	v_lshlrev_b32_e32 v0, 16, v92
	v_mul_f32_e32 v50, v50, v0
	v_and_b32_e32 v0, 0xffff0000, v92
	v_and_b32_e32 v46, 0xffff0000, v46
	v_mul_f32_e32 v51, v46, v0
	v_lshlrev_b32_e32 v0, 16, v93
	v_lshlrev_b32_e32 v46, 16, v47
	v_mul_f32_e32 v52, v46, v0
	v_and_b32_e32 v0, 0xffff0000, v93
	v_and_b32_e32 v46, 0xffff0000, v47
	v_mul_f32_e32 v53, v46, v0
	v_lshlrev_b32_e32 v0, 16, v94
	v_lshlrev_b32_e32 v46, 16, v48
	v_mul_f32_e32 v46, v46, v0
	v_and_b32_e32 v0, 0xffff0000, v94
	v_and_b32_e32 v47, 0xffff0000, v48
	v_mul_f32_e32 v47, v47, v0
	v_lshlrev_b32_e32 v0, 16, v95
	v_lshlrev_b32_e32 v48, 16, v49
	v_mul_f32_e32 v48, v48, v0
	v_and_b32_e32 v0, 0xffff0000, v95
	v_and_b32_e32 v49, 0xffff0000, v49
	v_mul_f32_e32 v49, v49, v0
	s_waitcnt lgkmcnt(0)
	v_lshlrev_b32_e32 v0, 16, v104
	s_waitcnt vmcnt(10)
	v_lshlrev_b32_e32 v91, 16, v42
	v_mul_f32_e32 v95, v91, v0
	v_and_b32_e32 v0, 0xffff0000, v104
	v_and_b32_e32 v42, 0xffff0000, v42
	v_mul_f32_e32 v96, v42, v0
	v_lshlrev_b32_e32 v0, 16, v105
	v_lshlrev_b32_e32 v42, 16, v43
	v_mul_f32_e32 v97, v42, v0
	v_and_b32_e32 v0, 0xffff0000, v105
	v_and_b32_e32 v42, 0xffff0000, v43
	v_mul_f32_e32 v98, v42, v0
	v_lshlrev_b32_e32 v0, 16, v106
	v_lshlrev_b32_e32 v42, 16, v44
	v_mul_f32_e32 v91, v42, v0
	v_and_b32_e32 v0, 0xffff0000, v106
	v_and_b32_e32 v42, 0xffff0000, v44
	v_mul_f32_e32 v92, v42, v0
	v_lshlrev_b32_e32 v0, 16, v107
	v_lshlrev_b32_e32 v42, 16, v45
	v_mul_f32_e32 v93, v42, v0
	v_and_b32_e32 v0, 0xffff0000, v107
	ds_read_b128 v[104:107], v69 offset:6240
	ds_read_b128 v[108:111], v69 offset:7280
	v_and_b32_e32 v42, 0xffff0000, v45
	v_mul_f32_e32 v94, v42, v0
	s_waitcnt vmcnt(9)
	v_lshlrev_b32_e32 v42, 16, v38
	s_waitcnt lgkmcnt(1)
	v_lshlrev_b32_e32 v0, 16, v104
	v_mul_f32_e32 v42, v42, v0
	v_and_b32_e32 v0, 0xffff0000, v104
	v_and_b32_e32 v38, 0xffff0000, v38
	v_mul_f32_e32 v43, v38, v0
	v_lshlrev_b32_e32 v0, 16, v105
	v_lshlrev_b32_e32 v38, 16, v39
	v_mul_f32_e32 v44, v38, v0
	v_and_b32_e32 v0, 0xffff0000, v105
	v_and_b32_e32 v38, 0xffff0000, v39
	v_mul_f32_e32 v45, v38, v0
	v_lshlrev_b32_e32 v0, 16, v106
	v_lshlrev_b32_e32 v38, 16, v40
	v_mul_f32_e32 v38, v38, v0
	v_and_b32_e32 v0, 0xffff0000, v106
	v_and_b32_e32 v39, 0xffff0000, v40
	v_mul_f32_e32 v39, v39, v0
	v_lshlrev_b32_e32 v0, 16, v107
	v_lshlrev_b32_e32 v40, 16, v41
	v_mul_f32_e32 v40, v40, v0
	v_and_b32_e32 v0, 0xffff0000, v107
	v_and_b32_e32 v41, 0xffff0000, v41
	v_mul_f32_e32 v41, v41, v0
	s_waitcnt lgkmcnt(0)
	v_lshlrev_b32_e32 v0, 16, v108
	s_waitcnt vmcnt(8)
	v_lshlrev_b32_e32 v99, 16, v34
	v_mul_f32_e32 v105, v99, v0
	v_and_b32_e32 v0, 0xffff0000, v108
	v_and_b32_e32 v34, 0xffff0000, v34
	v_mul_f32_e32 v106, v34, v0
	v_lshlrev_b32_e32 v0, 16, v109
	v_lshlrev_b32_e32 v34, 16, v35
	v_mul_f32_e32 v107, v34, v0
	v_and_b32_e32 v0, 0xffff0000, v109
	v_and_b32_e32 v34, 0xffff0000, v35
	v_mul_f32_e32 v108, v34, v0
	v_lshlrev_b32_e32 v0, 16, v110
	v_lshlrev_b32_e32 v34, 16, v36
	v_mul_f32_e32 v99, v34, v0
	v_and_b32_e32 v0, 0xffff0000, v110
	v_and_b32_e32 v34, 0xffff0000, v36
	v_mul_f32_e32 v36, v34, v0
	v_lshlrev_b32_e32 v0, 16, v111
	v_lshlrev_b32_e32 v34, 16, v37
	v_mul_f32_e32 v104, v34, v0
	v_and_b32_e32 v0, 0xffff0000, v111
	v_and_b32_e32 v34, 0xffff0000, v37
	v_mul_f32_e32 v37, v34, v0
	v_max3_f32 v0, |v71|, 0, |v72|
	v_max3_f32 v0, v0, |v73|, |v74|
	v_max3_f32 v0, v0, |v62|, |v63|
	v_max3_f32 v0, v0, |v64|, |v65|
	s_nop 1
	v_max_f32_dpp v0, v0, v0 quad_perm:[1,0,3,2] row_mask:0xf bank_mask:0xf
	s_nop 1
	v_max_f32_dpp v0, v0, v0 quad_perm:[2,3,0,1] row_mask:0xf bank_mask:0xf
	s_nop 1
	v_max_f32_dpp v0, v0, v0 row_half_mirror row_mask:0xf bank_mask:0xf
	s_nop 1
	v_max_f32_dpp v0, v0, v0 row_ror:8 row_mask:0xf bank_mask:0xf
	v_mov_b32_e32 v114, v0
	s_nop 1
	v_permlane16_swap_b32_e32 v0, v114
	s_nop 0
	v_max_f32_e32 v0, v0, v114
	v_mov_b32_e32 v114, v0
	s_nop 1
	v_permlane32_swap_b32_e32 v0, v114
	s_nop 0
	v_max_f32_e32 v0, v0, v114
	v_mov_b32_e32 v114, v0
	v_max3_f32 v34, |v79|, 0, |v80|
	v_max3_f32 v34, v34, |v81|, |v82|
	v_max3_f32 v34, v34, |v75|, |v76|
	v_max3_f32 v34, v34, |v77|, |v78|
	s_waitcnt lgkmcnt(0)
	v_max_f32_e32 v114, v114, v114
	v_max_f32_e32 v0, v0, v114
	s_nop 1
	v_max_f32_dpp v34, v34, v34 quad_perm:[1,0,3,2] row_mask:0xf bank_mask:0xf
	s_nop 1
	v_max_f32_dpp v34, v34, v34 quad_perm:[2,3,0,1] row_mask:0xf bank_mask:0xf
	s_nop 1
	v_max_f32_dpp v34, v34, v34 row_half_mirror row_mask:0xf bank_mask:0xf
	s_nop 1
	v_max_f32_dpp v34, v34, v34 row_ror:8 row_mask:0xf bank_mask:0xf
	v_mov_b32_e32 v114, v34
	s_nop 1
	v_permlane16_swap_b32_e32 v34, v114
	s_nop 0
	v_max_f32_e32 v34, v34, v114
	v_mov_b32_e32 v114, v34
	s_nop 1
	v_permlane32_swap_b32_e32 v34, v114
	s_nop 0
	v_max_f32_e32 v34, v34, v114
	v_mov_b32_e32 v114, v34
	v_max3_f32 v35, |v58|, 0, |v59|
	v_max3_f32 v35, v35, |v60|, |v61|
	v_max3_f32 v35, v35, |v54|, |v55|
	v_max3_f32 v35, v35, |v56|, |v57|
	s_waitcnt lgkmcnt(0)
	v_max_f32_e32 v114, v114, v114
	v_max_f32_e32 v34, v34, v114
	s_nop 1
	v_max_f32_dpp v35, v35, v35 quad_perm:[1,0,3,2] row_mask:0xf bank_mask:0xf
	s_nop 1
	v_max_f32_dpp v35, v35, v35 quad_perm:[2,3,0,1] row_mask:0xf bank_mask:0xf
	s_nop 1
	v_max_f32_dpp v35, v35, v35 row_half_mirror row_mask:0xf bank_mask:0xf
	s_nop 1
	v_max_f32_dpp v35, v35, v35 row_ror:8 row_mask:0xf bank_mask:0xf
	v_mov_b32_e32 v114, v35
	s_nop 1
	v_permlane16_swap_b32_e32 v35, v114
	s_nop 0
	v_max_f32_e32 v35, v35, v114
	v_mov_b32_e32 v114, v35
	s_nop 1
	v_permlane32_swap_b32_e32 v35, v114
	s_nop 0
	v_max_f32_e32 v35, v35, v114
	v_mov_b32_e32 v114, v35
	v_max3_f32 v109, |v87|, 0, |v88|
	v_max3_f32 v109, v109, |v89|, |v90|
	v_max3_f32 v109, v109, |v83|, |v84|
	v_max3_f32 v109, v109, |v85|, |v86|
	s_waitcnt lgkmcnt(0)
	v_max_f32_e32 v114, v114, v114
	v_max_f32_e32 v35, v35, v114
	s_nop 1
	v_max_f32_dpp v109, v109, v109 quad_perm:[1,0,3,2] row_mask:0xf bank_mask:0xf
	s_nop 1
	v_max_f32_dpp v109, v109, v109 quad_perm:[2,3,0,1] row_mask:0xf bank_mask:0xf
	s_nop 1
	v_max_f32_dpp v109, v109, v109 row_half_mirror row_mask:0xf bank_mask:0xf
	s_nop 1
	v_max_f32_dpp v109, v109, v109 row_ror:8 row_mask:0xf bank_mask:0xf
	v_mov_b32_e32 v114, v109
	s_nop 1
	v_permlane16_swap_b32_e32 v109, v114
	s_nop 0
	v_max_f32_e32 v109, v109, v114
	v_mov_b32_e32 v114, v109
	s_nop 1
	v_permlane32_swap_b32_e32 v109, v114
	s_nop 0
	v_max_f32_e32 v109, v109, v114
	v_mov_b32_e32 v114, v109
	v_max3_f32 v110, |v50|, 0, |v51|
	v_max3_f32 v110, v110, |v52|, |v53|
	v_max3_f32 v110, v110, |v46|, |v47|
	v_max3_f32 v110, v110, |v48|, |v49|
	s_waitcnt lgkmcnt(0)
	v_max_f32_e32 v114, v114, v114
	v_max_f32_e32 v109, v109, v114
	s_nop 1
	v_max_f32_dpp v110, v110, v110 quad_perm:[1,0,3,2] row_mask:0xf bank_mask:0xf
	s_nop 1
	v_max_f32_dpp v110, v110, v110 quad_perm:[2,3,0,1] row_mask:0xf bank_mask:0xf
	s_nop 1
	v_max_f32_dpp v110, v110, v110 row_half_mirror row_mask:0xf bank_mask:0xf
	s_nop 1
	v_max_f32_dpp v110, v110, v110 row_ror:8 row_mask:0xf bank_mask:0xf
	v_mov_b32_e32 v114, v110
	s_nop 1
	v_permlane16_swap_b32_e32 v110, v114
	s_nop 0
	v_max_f32_e32 v110, v110, v114
	v_mov_b32_e32 v114, v110
	s_nop 1
	v_permlane32_swap_b32_e32 v110, v114
	s_nop 0
	v_max_f32_e32 v110, v110, v114
	v_mov_b32_e32 v114, v110
	v_max3_f32 v111, |v95|, 0, |v96|
	v_max3_f32 v111, v111, |v97|, |v98|
	v_max3_f32 v111, v111, |v91|, |v92|
	v_max3_f32 v111, v111, |v93|, |v94|
	s_waitcnt lgkmcnt(0)
	v_max_f32_e32 v114, v114, v114
	v_max_f32_e32 v110, v110, v114
	s_nop 1
	v_max_f32_dpp v111, v111, v111 quad_perm:[1,0,3,2] row_mask:0xf bank_mask:0xf
	s_nop 1
	v_max_f32_dpp v111, v111, v111 quad_perm:[2,3,0,1] row_mask:0xf bank_mask:0xf
	s_nop 1
	v_max_f32_dpp v111, v111, v111 row_half_mirror row_mask:0xf bank_mask:0xf
	s_nop 1
	v_max_f32_dpp v111, v111, v111 row_ror:8 row_mask:0xf bank_mask:0xf
	v_mov_b32_e32 v114, v111
	s_nop 1
	v_permlane16_swap_b32_e32 v111, v114
	s_nop 0
	v_max_f32_e32 v111, v111, v114
	v_mov_b32_e32 v114, v111
	s_nop 1
	v_permlane32_swap_b32_e32 v111, v114
	s_nop 0
	v_max_f32_e32 v111, v111, v114
	v_mov_b32_e32 v114, v111
	v_max3_f32 v112, |v42|, 0, |v43|
	v_max3_f32 v112, v112, |v44|, |v45|
	v_max3_f32 v112, v112, |v38|, |v39|
	v_max3_f32 v112, v112, |v40|, |v41|
	s_waitcnt lgkmcnt(0)
	v_max_f32_e32 v114, v114, v114
	v_max_f32_e32 v111, v111, v114
	s_nop 1
	v_max_f32_dpp v112, v112, v112 quad_perm:[1,0,3,2] row_mask:0xf bank_mask:0xf
	s_nop 1
	v_max_f32_dpp v112, v112, v112 quad_perm:[2,3,0,1] row_mask:0xf bank_mask:0xf
	s_nop 1
	v_max_f32_dpp v112, v112, v112 row_half_mirror row_mask:0xf bank_mask:0xf
	s_nop 1
	v_max_f32_dpp v112, v112, v112 row_ror:8 row_mask:0xf bank_mask:0xf
	v_mov_b32_e32 v114, v112
	s_nop 1
	v_permlane16_swap_b32_e32 v112, v114
	s_nop 0
	v_max_f32_e32 v112, v112, v114
	v_mov_b32_e32 v114, v112
	s_nop 1
	v_permlane32_swap_b32_e32 v112, v114
	s_nop 0
	v_max_f32_e32 v112, v112, v114
	v_mov_b32_e32 v114, v112
	v_max3_f32 v113, |v105|, 0, |v106|
	v_max3_f32 v113, v113, |v107|, |v108|
	v_max3_f32 v113, v113, |v99|, |v36|
	v_max3_f32 v113, v113, |v104|, |v37|
	s_waitcnt lgkmcnt(0)
	v_max_f32_e32 v114, v114, v114
	v_max_f32_e32 v112, v112, v114
	s_nop 1
	v_max_f32_dpp v113, v113, v113 quad_perm:[1,0,3,2] row_mask:0xf bank_mask:0xf
	s_nop 1
	v_max_f32_dpp v113, v113, v113 quad_perm:[2,3,0,1] row_mask:0xf bank_mask:0xf
	s_nop 1
	v_max_f32_dpp v113, v113, v113 row_half_mirror row_mask:0xf bank_mask:0xf
	s_nop 1
	v_max_f32_dpp v113, v113, v113 row_ror:8 row_mask:0xf bank_mask:0xf
	v_mov_b32_e32 v114, v113
	s_nop 1
	v_permlane16_swap_b32_e32 v113, v114
	s_nop 0
	v_max_f32_e32 v113, v113, v114
	v_mov_b32_e32 v114, v113
	s_nop 1
	v_permlane32_swap_b32_e32 v113, v114
	s_nop 0
	v_max_f32_e32 v113, v113, v114
	v_mov_b32_e32 v114, v113
	s_waitcnt lgkmcnt(0)
	v_max_f32_e32 v114, v114, v114
	v_max_f32_e32 v113, v113, v114
	v_mov_b32_e32 v114, v0
	s_waitcnt lgkmcnt(0)
	v_max_f32_e32 v114, v114, v114
	v_max_f32_e32 v0, v0, v114
	v_mov_b32_e32 v114, v34
	s_waitcnt lgkmcnt(0)
	v_max_f32_e32 v114, v114, v114
	v_max_f32_e32 v34, v34, v114
	v_mov_b32_e32 v114, v35
	s_waitcnt lgkmcnt(0)
	v_max_f32_e32 v114, v114, v114
	v_max_f32_e32 v35, v35, v114
	v_mov_b32_e32 v114, v109
	s_waitcnt lgkmcnt(0)
	v_max_f32_e32 v114, v114, v114
	v_max_f32_e32 v109, v109, v114
	v_mov_b32_e32 v114, v110
	s_waitcnt lgkmcnt(0)
	v_max_f32_e32 v114, v114, v114
	v_max_f32_e32 v110, v110, v114
	v_mov_b32_e32 v114, v111
	s_waitcnt lgkmcnt(0)
	v_max_f32_e32 v114, v114, v114
	v_max_f32_e32 v111, v111, v114
	v_mov_b32_e32 v114, v112
	s_waitcnt lgkmcnt(0)
	v_max_f32_e32 v114, v114, v114
	v_max_f32_e32 v112, v112, v114
	v_mov_b32_e32 v114, v113
	s_waitcnt lgkmcnt(0)
	v_max_f32_e32 v114, v114, v114
	v_max_f32_e32 v113, v113, v114
	v_mov_b32_e32 v114, v0
	s_waitcnt lgkmcnt(0)
	v_max_f32_e32 v114, v114, v114
	v_max_f32_e32 v0, v0, v114
	v_mov_b32_e32 v114, v34
	s_waitcnt lgkmcnt(0)
	v_max_f32_e32 v114, v114, v114
	v_max_f32_e32 v34, v34, v114
	v_mov_b32_e32 v114, v35
	s_waitcnt lgkmcnt(0)
	v_max_f32_e32 v114, v114, v114
	v_max_f32_e32 v35, v35, v114
	v_mov_b32_e32 v114, v109
	s_waitcnt lgkmcnt(0)
	v_max_f32_e32 v114, v114, v114
	v_max_f32_e32 v109, v109, v114
	v_mov_b32_e32 v114, v110
	s_waitcnt lgkmcnt(0)
	v_max_f32_e32 v114, v114, v114
	v_max_f32_e32 v110, v110, v114
	v_mov_b32_e32 v114, v111
	s_waitcnt lgkmcnt(0)
	v_max_f32_e32 v114, v114, v114
	v_max_f32_e32 v111, v111, v114
	v_mov_b32_e32 v114, v112
	s_waitcnt lgkmcnt(0)
	v_max_f32_e32 v114, v114, v114
	v_max_f32_e32 v112, v112, v114
	v_mov_b32_e32 v114, v113
	s_waitcnt lgkmcnt(0)
	v_max_f32_e32 v114, v114, v114
	v_max_f32_e32 v113, v113, v114
	v_mov_b32_e32 v114, v0
	s_waitcnt lgkmcnt(0)
	v_max_f32_e32 v114, v114, v114
	v_max_f32_e32 v0, v0, v114
	v_mov_b32_e32 v114, v34
	s_waitcnt lgkmcnt(0)
	v_max_f32_e32 v114, v114, v114
	v_max_f32_e32 v34, v34, v114
	v_mov_b32_e32 v114, v35
	s_waitcnt lgkmcnt(0)
	v_max_f32_e32 v114, v114, v114
	v_max_f32_e32 v35, v35, v114
	v_mov_b32_e32 v114, v109
	s_waitcnt lgkmcnt(0)
	v_max_f32_e32 v114, v114, v114
	v_max_f32_e32 v109, v109, v114
	v_mov_b32_e32 v114, v110
	s_waitcnt lgkmcnt(0)
	v_max_f32_e32 v114, v114, v114
	v_max_f32_e32 v110, v110, v114
	v_mov_b32_e32 v114, v111
	s_waitcnt lgkmcnt(0)
	v_max_f32_e32 v114, v114, v114
	v_max_f32_e32 v111, v111, v114
	v_mov_b32_e32 v114, v112
	s_waitcnt lgkmcnt(0)
	v_max_f32_e32 v114, v114, v114
	v_max_f32_e32 v112, v112, v114
	v_mov_b32_e32 v114, v113
	s_waitcnt lgkmcnt(0)
	v_max_f32_e32 v114, v114, v114
	v_max_f32_e32 v114, v113, v114
	v_mov_b32_e32 v113, v0
	s_waitcnt lgkmcnt(0)
	v_max_f32_e32 v113, v113, v113
	v_max_f32_e32 v0, v0, v113
	v_mov_b32_e32 v113, v34
	s_waitcnt lgkmcnt(0)
	v_max_f32_e32 v113, v113, v113
	v_max_f32_e32 v120, v34, v113
	v_mov_b32_e32 v34, v35
	v_mov_b32_e32 v122, v120
	s_waitcnt lgkmcnt(0)
	v_max_f32_e32 v34, v34, v34
	v_max_f32_e32 v118, v35, v34
	v_mov_b32_e32 v34, v109
	v_mov_b32_e32 v121, v118
	s_waitcnt lgkmcnt(0)
	v_max_f32_e32 v34, v34, v34
	v_max_f32_e32 v116, v109, v34
	v_mov_b32_e32 v34, v110
	v_mov_b32_e32 v119, v116
	s_waitcnt lgkmcnt(0)
	v_max_f32_e32 v34, v34, v34
	v_max_f32_e32 v115, v110, v34
	v_mov_b32_e32 v34, v111
	v_mov_b32_e32 v117, v115
	s_waitcnt lgkmcnt(0)
	v_max_f32_e32 v34, v34, v34
	v_max_f32_e32 v113, v111, v34
	v_mov_b32_e32 v34, v112
	s_waitcnt lgkmcnt(0)
	v_max_f32_e32 v34, v34, v34
	v_max_f32_e32 v111, v112, v34
	v_mov_b32_e32 v34, v114
	v_mov_b32_e32 v112, v111
	s_waitcnt lgkmcnt(0)
	v_max_f32_e32 v34, v34, v34
	v_max_f32_e32 v109, v114, v34
	v_mov_b32_e32 v34, v0
	v_mov_b32_e32 v114, v113
	v_mov_b32_e32 v110, v109
	s_waitcnt lgkmcnt(0)
	v_max3_f32 v123, v0, v34, s72
	s_and_saveexec_b64 s[12:13], s[6:7]
	s_cbranch_execz .LBB0_490
	s_lshl_b64 s[4:5], s[16:17], 2
	s_add_u32 s4, s18, s4
	s_addc_u32 s5, s19, s5
	v_mul_f32_e32 v0, 0x3c010204, v123
	global_store_dword v1, v0, s[4:5]

.LBB0_504:
	s_or_b64 exec, exec, s[12:13]
	v_div_scale_f32 v38, s[4:5], v0, v0, s73
	v_rcp_f32_e32 v39, v38
	s_lshl_b64 s[4:5], s[10:11], 9
	s_waitcnt vmcnt(7)
	v_lshlrev_b32_e32 v71, 16, v2
	v_and_b32_e32 v2, 0xffff0000, v2
	v_fma_f32 v40, -v38, v39, 1.0
	v_fmac_f32_e32 v39, v40, v39
	v_div_scale_f32 v40, vcc, s73, v0, s73
	v_mul_f32_e32 v41, v40, v39
	v_fma_f32 v42, -v38, v41, v40
	v_fmac_f32_e32 v41, v42, v39
	v_fma_f32 v38, -v38, v41, v40
	v_div_fmas_f32 v38, v38, v39, v41
	v_div_fixup_f32 v0, v38, v0, s73
	v_mul_f32_e32 v39, v106, v0
	v_mul_f32_e32 v40, v107, v0
	v_mul_f32_e32 v38, v105, v0
	v_mul_f32_e32 v41, v108, v0
	v_rndne_f32_e32 v39, v39
	v_rndne_f32_e32 v40, v40
	v_rndne_f32_e32 v38, v38
	v_cvt_i32_f32_e32 v39, v39
	v_cvt_i32_f32_e32 v40, v40
	v_rndne_f32_e32 v41, v41
	v_cvt_i32_f32_e32 v38, v38
	v_cvt_i32_f32_e32 v41, v41
	v_med3_i32 v39, v39, s84, v236
	v_med3_i32 v40, v40, s84, v236
	v_med3_i32 v38, v38, s84, v236
	v_med3_i32 v41, v41, s84, v236
	v_lshlrev_b32_e32 v39, 8, v39
	v_lshlrev_b32_e32 v40, 16, v40
	v_and_b32_e32 v39, 0xff00, v39
	v_and_b32_e32 v40, 0xff0000, v40
	v_perm_b32 v38, v41, v38, s60
	v_or3_b32 v38, v38, v39, v40
	v_mul_f32_e32 v39, v99, v0
	v_mul_f32_e32 v36, v36, v0
	v_mul_f32_e32 v40, v104, v0
	v_mul_f32_e32 v0, v37, v0
	v_rndne_f32_e32 v37, v39
	v_rndne_f32_e32 v36, v36
	v_rndne_f32_e32 v39, v40
	v_cvt_i32_f32_e32 v36, v36
	v_cvt_i32_f32_e32 v39, v39
	v_rndne_f32_e32 v0, v0
	v_cvt_i32_f32_e32 v37, v37
	v_cvt_i32_f32_e32 v0, v0
	v_med3_i32 v36, v36, s84, v236
	v_med3_i32 v39, v39, s84, v236
	v_med3_i32 v37, v37, s84, v236
	v_med3_i32 v0, v0, s84, v236
	v_lshlrev_b32_e32 v36, 8, v36
	v_lshlrev_b32_e32 v39, 16, v39
	v_and_b32_e32 v36, 0xff00, v36
	v_and_b32_e32 v39, 0xff0000, v39
	v_perm_b32 v0, v0, v37, s60
	v_or3_b32 v39, v0, v36, v39
	v_lshl_add_u64 v[36:37], v[34:35], 0, s[4:5]
	s_or_b32 s4, s23, 8
	s_mulk_i32 s4, 0x410
	v_add_u32_e32 v0, s4, v70
	global_store_dwordx2 v[36:37], v[38:39], off
	ds_read_b128 v[36:39], v0
	ds_read_b128 v[72:75], v69 offset:13520
	v_lshlrev_b32_e32 v40, 16, v30
	v_and_b32_e32 v30, 0xffff0000, v30
	s_add_u32 s10, s20, 0xffffff90
	s_waitcnt lgkmcnt(1)
	v_lshlrev_b32_e32 v0, 16, v36
	v_mul_f32_e32 v63, v40, v0
	v_and_b32_e32 v0, 0xffff0000, v36
	v_mul_f32_e32 v64, v30, v0
	v_lshlrev_b32_e32 v0, 16, v37
	v_lshlrev_b32_e32 v30, 16, v31
	v_mul_f32_e32 v65, v30, v0
	v_and_b32_e32 v0, 0xffff0000, v37
	v_and_b32_e32 v30, 0xffff0000, v31
	v_mul_f32_e32 v70, v30, v0
	v_lshlrev_b32_e32 v0, 16, v38
	v_lshlrev_b32_e32 v30, 16, v32
	v_mul_f32_e32 v59, v30, v0
	v_and_b32_e32 v0, 0xffff0000, v38
	v_and_b32_e32 v30, 0xffff0000, v32
	v_mul_f32_e32 v60, v30, v0
	v_lshlrev_b32_e32 v0, 16, v39
	v_lshlrev_b32_e32 v30, 16, v33
	v_mul_f32_e32 v61, v30, v0
	v_and_b32_e32 v0, 0xffff0000, v39
	v_and_b32_e32 v30, 0xffff0000, v33
	v_mul_f32_e32 v62, v30, v0
	ds_read_b128 v[30:33], v69 offset:9360
	v_lshlrev_b32_e32 v36, 16, v26
	v_and_b32_e32 v26, 0xffff0000, v26
	s_addc_u32 s11, s21, -1
	s_waitcnt lgkmcnt(0)
	v_lshlrev_b32_e32 v0, 16, v30
	v_mul_f32_e32 v55, v36, v0
	v_and_b32_e32 v0, 0xffff0000, v30
	v_mul_f32_e32 v56, v26, v0
	v_lshlrev_b32_e32 v0, 16, v31
	v_lshlrev_b32_e32 v26, 16, v27
	v_mul_f32_e32 v57, v26, v0
	v_and_b32_e32 v0, 0xffff0000, v31
	v_and_b32_e32 v26, 0xffff0000, v27
	v_mul_f32_e32 v58, v26, v0
	v_lshlrev_b32_e32 v0, 16, v32
	v_lshlrev_b32_e32 v26, 16, v28
	v_mul_f32_e32 v51, v26, v0
	v_and_b32_e32 v0, 0xffff0000, v32
	v_and_b32_e32 v26, 0xffff0000, v28
	v_mul_f32_e32 v52, v26, v0
	v_lshlrev_b32_e32 v0, 16, v33
	v_lshlrev_b32_e32 v26, 16, v29
	v_mul_f32_e32 v53, v26, v0
	v_and_b32_e32 v0, 0xffff0000, v33
	v_and_b32_e32 v26, 0xffff0000, v29
	v_mul_f32_e32 v54, v26, v0
	ds_read_b128 v[26:29], v69 offset:10400
	v_lshlrev_b32_e32 v30, 16, v22
	v_and_b32_e32 v22, 0xffff0000, v22
	s_waitcnt lgkmcnt(0)
	v_lshlrev_b32_e32 v0, 16, v26
	v_mul_f32_e32 v47, v30, v0
	v_and_b32_e32 v0, 0xffff0000, v26
	v_mul_f32_e32 v48, v22, v0
	v_lshlrev_b32_e32 v0, 16, v27
	v_lshlrev_b32_e32 v22, 16, v23
	v_mul_f32_e32 v49, v22, v0
	v_and_b32_e32 v0, 0xffff0000, v27
	v_and_b32_e32 v22, 0xffff0000, v23
	v_mul_f32_e32 v50, v22, v0
	v_lshlrev_b32_e32 v0, 16, v28
	v_lshlrev_b32_e32 v22, 16, v24
	v_mul_f32_e32 v43, v22, v0
	v_and_b32_e32 v0, 0xffff0000, v28
	v_and_b32_e32 v22, 0xffff0000, v24
	v_mul_f32_e32 v44, v22, v0
	v_lshlrev_b32_e32 v0, 16, v29
	v_lshlrev_b32_e32 v22, 16, v25
	v_mul_f32_e32 v45, v22, v0
	v_and_b32_e32 v0, 0xffff0000, v29
	v_and_b32_e32 v22, 0xffff0000, v25
	v_mul_f32_e32 v46, v22, v0
	ds_read_b128 v[22:25], v69 offset:11440
	v_lshlrev_b32_e32 v26, 16, v18
	v_and_b32_e32 v18, 0xffff0000, v18
	s_waitcnt lgkmcnt(0)
	v_lshlrev_b32_e32 v0, 16, v22
	v_mul_f32_e32 v39, v26, v0
	v_and_b32_e32 v0, 0xffff0000, v22
	v_mul_f32_e32 v40, v18, v0
	v_lshlrev_b32_e32 v0, 16, v23
	v_lshlrev_b32_e32 v18, 16, v19
	v_mul_f32_e32 v41, v18, v0
	v_and_b32_e32 v0, 0xffff0000, v23
	v_and_b32_e32 v18, 0xffff0000, v19
	v_mul_f32_e32 v42, v18, v0
	v_lshlrev_b32_e32 v0, 16, v24
	v_lshlrev_b32_e32 v18, 16, v20
	v_mul_f32_e32 v33, v18, v0
	v_and_b32_e32 v0, 0xffff0000, v24
	v_and_b32_e32 v18, 0xffff0000, v20
	v_mul_f32_e32 v36, v18, v0
	v_lshlrev_b32_e32 v0, 16, v25
	v_lshlrev_b32_e32 v18, 16, v21
	v_mul_f32_e32 v37, v18, v0
	v_and_b32_e32 v0, 0xffff0000, v25
	v_and_b32_e32 v18, 0xffff0000, v21
	v_mul_f32_e32 v38, v18, v0
	ds_read_b128 v[18:21], v69 offset:12480
	v_lshlrev_b32_e32 v22, 16, v14
	v_and_b32_e32 v14, 0xffff0000, v14
	s_waitcnt lgkmcnt(0)
	v_lshlrev_b32_e32 v0, 16, v18
	v_mul_f32_e32 v29, v22, v0
	v_and_b32_e32 v0, 0xffff0000, v18
	v_mul_f32_e32 v30, v14, v0
	v_lshlrev_b32_e32 v0, 16, v19
	v_lshlrev_b32_e32 v14, 16, v15
	v_mul_f32_e32 v31, v14, v0
	v_and_b32_e32 v0, 0xffff0000, v19
	v_and_b32_e32 v14, 0xffff0000, v15
	v_mul_f32_e32 v32, v14, v0
	v_lshlrev_b32_e32 v0, 16, v20
	v_lshlrev_b32_e32 v14, 16, v16
	v_mul_f32_e32 v25, v14, v0
	v_and_b32_e32 v0, 0xffff0000, v20
	v_and_b32_e32 v14, 0xffff0000, v16
	v_mul_f32_e32 v26, v14, v0
	v_lshlrev_b32_e32 v0, 16, v21
	v_lshlrev_b32_e32 v14, 16, v17
	v_mul_f32_e32 v27, v14, v0
	v_and_b32_e32 v0, 0xffff0000, v21
	v_and_b32_e32 v14, 0xffff0000, v17
	v_mul_f32_e32 v28, v14, v0
	v_lshlrev_b32_e32 v0, 16, v72
	v_lshlrev_b32_e32 v14, 16, v10
	v_mul_f32_e32 v21, v14, v0
	v_and_b32_e32 v0, 0xffff0000, v72
	v_and_b32_e32 v10, 0xffff0000, v10
	v_mul_f32_e32 v22, v10, v0
	v_lshlrev_b32_e32 v0, 16, v73
	v_lshlrev_b32_e32 v10, 16, v11
	v_mul_f32_e32 v23, v10, v0
	v_and_b32_e32 v0, 0xffff0000, v73
	v_and_b32_e32 v10, 0xffff0000, v11
	v_mul_f32_e32 v24, v10, v0
	v_lshlrev_b32_e32 v0, 16, v74
	v_lshlrev_b32_e32 v10, 16, v12
	v_mul_f32_e32 v17, v10, v0
	v_and_b32_e32 v0, 0xffff0000, v74
	v_and_b32_e32 v10, 0xffff0000, v12
	v_mul_f32_e32 v18, v10, v0
	v_lshlrev_b32_e32 v0, 16, v75
	v_lshlrev_b32_e32 v10, 16, v13
	v_mul_f32_e32 v19, v10, v0
	v_and_b32_e32 v0, 0xffff0000, v75
	ds_read_b128 v[72:75], v69 offset:14560
	v_and_b32_e32 v10, 0xffff0000, v13
	v_mul_f32_e32 v20, v10, v0
	v_lshlrev_b32_e32 v10, 16, v6
	v_and_b32_e32 v6, 0xffff0000, v6
	s_waitcnt lgkmcnt(0)
	v_lshlrev_b32_e32 v0, 16, v72
	v_mul_f32_e32 v13, v10, v0
	v_and_b32_e32 v0, 0xffff0000, v72
	v_mul_f32_e32 v14, v6, v0
	v_lshlrev_b32_e32 v0, 16, v73
	v_lshlrev_b32_e32 v6, 16, v7
	v_mul_f32_e32 v15, v6, v0
	v_and_b32_e32 v0, 0xffff0000, v73
	v_and_b32_e32 v6, 0xffff0000, v7
	v_mul_f32_e32 v16, v6, v0
	v_lshlrev_b32_e32 v0, 16, v74
	v_lshlrev_b32_e32 v6, 16, v8
	v_mul_f32_e32 v0, v6, v0
	v_and_b32_e32 v6, 0xffff0000, v74
	v_and_b32_e32 v7, 0xffff0000, v8
	v_mul_f32_e32 v10, v7, v6
	v_lshlrev_b32_e32 v6, 16, v75
	v_lshlrev_b32_e32 v7, 16, v9
	v_mul_f32_e32 v11, v7, v6
	v_and_b32_e32 v6, 0xffff0000, v75
	v_and_b32_e32 v7, 0xffff0000, v9
	v_mul_f32_e32 v12, v7, v6
	ds_read_b128 v[6:9], v69 offset:15600
	v_max3_f32 v72, |v47|, 0, |v48|
	v_max3_f32 v72, v72, |v49|, |v50|
	v_max3_f32 v72, v72, |v43|, |v44|
	v_max3_f32 v72, v72, |v45|, |v46|
	s_waitcnt lgkmcnt(0)
	v_lshlrev_b32_e32 v69, 16, v6
	v_and_b32_e32 v6, 0xffff0000, v6
	v_mul_f32_e32 v69, v71, v69
	v_mul_f32_e32 v6, v2, v6
	v_lshlrev_b32_e32 v2, 16, v7
	v_lshlrev_b32_e32 v71, 16, v3
	v_mul_f32_e32 v71, v71, v2
	v_and_b32_e32 v2, 0xffff0000, v7
	v_and_b32_e32 v3, 0xffff0000, v3
	v_mul_f32_e32 v7, v3, v2
	v_lshlrev_b32_e32 v2, 16, v8
	v_lshlrev_b32_e32 v3, 16, v4
	v_mul_f32_e32 v2, v3, v2
	v_and_b32_e32 v3, 0xffff0000, v8
	v_and_b32_e32 v4, 0xffff0000, v4
	v_mul_f32_e32 v3, v4, v3
	v_lshlrev_b32_e32 v4, 16, v9
	v_lshlrev_b32_e32 v8, 16, v5
	v_mul_f32_e32 v4, v8, v4
	v_and_b32_e32 v8, 0xffff0000, v9
	v_and_b32_e32 v5, 0xffff0000, v5
	v_mul_f32_e32 v5, v5, v8
	v_max3_f32 v8, |v63|, 0, |v64|
	v_max3_f32 v8, v8, |v65|, |v70|
	v_max3_f32 v8, v8, |v59|, |v60|
	v_max3_f32 v8, v8, |v61|, |v62|
	s_nop 1
	v_max_f32_dpp v8, v8, v8 quad_perm:[1,0,3,2] row_mask:0xf bank_mask:0xf
	s_nop 1
	v_max_f32_dpp v8, v8, v8 quad_perm:[2,3,0,1] row_mask:0xf bank_mask:0xf
	s_nop 1
	v_max_f32_dpp v8, v8, v8 row_half_mirror row_mask:0xf bank_mask:0xf
	s_nop 1
	v_max_f32_dpp v8, v8, v8 row_ror:8 row_mask:0xf bank_mask:0xf
	v_mov_b32_e32 v78, v8
	s_nop 1
	v_permlane16_swap_b32_e32 v8, v78
	s_nop 0
	v_max_f32_e32 v8, v8, v78
	v_mov_b32_e32 v78, v8
	s_nop 1
	v_permlane32_swap_b32_e32 v8, v78
	s_nop 0
	v_max_f32_e32 v8, v8, v78
	v_mov_b32_e32 v78, v8
	v_max3_f32 v9, |v55|, 0, |v56|
	v_max3_f32 v9, v9, |v57|, |v58|
	v_max3_f32 v9, v9, |v51|, |v52|
	v_max3_f32 v9, v9, |v53|, |v54|
	s_waitcnt lgkmcnt(0)
	v_max_f32_e32 v78, v78, v78
	v_max_f32_e32 v8, v8, v78
	s_nop 1
	v_max_f32_dpp v9, v9, v9 quad_perm:[1,0,3,2] row_mask:0xf bank_mask:0xf
	s_nop 1
	v_max_f32_dpp v9, v9, v9 quad_perm:[2,3,0,1] row_mask:0xf bank_mask:0xf
	s_nop 1
	v_max_f32_dpp v9, v9, v9 row_half_mirror row_mask:0xf bank_mask:0xf
	s_nop 1
	v_max_f32_dpp v9, v9, v9 row_ror:8 row_mask:0xf bank_mask:0xf
	v_mov_b32_e32 v78, v9
	s_nop 1
	v_permlane16_swap_b32_e32 v9, v78
	s_nop 0
	v_max_f32_e32 v9, v9, v78
	v_mov_b32_e32 v78, v9
	s_nop 1
	v_permlane32_swap_b32_e32 v9, v78
	s_nop 0
	v_max_f32_e32 v9, v9, v78
	v_mov_b32_e32 v78, v9
	v_max3_f32 v73, |v39|, 0, |v40|
	v_max3_f32 v73, v73, |v41|, |v42|
	v_max3_f32 v73, v73, |v33|, |v36|
	v_max3_f32 v73, v73, |v37|, |v38|
	s_waitcnt lgkmcnt(0)
	v_max_f32_e32 v78, v78, v78
	v_max_f32_e32 v9, v9, v78
	s_nop 1
	v_max_f32_dpp v72, v72, v72 quad_perm:[1,0,3,2] row_mask:0xf bank_mask:0xf
	s_nop 1
	v_max_f32_dpp v72, v72, v72 quad_perm:[2,3,0,1] row_mask:0xf bank_mask:0xf
	s_nop 1
	v_max_f32_dpp v72, v72, v72 row_half_mirror row_mask:0xf bank_mask:0xf
	s_nop 1
	v_max_f32_dpp v72, v72, v72 row_ror:8 row_mask:0xf bank_mask:0xf
	v_mov_b32_e32 v78, v72
	s_nop 1
	v_permlane16_swap_b32_e32 v72, v78
	s_nop 0
	v_max_f32_e32 v72, v72, v78
	v_mov_b32_e32 v78, v72
	s_nop 1
	v_permlane32_swap_b32_e32 v72, v78
	s_nop 0
	v_max_f32_e32 v72, v72, v78
	v_mov_b32_e32 v78, v72
	v_max3_f32 v74, |v29|, 0, |v30|
	v_max3_f32 v74, v74, |v31|, |v32|
	v_max3_f32 v74, v74, |v25|, |v26|
	v_max3_f32 v74, v74, |v27|, |v28|
	s_waitcnt lgkmcnt(0)
	v_max_f32_e32 v78, v78, v78
	v_max_f32_e32 v72, v72, v78
	s_nop 1
	v_max_f32_dpp v73, v73, v73 quad_perm:[1,0,3,2] row_mask:0xf bank_mask:0xf
	s_nop 1
	v_max_f32_dpp v73, v73, v73 quad_perm:[2,3,0,1] row_mask:0xf bank_mask:0xf
	s_nop 1
	v_max_f32_dpp v73, v73, v73 row_half_mirror row_mask:0xf bank_mask:0xf
	s_nop 1
	v_max_f32_dpp v73, v73, v73 row_ror:8 row_mask:0xf bank_mask:0xf
	v_mov_b32_e32 v78, v73
	s_nop 1
	v_permlane16_swap_b32_e32 v73, v78
	s_nop 0
	v_max_f32_e32 v73, v73, v78
	v_mov_b32_e32 v78, v73
	s_nop 1
	v_permlane32_swap_b32_e32 v73, v78
	s_nop 0
	v_max_f32_e32 v73, v73, v78
	v_mov_b32_e32 v78, v73
	v_max3_f32 v75, |v21|, 0, |v22|
	v_max3_f32 v75, v75, |v23|, |v24|
	v_max3_f32 v75, v75, |v17|, |v18|
	v_max3_f32 v75, v75, |v19|, |v20|
	s_waitcnt lgkmcnt(0)
	v_max_f32_e32 v78, v78, v78
	v_max_f32_e32 v73, v73, v78
	s_nop 1
	v_max_f32_dpp v74, v74, v74 quad_perm:[1,0,3,2] row_mask:0xf bank_mask:0xf
	s_nop 1
	v_max_f32_dpp v74, v74, v74 quad_perm:[2,3,0,1] row_mask:0xf bank_mask:0xf
	s_nop 1
	v_max_f32_dpp v74, v74, v74 row_half_mirror row_mask:0xf bank_mask:0xf
	s_nop 1
	v_max_f32_dpp v74, v74, v74 row_ror:8 row_mask:0xf bank_mask:0xf
	v_mov_b32_e32 v78, v74
	s_nop 1
	v_permlane16_swap_b32_e32 v74, v78
	s_nop 0
	v_max_f32_e32 v74, v74, v78
	v_mov_b32_e32 v78, v74
	s_nop 1
	v_permlane32_swap_b32_e32 v74, v78
	s_nop 0
	v_max_f32_e32 v74, v74, v78
	v_mov_b32_e32 v78, v74
	v_max3_f32 v76, |v13|, 0, |v14|
	v_max3_f32 v76, v76, |v15|, |v16|
	v_max3_f32 v76, v76, |v0|, |v10|
	v_max3_f32 v76, v76, |v11|, |v12|
	s_waitcnt lgkmcnt(0)
	v_max_f32_e32 v78, v78, v78
	v_max_f32_e32 v74, v74, v78
	s_nop 1
	v_max_f32_dpp v75, v75, v75 quad_perm:[1,0,3,2] row_mask:0xf bank_mask:0xf
	s_nop 1
	v_max_f32_dpp v75, v75, v75 quad_perm:[2,3,0,1] row_mask:0xf bank_mask:0xf
	s_nop 1
	v_max_f32_dpp v75, v75, v75 row_half_mirror row_mask:0xf bank_mask:0xf
	s_nop 1
	v_max_f32_dpp v75, v75, v75 row_ror:8 row_mask:0xf bank_mask:0xf
	v_mov_b32_e32 v78, v75
	s_nop 1
	v_permlane16_swap_b32_e32 v75, v78
	s_nop 0
	v_max_f32_e32 v75, v75, v78
	v_mov_b32_e32 v78, v75
	s_nop 1
	v_permlane32_swap_b32_e32 v75, v78
	s_nop 0
	v_max_f32_e32 v75, v75, v78
	v_mov_b32_e32 v78, v75
	v_max3_f32 v77, |v69|, 0, |v6|
	v_max3_f32 v77, v77, |v71|, |v7|
	v_max3_f32 v77, v77, |v2|, |v3|
	v_max3_f32 v77, v77, |v4|, |v5|
	s_waitcnt lgkmcnt(0)
	v_max_f32_e32 v78, v78, v78
	v_max_f32_e32 v75, v75, v78
	s_nop 1
	v_max_f32_dpp v76, v76, v76 quad_perm:[1,0,3,2] row_mask:0xf bank_mask:0xf
	s_nop 1
	v_max_f32_dpp v76, v76, v76 quad_perm:[2,3,0,1] row_mask:0xf bank_mask:0xf
	s_nop 1
	v_max_f32_dpp v76, v76, v76 row_half_mirror row_mask:0xf bank_mask:0xf
	s_nop 1
	v_max_f32_dpp v76, v76, v76 row_ror:8 row_mask:0xf bank_mask:0xf
	v_mov_b32_e32 v78, v76
	s_nop 1
	v_permlane16_swap_b32_e32 v76, v78
	s_nop 0
	v_max_f32_e32 v76, v76, v78
	v_mov_b32_e32 v78, v76
	s_nop 1
	v_permlane32_swap_b32_e32 v76, v78
	s_nop 0
	v_max_f32_e32 v76, v76, v78
	v_mov_b32_e32 v78, v76
	s_waitcnt lgkmcnt(0)
	v_max_f32_e32 v78, v78, v78
	v_max_f32_e32 v76, v76, v78
	s_nop 1
	v_max_f32_dpp v77, v77, v77 quad_perm:[1,0,3,2] row_mask:0xf bank_mask:0xf
	s_nop 1
	v_max_f32_dpp v77, v77, v77 quad_perm:[2,3,0,1] row_mask:0xf bank_mask:0xf
	s_nop 1
	v_max_f32_dpp v77, v77, v77 row_half_mirror row_mask:0xf bank_mask:0xf
	s_nop 1
	v_max_f32_dpp v77, v77, v77 row_ror:8 row_mask:0xf bank_mask:0xf
	v_mov_b32_e32 v78, v77
	s_nop 1
	v_permlane16_swap_b32_e32 v77, v78
	s_nop 0
	v_max_f32_e32 v77, v77, v78
	v_mov_b32_e32 v78, v77
	s_nop 1
	v_permlane32_swap_b32_e32 v77, v78
	s_nop 0
	v_max_f32_e32 v77, v77, v78
	v_mov_b32_e32 v78, v77
	s_waitcnt lgkmcnt(0)
	v_max_f32_e32 v78, v78, v78
	v_max_f32_e32 v77, v77, v78
	v_mov_b32_e32 v78, v8
	s_waitcnt lgkmcnt(0)
	v_max_f32_e32 v78, v78, v78
	v_max_f32_e32 v8, v8, v78
	v_mov_b32_e32 v78, v9
	s_waitcnt lgkmcnt(0)
	v_max_f32_e32 v78, v78, v78
	v_max_f32_e32 v9, v9, v78
	v_mov_b32_e32 v78, v72
	s_waitcnt lgkmcnt(0)
	v_max_f32_e32 v78, v78, v78
	v_max_f32_e32 v72, v72, v78
	v_mov_b32_e32 v78, v73
	s_waitcnt lgkmcnt(0)
	v_max_f32_e32 v78, v78, v78
	v_max_f32_e32 v73, v73, v78
	v_mov_b32_e32 v78, v74
	s_waitcnt lgkmcnt(0)
	v_max_f32_e32 v78, v78, v78
	v_max_f32_e32 v74, v74, v78
	v_mov_b32_e32 v78, v75
	s_waitcnt lgkmcnt(0)
	v_max_f32_e32 v78, v78, v78
	v_max_f32_e32 v75, v75, v78
	v_mov_b32_e32 v78, v76
	s_waitcnt lgkmcnt(0)
	v_max_f32_e32 v78, v78, v78
	v_max_f32_e32 v76, v76, v78
	v_mov_b32_e32 v78, v77
	s_waitcnt lgkmcnt(0)
	v_max_f32_e32 v78, v78, v78
	v_max_f32_e32 v77, v77, v78
	v_mov_b32_e32 v78, v8
	s_waitcnt lgkmcnt(0)
	v_max_f32_e32 v78, v78, v78
	v_max_f32_e32 v8, v8, v78
	v_mov_b32_e32 v78, v9
	s_waitcnt lgkmcnt(0)
	v_max_f32_e32 v78, v78, v78
	v_max_f32_e32 v9, v9, v78
	v_mov_b32_e32 v78, v72
	s_waitcnt lgkmcnt(0)
	v_max_f32_e32 v78, v78, v78
	v_max_f32_e32 v72, v72, v78
	v_mov_b32_e32 v78, v73
	s_waitcnt lgkmcnt(0)
	v_max_f32_e32 v78, v78, v78
	v_max_f32_e32 v73, v73, v78
	v_mov_b32_e32 v78, v74
	s_waitcnt lgkmcnt(0)
	v_max_f32_e32 v78, v78, v78
	v_max_f32_e32 v74, v74, v78
	v_mov_b32_e32 v78, v75
	s_waitcnt lgkmcnt(0)
	v_max_f32_e32 v78, v78, v78
	v_max_f32_e32 v75, v75, v78
	v_mov_b32_e32 v78, v76
	s_waitcnt lgkmcnt(0)
	v_max_f32_e32 v78, v78, v78
	v_max_f32_e32 v76, v76, v78
	v_mov_b32_e32 v78, v77
	s_waitcnt lgkmcnt(0)
	v_max_f32_e32 v78, v78, v78
	v_max_f32_e32 v77, v77, v78
	v_mov_b32_e32 v78, v8
	s_waitcnt lgkmcnt(0)
	v_max_f32_e32 v78, v78, v78
	v_max_f32_e32 v8, v8, v78
	v_mov_b32_e32 v78, v9
	s_waitcnt lgkmcnt(0)
	v_max_f32_e32 v78, v78, v78
	v_max_f32_e32 v9, v9, v78
	v_mov_b32_e32 v78, v72
	s_waitcnt lgkmcnt(0)
	v_max_f32_e32 v78, v78, v78
	v_max_f32_e32 v72, v72, v78
	v_mov_b32_e32 v78, v73
	s_waitcnt lgkmcnt(0)
	v_max_f32_e32 v78, v78, v78
	v_max_f32_e32 v73, v73, v78
	v_mov_b32_e32 v78, v74
	s_waitcnt lgkmcnt(0)
	v_max_f32_e32 v78, v78, v78
	v_max_f32_e32 v74, v74, v78
	v_mov_b32_e32 v78, v75
	s_waitcnt lgkmcnt(0)
	v_max_f32_e32 v78, v78, v78
	v_max_f32_e32 v78, v75, v78
	v_mov_b32_e32 v75, v76
	v_mov_b32_e32 v68, v77
	s_waitcnt lgkmcnt(0)
	v_max_f32_e32 v75, v75, v75
	s_waitcnt lgkmcnt(0)
	v_max_f32_e32 v68, v68, v68
	v_max_f32_e32 v80, v77, v68
	v_mov_b32_e32 v68, v8
	v_max_f32_e32 v76, v76, v75
	s_waitcnt lgkmcnt(0)
	v_max_f32_e32 v68, v68, v68
	v_max_f32_e32 v82, v8, v68
	v_mov_b32_e32 v8, v9
	v_mov_b32_e32 v83, v82
	s_waitcnt lgkmcnt(0)
	v_max_f32_e32 v8, v8, v8
	v_max_f32_e32 v79, v9, v8
	v_mov_b32_e32 v8, v72
	v_mov_b32_e32 v81, v79
	s_waitcnt lgkmcnt(0)
	v_max_f32_e32 v8, v8, v8
	v_max_f32_e32 v77, v72, v8
	v_mov_b32_e32 v8, v73
	s_waitcnt lgkmcnt(0)
	v_max_f32_e32 v8, v8, v8
	v_max_f32_e32 v75, v73, v8
	v_mov_b32_e32 v8, v74
	s_waitcnt lgkmcnt(0)
	v_max_f32_e32 v8, v8, v8
	v_max_f32_e32 v74, v74, v8
	v_mov_b32_e32 v8, v78
	s_waitcnt lgkmcnt(0)
	v_max_f32_e32 v8, v8, v8
	v_max_f32_e32 v72, v78, v8
	v_mov_b32_e32 v8, v76
	v_mov_b32_e32 v78, v75
	v_mov_b32_e32 v73, v72
	s_waitcnt lgkmcnt(0)
	v_max_f32_e32 v8, v8, v8
	v_max_f32_e32 v68, v76, v8
	v_mov_b32_e32 v8, v80
	v_mov_b32_e32 v76, v74
	v_mov_b32_e32 v67, v68
	s_waitcnt lgkmcnt(0)
	v_max_f32_e32 v8, v8, v8
	v_max_f32_e32 v8, v80, v8
	v_mov_b32_e32 v80, v77
	v_mov_b32_e32 v9, v8
	v_max3_f32 v66, v82, v83, s72
	s_and_saveexec_b64 s[12:13], s[6:7]
	s_cbranch_execz .LBB0_506
	s_lshl_b64 s[4:5], s[10:11], 2
	s_add_u32 s4, s18, s4
	s_addc_u32 s5, s19, s5
	v_mul_f32_e32 v82, 0x3c010204, v66
	global_store_dword v1, v82, s[4:5]

.LBB0_546:
	s_mul_i32 s5, s30, 0x2080
	s_mul_i32 s4, s31, 0x2080
	v_add_u32_e32 v223, s5, v222
	v_add_u32_e32 v232, s4, v222
	ds_read_u16 v154, v223
	ds_read_u16 v155, v232
	s_add_i32 s30, s30, 2
	s_add_i32 s31, s31, 2
	s_add_i32 s33, s33, -2
	s_waitcnt lgkmcnt(0)
	v_lshlrev_b32_e32 v194, 16, v154
	v_lshlrev_b32_e32 v195, 16, v155
	ds_read_u16 v154, v223 offset:1040
	ds_read_u16 v155, v232 offset:1040
	v_pk_fma_f32 v[194:195], v[42:43], v[194:195], v[152:153]
	s_cmp_lg_u32 s33, 0
	s_waitcnt lgkmcnt(1)
	v_lshlrev_b32_e32 v196, 16, v154
	s_waitcnt lgkmcnt(0)
	v_lshlrev_b32_e32 v197, 16, v155
	ds_read_u16 v154, v223 offset:2080
	ds_read_u16 v155, v232 offset:2080
	v_pk_fma_f32 v[194:195], v[44:45], v[196:197], v[194:195]
	v_pk_fma_f32 v[196:197], v[42:43], v[196:197], v[152:153]
	s_waitcnt lgkmcnt(1)
	v_lshlrev_b32_e32 v224, 16, v154
	s_waitcnt lgkmcnt(0)
	v_lshlrev_b32_e32 v225, 16, v155
	ds_read_u16 v154, v223 offset:3120
	ds_read_u16 v155, v232 offset:3120
	v_pk_fma_f32 v[194:195], v[46:47], v[224:225], v[194:195]
	v_pk_fma_f32 v[196:197], v[44:45], v[224:225], v[196:197]
	v_pk_fma_f32 v[224:225], v[42:43], v[224:225], v[152:153]
	s_waitcnt lgkmcnt(1)
	v_lshlrev_b32_e32 v226, 16, v154
	s_waitcnt lgkmcnt(0)
	v_lshlrev_b32_e32 v227, 16, v155
	ds_read_u16 v154, v223 offset:4160
	ds_read_u16 v155, v232 offset:4160
	v_pk_fma_f32 v[194:195], v[48:49], v[226:227], v[194:195]
	v_pk_fma_f32 v[196:197], v[46:47], v[226:227], v[196:197]
	v_pk_fma_f32 v[224:225], v[44:45], v[226:227], v[224:225]
	s_waitcnt lgkmcnt(1)
	v_lshlrev_b32_e32 v218, 16, v154
	s_waitcnt lgkmcnt(0)
	v_lshlrev_b32_e32 v219, 16, v155
	ds_read_u16 v154, v223 offset:5200
	ds_read_u16 v155, v232 offset:5200
	v_pk_fma_f32 v[226:227], v[42:43], v[226:227], v[152:153]
	v_pk_fma_f32 v[194:195], v[50:51], v[218:219], v[194:195]
	v_pk_fma_f32 v[196:197], v[48:49], v[218:219], v[196:197]
	s_waitcnt lgkmcnt(1)
	v_lshlrev_b32_e32 v198, 16, v154
	s_waitcnt lgkmcnt(0)
	v_lshlrev_b32_e32 v199, 16, v155
	ds_read_u16 v154, v223 offset:6240
	ds_read_u16 v155, v232 offset:6240
	v_pk_fma_f32 v[224:225], v[46:47], v[218:219], v[224:225]
	v_pk_fma_f32 v[226:227], v[44:45], v[218:219], v[226:227]
	v_pk_fma_f32 v[218:219], v[42:43], v[218:219], v[152:153]
	s_waitcnt lgkmcnt(1)
	v_lshlrev_b32_e32 v174, 16, v154
	s_waitcnt lgkmcnt(0)
	v_lshlrev_b32_e32 v175, 16, v155
	ds_read_u16 v154, v223 offset:7280
	ds_read_u16 v155, v232 offset:7280
	ds_read_u16 v156, v223 offset:8320
	ds_read_u16 v157, v232 offset:8320
	ds_read_u16 v158, v223 offset:9360
	ds_read_u16 v159, v232 offset:9360
	ds_read_u16 v160, v223 offset:10400
	ds_read_u16 v161, v232 offset:10400
	ds_read_u16 v162, v223 offset:11440
	ds_read_u16 v163, v232 offset:11440
	v_pk_fma_f32 v[194:195], v[52:53], v[198:199], v[194:195]
	v_pk_fma_f32 v[196:197], v[50:51], v[198:199], v[196:197]
	v_pk_fma_f32 v[224:225], v[48:49], v[198:199], v[224:225]
	v_pk_fma_f32 v[226:227], v[46:47], v[198:199], v[226:227]
	v_pk_fma_f32 v[218:219], v[44:45], v[198:199], v[218:219]
	v_pk_fma_f32 v[198:199], v[42:43], v[198:199], v[152:153]
	s_waitcnt lgkmcnt(8)
	v_lshlrev_b32_e32 v155, 16, v155
	v_lshlrev_b32_e32 v154, 16, v154
	ds_read_u16 v164, v223 offset:12480
	ds_read_u16 v165, v232 offset:12480
	v_pk_fma_f32 v[194:195], v[54:55], v[174:175], v[194:195]
	v_pk_fma_f32 v[196:197], v[52:53], v[174:175], v[196:197]
	v_pk_fma_f32 v[224:225], v[50:51], v[174:175], v[224:225]
	v_pk_fma_f32 v[226:227], v[48:49], v[174:175], v[226:227]
	v_pk_fma_f32 v[218:219], v[46:47], v[174:175], v[218:219]
	v_pk_fma_f32 v[198:199], v[44:45], v[174:175], v[198:199]
	v_pk_fma_f32 v[174:175], v[42:43], v[174:175], v[152:153]
	s_waitcnt lgkmcnt(8)
	v_lshlrev_b32_e32 v157, 16, v157
	v_lshlrev_b32_e32 v156, 16, v156
	ds_read_u16 v166, v223 offset:13520
	ds_read_u16 v167, v232 offset:13520
	v_pk_fma_f32 v[194:195], v[56:57], v[154:155], v[194:195]
	v_pk_fma_f32 v[196:197], v[54:55], v[154:155], v[196:197]
	v_pk_fma_f32 v[224:225], v[52:53], v[154:155], v[224:225]
	v_pk_fma_f32 v[226:227], v[50:51], v[154:155], v[226:227]
	v_pk_fma_f32 v[218:219], v[48:49], v[154:155], v[218:219]
	v_pk_fma_f32 v[198:199], v[46:47], v[154:155], v[198:199]
	v_pk_fma_f32 v[174:175], v[44:45], v[154:155], v[174:175]
	v_pk_fma_f32 v[154:155], v[42:43], v[154:155], v[152:153]
	s_waitcnt lgkmcnt(8)
	v_lshlrev_b32_e32 v159, 16, v159
	v_lshlrev_b32_e32 v158, 16, v158
	ds_read_u16 v168, v223 offset:14560
	ds_read_u16 v169, v232 offset:14560
	v_pk_fma_f32 v[154:155], v[44:45], v[156:157], v[154:155]
	s_waitcnt lgkmcnt(8)
	v_lshlrev_b32_e32 v161, 16, v161
	v_lshlrev_b32_e32 v160, 16, v160
	ds_read_u16 v170, v223 offset:15600
	ds_read_u16 v171, v232 offset:15600
	v_pk_fma_f32 v[194:195], v[58:59], v[156:157], v[194:195]
	v_pk_fma_f32 v[196:197], v[56:57], v[156:157], v[196:197]
	v_pk_fma_f32 v[224:225], v[54:55], v[156:157], v[224:225]
	v_pk_fma_f32 v[226:227], v[52:53], v[156:157], v[226:227]
	v_pk_fma_f32 v[218:219], v[50:51], v[156:157], v[218:219]
	v_pk_fma_f32 v[198:199], v[48:49], v[156:157], v[198:199]
	v_pk_fma_f32 v[174:175], v[46:47], v[156:157], v[174:175]
	v_pk_fma_f32 v[154:155], v[46:47], v[158:159], v[154:155]
	s_waitcnt lgkmcnt(8)
	v_lshlrev_b32_e32 v163, 16, v163
	v_lshlrev_b32_e32 v162, 16, v162
	ds_read_u16 v172, v223 offset:16640
	ds_read_u16 v173, v232 offset:16640
	v_pk_fma_f32 v[194:195], v[60:61], v[158:159], v[194:195]
	v_pk_fma_f32 v[196:197], v[58:59], v[158:159], v[196:197]
	v_pk_fma_f32 v[224:225], v[56:57], v[158:159], v[224:225]
	v_pk_fma_f32 v[226:227], v[54:55], v[158:159], v[226:227]
	v_pk_fma_f32 v[218:219], v[52:53], v[158:159], v[218:219]
	v_pk_fma_f32 v[198:199], v[50:51], v[158:159], v[198:199]
	v_pk_fma_f32 v[174:175], v[48:49], v[158:159], v[174:175]
	v_pk_fma_f32 v[154:155], v[48:49], v[160:161], v[154:155]
	s_waitcnt lgkmcnt(8)
	v_lshlrev_b32_e32 v165, 16, v165
	v_lshlrev_b32_e32 v164, 16, v164
	ds_read_u16 v176, v223 offset:17680
	ds_read_u16 v177, v232 offset:17680
	v_pk_fma_f32 v[194:195], v[62:63], v[160:161], v[194:195]
	v_pk_fma_f32 v[196:197], v[60:61], v[160:161], v[196:197]
	v_pk_fma_f32 v[224:225], v[58:59], v[160:161], v[224:225]
	v_pk_fma_f32 v[226:227], v[56:57], v[160:161], v[226:227]
	v_pk_fma_f32 v[218:219], v[54:55], v[160:161], v[218:219]
	v_pk_fma_f32 v[198:199], v[52:53], v[160:161], v[198:199]
	v_pk_fma_f32 v[174:175], v[50:51], v[160:161], v[174:175]
	v_pk_fma_f32 v[154:155], v[50:51], v[162:163], v[154:155]
	s_waitcnt lgkmcnt(8)
	v_lshlrev_b32_e32 v167, 16, v167
	v_lshlrev_b32_e32 v166, 16, v166
	ds_read_u16 v178, v223 offset:18720
	ds_read_u16 v179, v232 offset:18720
	v_pk_fma_f32 v[194:195], v[64:65], v[162:163], v[194:195]
	v_pk_fma_f32 v[196:197], v[62:63], v[162:163], v[196:197]
	v_pk_fma_f32 v[224:225], v[60:61], v[162:163], v[224:225]
	v_pk_fma_f32 v[226:227], v[58:59], v[162:163], v[226:227]
	v_pk_fma_f32 v[218:219], v[56:57], v[162:163], v[218:219]
	v_pk_fma_f32 v[198:199], v[54:55], v[162:163], v[198:199]
	v_pk_fma_f32 v[174:175], v[52:53], v[162:163], v[174:175]
	v_pk_fma_f32 v[154:155], v[52:53], v[164:165], v[154:155]
	s_waitcnt lgkmcnt(8)
	v_lshlrev_b32_e32 v169, 16, v169
	v_lshlrev_b32_e32 v168, 16, v168
	ds_read_u16 v180, v223 offset:19760
	ds_read_u16 v181, v232 offset:19760
	v_pk_fma_f32 v[194:195], v[114:115], v[164:165], v[194:195]
	v_pk_fma_f32 v[196:197], v[64:65], v[164:165], v[196:197]
	v_pk_fma_f32 v[224:225], v[62:63], v[164:165], v[224:225]
	v_pk_fma_f32 v[226:227], v[60:61], v[164:165], v[226:227]
	v_pk_fma_f32 v[218:219], v[58:59], v[164:165], v[218:219]
	v_pk_fma_f32 v[198:199], v[56:57], v[164:165], v[198:199]
	v_pk_fma_f32 v[174:175], v[54:55], v[164:165], v[174:175]
	v_pk_fma_f32 v[154:155], v[54:55], v[166:167], v[154:155]
	s_waitcnt lgkmcnt(8)
	v_lshlrev_b32_e32 v171, 16, v171
	v_lshlrev_b32_e32 v170, 16, v170
	ds_read_u16 v182, v223 offset:20800
	ds_read_u16 v183, v232 offset:20800
	v_pk_fma_f32 v[194:195], v[116:117], v[166:167], v[194:195]
	v_pk_fma_f32 v[196:197], v[114:115], v[166:167], v[196:197]
	v_pk_fma_f32 v[224:225], v[64:65], v[166:167], v[224:225]
	v_pk_fma_f32 v[226:227], v[62:63], v[166:167], v[226:227]
	v_pk_fma_f32 v[218:219], v[60:61], v[166:167], v[218:219]
	v_pk_fma_f32 v[198:199], v[58:59], v[166:167], v[198:199]
	v_pk_fma_f32 v[174:175], v[56:57], v[166:167], v[174:175]
	v_pk_fma_f32 v[154:155], v[56:57], v[168:169], v[154:155]
	s_waitcnt lgkmcnt(8)
	v_lshlrev_b32_e32 v173, 16, v173
	v_lshlrev_b32_e32 v172, 16, v172
	ds_read_u16 v184, v223 offset:21840
	ds_read_u16 v185, v232 offset:21840
	v_pk_fma_f32 v[194:195], v[118:119], v[168:169], v[194:195]
	v_pk_fma_f32 v[196:197], v[116:117], v[168:169], v[196:197]
	v_pk_fma_f32 v[224:225], v[114:115], v[168:169], v[224:225]
	v_pk_fma_f32 v[226:227], v[64:65], v[168:169], v[226:227]
	v_pk_fma_f32 v[218:219], v[62:63], v[168:169], v[218:219]
	v_pk_fma_f32 v[198:199], v[60:61], v[168:169], v[198:199]
	v_pk_fma_f32 v[174:175], v[58:59], v[168:169], v[174:175]
	v_pk_fma_f32 v[154:155], v[58:59], v[170:171], v[154:155]
	s_waitcnt lgkmcnt(8)
	v_lshlrev_b32_e32 v177, 16, v177
	v_lshlrev_b32_e32 v176, 16, v176
	ds_read_u16 v186, v223 offset:22880
	ds_read_u16 v187, v232 offset:22880
	v_pk_fma_f32 v[194:195], v[120:121], v[170:171], v[194:195]
	v_pk_fma_f32 v[196:197], v[118:119], v[170:171], v[196:197]
	v_pk_fma_f32 v[224:225], v[116:117], v[170:171], v[224:225]
	v_pk_fma_f32 v[226:227], v[114:115], v[170:171], v[226:227]
	v_pk_fma_f32 v[218:219], v[64:65], v[170:171], v[218:219]
	v_pk_fma_f32 v[198:199], v[62:63], v[170:171], v[198:199]
	v_pk_fma_f32 v[174:175], v[60:61], v[170:171], v[174:175]
	v_pk_fma_f32 v[154:155], v[60:61], v[172:173], v[154:155]
	s_waitcnt lgkmcnt(8)
	v_lshlrev_b32_e32 v179, 16, v179
	v_lshlrev_b32_e32 v178, 16, v178
	ds_read_u16 v188, v223 offset:23920
	ds_read_u16 v189, v232 offset:23920
	v_pk_fma_f32 v[194:195], v[122:123], v[172:173], v[194:195]
	v_pk_fma_f32 v[196:197], v[120:121], v[172:173], v[196:197]
	v_pk_fma_f32 v[224:225], v[118:119], v[172:173], v[224:225]
	v_pk_fma_f32 v[226:227], v[116:117], v[172:173], v[226:227]
	v_pk_fma_f32 v[218:219], v[114:115], v[172:173], v[218:219]
	v_pk_fma_f32 v[198:199], v[64:65], v[172:173], v[198:199]
	v_pk_fma_f32 v[174:175], v[62:63], v[172:173], v[174:175]
	v_pk_fma_f32 v[154:155], v[62:63], v[176:177], v[154:155]
	s_waitcnt lgkmcnt(8)
	v_lshlrev_b32_e32 v181, 16, v181
	v_lshlrev_b32_e32 v180, 16, v180
	ds_read_u16 v190, v223 offset:24960
	ds_read_u16 v191, v232 offset:24960
	v_pk_fma_f32 v[194:195], v[124:125], v[176:177], v[194:195]
	v_pk_fma_f32 v[196:197], v[122:123], v[176:177], v[196:197]
	v_pk_fma_f32 v[224:225], v[120:121], v[176:177], v[224:225]
	v_pk_fma_f32 v[226:227], v[118:119], v[176:177], v[226:227]
	v_pk_fma_f32 v[218:219], v[116:117], v[176:177], v[218:219]
	v_pk_fma_f32 v[198:199], v[114:115], v[176:177], v[198:199]
	v_pk_fma_f32 v[174:175], v[64:65], v[176:177], v[174:175]
	v_pk_fma_f32 v[154:155], v[64:65], v[178:179], v[154:155]
	s_waitcnt lgkmcnt(8)
	v_lshlrev_b32_e32 v183, 16, v183
	v_lshlrev_b32_e32 v182, 16, v182
	ds_read_u16 v192, v223 offset:26000
	ds_read_u16 v193, v232 offset:26000
	v_pk_fma_f32 v[194:195], v[126:127], v[178:179], v[194:195]
	v_pk_fma_f32 v[196:197], v[124:125], v[178:179], v[196:197]
	v_pk_fma_f32 v[224:225], v[122:123], v[178:179], v[224:225]
	v_pk_fma_f32 v[226:227], v[120:121], v[178:179], v[226:227]
	v_pk_fma_f32 v[218:219], v[118:119], v[178:179], v[218:219]
	v_pk_fma_f32 v[198:199], v[116:117], v[178:179], v[198:199]
	v_pk_fma_f32 v[174:175], v[114:115], v[178:179], v[174:175]
	v_pk_fma_f32 v[154:155], v[114:115], v[180:181], v[154:155]
	s_waitcnt lgkmcnt(8)
	v_lshlrev_b32_e32 v185, 16, v185
	v_lshlrev_b32_e32 v184, 16, v184
	ds_read_u16 v200, v223 offset:27040
	ds_read_u16 v201, v232 offset:27040
	v_pk_fma_f32 v[194:195], v[128:129], v[180:181], v[194:195]
	v_pk_fma_f32 v[196:197], v[126:127], v[180:181], v[196:197]
	v_pk_fma_f32 v[224:225], v[124:125], v[180:181], v[224:225]
	v_pk_fma_f32 v[226:227], v[122:123], v[180:181], v[226:227]
	v_pk_fma_f32 v[218:219], v[120:121], v[180:181], v[218:219]
	v_pk_fma_f32 v[198:199], v[118:119], v[180:181], v[198:199]
	v_pk_fma_f32 v[174:175], v[116:117], v[180:181], v[174:175]
	v_pk_fma_f32 v[154:155], v[116:117], v[182:183], v[154:155]
	s_waitcnt lgkmcnt(8)
	v_lshlrev_b32_e32 v187, 16, v187
	v_lshlrev_b32_e32 v186, 16, v186
	ds_read_u16 v202, v223 offset:28080
	ds_read_u16 v203, v232 offset:28080
	v_pk_fma_f32 v[194:195], v[130:131], v[182:183], v[194:195]
	v_pk_fma_f32 v[196:197], v[128:129], v[182:183], v[196:197]
	v_pk_fma_f32 v[224:225], v[126:127], v[182:183], v[224:225]
	v_pk_fma_f32 v[226:227], v[124:125], v[182:183], v[226:227]
	v_pk_fma_f32 v[218:219], v[122:123], v[182:183], v[218:219]
	v_pk_fma_f32 v[198:199], v[120:121], v[182:183], v[198:199]
	v_pk_fma_f32 v[174:175], v[118:119], v[182:183], v[174:175]
	v_pk_fma_f32 v[154:155], v[118:119], v[184:185], v[154:155]
	s_waitcnt lgkmcnt(8)
	v_lshlrev_b32_e32 v189, 16, v189
	v_lshlrev_b32_e32 v188, 16, v188
	ds_read_u16 v204, v223 offset:29120
	ds_read_u16 v205, v232 offset:29120
	v_pk_fma_f32 v[194:195], v[132:133], v[184:185], v[194:195]
	v_pk_fma_f32 v[196:197], v[130:131], v[184:185], v[196:197]
	v_pk_fma_f32 v[224:225], v[128:129], v[184:185], v[224:225]
	v_pk_fma_f32 v[226:227], v[126:127], v[184:185], v[226:227]
	v_pk_fma_f32 v[218:219], v[124:125], v[184:185], v[218:219]
	v_pk_fma_f32 v[198:199], v[122:123], v[184:185], v[198:199]
	v_pk_fma_f32 v[174:175], v[120:121], v[184:185], v[174:175]
	v_pk_fma_f32 v[154:155], v[120:121], v[186:187], v[154:155]
	s_waitcnt lgkmcnt(8)
	v_lshlrev_b32_e32 v191, 16, v191
	v_lshlrev_b32_e32 v190, 16, v190
	ds_read_u16 v206, v223 offset:30160
	ds_read_u16 v207, v232 offset:30160
	v_pk_fma_f32 v[194:195], v[134:135], v[186:187], v[194:195]
	v_pk_fma_f32 v[196:197], v[132:133], v[186:187], v[196:197]
	v_pk_fma_f32 v[224:225], v[130:131], v[186:187], v[224:225]
	v_pk_fma_f32 v[226:227], v[128:129], v[186:187], v[226:227]
	v_pk_fma_f32 v[218:219], v[126:127], v[186:187], v[218:219]
	v_pk_fma_f32 v[198:199], v[124:125], v[186:187], v[198:199]
	v_pk_fma_f32 v[174:175], v[122:123], v[186:187], v[174:175]
	v_pk_fma_f32 v[154:155], v[122:123], v[188:189], v[154:155]
	s_waitcnt lgkmcnt(8)
	v_lshlrev_b32_e32 v193, 16, v193
	v_lshlrev_b32_e32 v192, 16, v192
	ds_read_u16 v208, v223 offset:31200
	ds_read_u16 v209, v232 offset:31200
	v_pk_fma_f32 v[194:195], v[136:137], v[188:189], v[194:195]
	v_pk_fma_f32 v[196:197], v[134:135], v[188:189], v[196:197]
	v_pk_fma_f32 v[224:225], v[132:133], v[188:189], v[224:225]
	v_pk_fma_f32 v[226:227], v[130:131], v[188:189], v[226:227]
	v_pk_fma_f32 v[218:219], v[128:129], v[188:189], v[218:219]
	v_pk_fma_f32 v[198:199], v[126:127], v[188:189], v[198:199]
	v_pk_fma_f32 v[174:175], v[124:125], v[188:189], v[174:175]
	v_pk_fma_f32 v[154:155], v[124:125], v[190:191], v[154:155]
	s_waitcnt lgkmcnt(8)
	v_lshlrev_b32_e32 v201, 16, v201
	v_lshlrev_b32_e32 v200, 16, v200
	ds_read_u16 v210, v223 offset:32240
	ds_read_u16 v211, v232 offset:32240
	v_pk_fma_f32 v[194:195], v[138:139], v[190:191], v[194:195]
	v_pk_fma_f32 v[196:197], v[136:137], v[190:191], v[196:197]
	v_pk_fma_f32 v[224:225], v[134:135], v[190:191], v[224:225]
	v_pk_fma_f32 v[226:227], v[132:133], v[190:191], v[226:227]
	v_pk_fma_f32 v[218:219], v[130:131], v[190:191], v[218:219]
	v_pk_fma_f32 v[198:199], v[128:129], v[190:191], v[198:199]
	v_pk_fma_f32 v[174:175], v[126:127], v[190:191], v[174:175]
	v_pk_fma_f32 v[154:155], v[126:127], v[192:193], v[154:155]
	s_waitcnt lgkmcnt(8)
	v_lshlrev_b32_e32 v203, 16, v203
	v_lshlrev_b32_e32 v202, 16, v202
	ds_read_u16 v212, v223 offset:33280
	ds_read_u16 v213, v232 offset:33280
	v_pk_fma_f32 v[194:195], v[140:141], v[192:193], v[194:195]
	v_pk_fma_f32 v[196:197], v[138:139], v[192:193], v[196:197]
	v_pk_fma_f32 v[224:225], v[136:137], v[192:193], v[224:225]
	v_pk_fma_f32 v[226:227], v[134:135], v[192:193], v[226:227]
	v_pk_fma_f32 v[218:219], v[132:133], v[192:193], v[218:219]
	v_pk_fma_f32 v[198:199], v[130:131], v[192:193], v[198:199]
	v_pk_fma_f32 v[174:175], v[128:129], v[192:193], v[174:175]
	v_pk_fma_f32 v[154:155], v[128:129], v[200:201], v[154:155]
	s_waitcnt lgkmcnt(8)
	v_lshlrev_b32_e32 v205, 16, v205
	v_lshlrev_b32_e32 v204, 16, v204
	ds_read_u16 v214, v223 offset:34320
	ds_read_u16 v215, v232 offset:34320
	v_pk_fma_f32 v[194:195], v[142:143], v[200:201], v[194:195]
	v_pk_fma_f32 v[196:197], v[140:141], v[200:201], v[196:197]
	v_pk_fma_f32 v[224:225], v[138:139], v[200:201], v[224:225]
	v_pk_fma_f32 v[226:227], v[136:137], v[200:201], v[226:227]
	v_pk_fma_f32 v[218:219], v[134:135], v[200:201], v[218:219]
	v_pk_fma_f32 v[198:199], v[132:133], v[200:201], v[198:199]
	v_pk_fma_f32 v[174:175], v[130:131], v[200:201], v[174:175]
	v_pk_fma_f32 v[154:155], v[130:131], v[202:203], v[154:155]
	s_waitcnt lgkmcnt(8)
	v_lshlrev_b32_e32 v207, 16, v207
	v_lshlrev_b32_e32 v206, 16, v206
	ds_read_u16 v216, v223 offset:35360
	ds_read_u16 v217, v232 offset:35360
	v_pk_fma_f32 v[194:195], v[144:145], v[202:203], v[194:195]
	v_pk_fma_f32 v[196:197], v[142:143], v[202:203], v[196:197]
	v_pk_fma_f32 v[224:225], v[140:141], v[202:203], v[224:225]
	v_pk_fma_f32 v[226:227], v[138:139], v[202:203], v[226:227]
	v_pk_fma_f32 v[218:219], v[136:137], v[202:203], v[218:219]
	v_pk_fma_f32 v[198:199], v[134:135], v[202:203], v[198:199]
	v_pk_fma_f32 v[174:175], v[132:133], v[202:203], v[174:175]
	v_pk_fma_f32 v[154:155], v[132:133], v[204:205], v[154:155]
	s_waitcnt lgkmcnt(8)
	v_lshlrev_b32_e32 v209, 16, v209
	v_lshlrev_b32_e32 v208, 16, v208
	ds_read_u16 v220, v223 offset:36400
	ds_read_u16 v221, v232 offset:36400
	v_pk_fma_f32 v[194:195], v[146:147], v[204:205], v[194:195]
	v_pk_fma_f32 v[196:197], v[144:145], v[204:205], v[196:197]
	v_pk_fma_f32 v[224:225], v[142:143], v[204:205], v[224:225]
	v_pk_fma_f32 v[226:227], v[140:141], v[204:205], v[226:227]
	v_pk_fma_f32 v[218:219], v[138:139], v[204:205], v[218:219]
	v_pk_fma_f32 v[198:199], v[136:137], v[204:205], v[198:199]
	v_pk_fma_f32 v[174:175], v[134:135], v[204:205], v[174:175]
	v_pk_fma_f32 v[154:155], v[134:135], v[206:207], v[154:155]
	s_waitcnt lgkmcnt(8)
	v_lshlrev_b32_e32 v211, 16, v211
	v_lshlrev_b32_e32 v210, 16, v210
	ds_read_u16 v228, v223 offset:37440
	ds_read_u16 v229, v232 offset:37440
	v_pk_fma_f32 v[194:195], v[148:149], v[206:207], v[194:195]
	v_pk_fma_f32 v[196:197], v[146:147], v[206:207], v[196:197]
	v_pk_fma_f32 v[224:225], v[144:145], v[206:207], v[224:225]
	v_pk_fma_f32 v[226:227], v[142:143], v[206:207], v[226:227]
	v_pk_fma_f32 v[218:219], v[140:141], v[206:207], v[218:219]
	v_pk_fma_f32 v[198:199], v[138:139], v[206:207], v[198:199]
	v_pk_fma_f32 v[174:175], v[136:137], v[206:207], v[174:175]
	v_pk_fma_f32 v[154:155], v[136:137], v[208:209], v[154:155]
	s_waitcnt lgkmcnt(8)
	v_lshlrev_b32_e32 v213, 16, v213
	v_lshlrev_b32_e32 v212, 16, v212
	ds_read_u16 v230, v223 offset:38480
	ds_read_u16 v231, v232 offset:38480
	v_pk_fma_f32 v[194:195], v[150:151], v[208:209], v[194:195]
	v_pk_fma_f32 v[196:197], v[148:149], v[208:209], v[196:197]
	v_pk_fma_f32 v[224:225], v[146:147], v[208:209], v[224:225]
	v_pk_fma_f32 v[226:227], v[144:145], v[208:209], v[226:227]
	v_pk_fma_f32 v[218:219], v[142:143], v[208:209], v[218:219]
	v_pk_fma_f32 v[198:199], v[140:141], v[208:209], v[198:199]
	v_pk_fma_f32 v[174:175], v[138:139], v[208:209], v[174:175]
	v_pk_fma_f32 v[154:155], v[138:139], v[210:211], v[154:155]
	s_waitcnt lgkmcnt(8)
	v_lshlrev_b32_e32 v215, 16, v215
	v_lshlrev_b32_e32 v214, 16, v214
	v_pk_fma_f32 v[196:197], v[150:151], v[210:211], v[196:197]
	v_pk_fma_f32 v[224:225], v[148:149], v[210:211], v[224:225]
	v_pk_fma_f32 v[226:227], v[146:147], v[210:211], v[226:227]
	v_pk_fma_f32 v[218:219], v[144:145], v[210:211], v[218:219]
	v_pk_fma_f32 v[198:199], v[142:143], v[210:211], v[198:199]
	v_pk_fma_f32 v[174:175], v[140:141], v[210:211], v[174:175]
	v_pk_fma_f32 v[154:155], v[140:141], v[212:213], v[154:155]
	v_cvt_pk_bf16_f32 v156, v194, v195
	s_waitcnt lgkmcnt(6)
	v_lshlrev_b32_e32 v217, 16, v217
	v_lshlrev_b32_e32 v216, 16, v216
	v_pk_fma_f32 v[224:225], v[150:151], v[212:213], v[224:225]
	v_pk_fma_f32 v[226:227], v[148:149], v[212:213], v[226:227]
	v_pk_fma_f32 v[218:219], v[146:147], v[212:213], v[218:219]
	v_pk_fma_f32 v[198:199], v[144:145], v[212:213], v[198:199]
	v_pk_fma_f32 v[174:175], v[142:143], v[212:213], v[174:175]
	v_pk_fma_f32 v[154:155], v[142:143], v[214:215], v[154:155]
	ds_write_b16 v223, v156
	ds_write_b16_d16_hi v232, v156
	v_cvt_pk_bf16_f32 v156, v196, v197
	s_waitcnt lgkmcnt(6)
	v_lshlrev_b32_e32 v221, 16, v221
	v_lshlrev_b32_e32 v220, 16, v220
	v_pk_fma_f32 v[226:227], v[150:151], v[214:215], v[226:227]
	v_pk_fma_f32 v[218:219], v[148:149], v[214:215], v[218:219]
	v_pk_fma_f32 v[198:199], v[146:147], v[214:215], v[198:199]
	v_pk_fma_f32 v[174:175], v[144:145], v[214:215], v[174:175]
	v_pk_fma_f32 v[154:155], v[144:145], v[216:217], v[154:155]
	ds_write_b16 v223, v156 offset:1040
	ds_write_b16_d16_hi v232, v156 offset:1040
	v_cvt_pk_bf16_f32 v156, v224, v225
	s_waitcnt lgkmcnt(6)
	v_lshlrev_b32_e32 v229, 16, v229
	v_lshlrev_b32_e32 v228, 16, v228
	v_pk_fma_f32 v[218:219], v[150:151], v[216:217], v[218:219]
	v_pk_fma_f32 v[198:199], v[148:149], v[216:217], v[198:199]
	v_pk_fma_f32 v[174:175], v[146:147], v[216:217], v[174:175]
	v_pk_fma_f32 v[154:155], v[146:147], v[220:221], v[154:155]
	ds_write_b16 v223, v156 offset:2080
	ds_write_b16_d16_hi v232, v156 offset:2080
	v_cvt_pk_bf16_f32 v156, v226, v227
	s_waitcnt lgkmcnt(6)
	v_lshlrev_b32_e32 v231, 16, v231
	v_lshlrev_b32_e32 v230, 16, v230
	v_pk_fma_f32 v[198:199], v[150:151], v[220:221], v[198:199]
	v_pk_fma_f32 v[174:175], v[148:149], v[220:221], v[174:175]
	v_pk_fma_f32 v[154:155], v[148:149], v[228:229], v[154:155]
	ds_write_b16 v223, v156 offset:3120
	ds_write_b16_d16_hi v232, v156 offset:3120
	v_cvt_pk_bf16_f32 v156, v218, v219
	v_pk_fma_f32 v[174:175], v[150:151], v[228:229], v[174:175]
	v_pk_fma_f32 v[154:155], v[150:151], v[230:231], v[154:155]
	ds_write_b16 v223, v156 offset:4160
	ds_write_b16_d16_hi v232, v156 offset:4160
	v_cvt_pk_bf16_f32 v156, v198, v199
	ds_write_b16 v223, v156 offset:5200
	ds_write_b16_d16_hi v232, v156 offset:5200
	v_cvt_pk_bf16_f32 v156, v174, v175
	v_cvt_pk_bf16_f32 v154, v154, v155
	ds_write_b16 v223, v156 offset:6240
	ds_write_b16_d16_hi v232, v156 offset:6240
	ds_write_b16 v223, v154 offset:7280
	ds_write_b16_d16_hi v232, v154 offset:7280
	s_cbranch_scc1 .LBB0_546
	s_lshl_b64 s[38:39], s[52:53], 2
	s_add_u32 s4, s26, s38
	v_and_b32_e32 v52, 63, v0
	s_addc_u32 s5, s27, s39
	v_ashrrev_i32_e32 v50, 6, v0
	v_lshlrev_b32_e32 v0, 5, v52
	s_waitcnt lgkmcnt(0)
	s_barrier
	global_load_dwordx4 v[42:45], v0, s[4:5] offset:16
	global_load_dwordx4 v[46:49], v0, s[4:5]
	v_lshlrev_b32_e32 v0, 4, v52
	v_mul_lo_u32 v51, v50, s44
	v_add3_u32 v0, 0, v0, v51
	ds_read_b128 v[60:63], v0
	ds_read_b128 v[138:141], v0 offset:24960
	ds_read_b128 v[142:145], v0 offset:33280
	ds_read_b128 v[170:173], v0 offset:58240
	ds_read_b128 v[118:121], v0 offset:8320
	s_add_u32 s30, s28, 0x27c40000
	s_waitcnt lgkmcnt(3)
	v_lshlrev_b32_e32 v132, 16, v138
	v_and_b32_e32 v130, 0xffff0000, v138
	v_lshlrev_b32_e32 v134, 16, v139
	v_and_b32_e32 v133, 0xffff0000, v139
	v_lshlrev_b32_e32 v136, 16, v140
	v_and_b32_e32 v135, 0xffff0000, v140
	v_lshlrev_b32_e32 v139, 16, v141
	v_and_b32_e32 v137, 0xffff0000, v141
	s_waitcnt lgkmcnt(2)
	v_lshlrev_b32_e32 v141, 16, v142
	v_and_b32_e32 v138, 0xffff0000, v142
	v_lshlrev_b32_e32 v142, 16, v143
	v_and_b32_e32 v140, 0xffff0000, v143
	v_lshlrev_b32_e32 v150, 16, v144
	v_and_b32_e32 v143, 0xffff0000, v144
	v_lshlrev_b32_e32 v161, 16, v145
	v_and_b32_e32 v151, 0xffff0000, v145
	ds_read_b128 v[144:147], v0 offset:41600
	v_and_b32_e32 v53, 0xffff0000, v60
	v_and_b32_e32 v54, 0xffff0000, v61
	v_lshlrev_b32_e32 v55, 16, v60
	v_mul_f32_e32 v51, v53, v53
	v_lshlrev_b32_e32 v56, 16, v61
	v_mul_f32_e32 v57, v54, v54
	v_fmac_f32_e32 v51, v55, v55
	v_fmac_f32_e32 v57, v56, v56
	v_add_f32_e32 v51, v57, v51
	v_and_b32_e32 v57, 0xffff0000, v62
	v_lshlrev_b32_e32 v58, 16, v62
	v_mul_f32_e32 v59, v57, v57
	v_fmac_f32_e32 v59, v58, v58
	v_add_f32_e32 v51, v59, v51
	v_and_b32_e32 v59, 0xffff0000, v63
	v_lshlrev_b32_e32 v61, 16, v63
	v_mul_f32_e32 v60, v59, v59
	v_fmac_f32_e32 v60, v61, v61
	v_add_f32_e32 v116, v60, v51
	s_waitcnt lgkmcnt(0)
	v_lshlrev_b32_e32 v162, 16, v144
	v_and_b32_e32 v152, 0xffff0000, v144
	v_lshlrev_b32_e32 v164, 16, v145
	v_and_b32_e32 v163, 0xffff0000, v145
	v_lshlrev_b32_e32 v166, 16, v146
	v_and_b32_e32 v165, 0xffff0000, v146
	v_lshlrev_b32_e32 v168, 16, v147
	v_and_b32_e32 v167, 0xffff0000, v147
	ds_read_b128 v[144:147], v0 offset:49920
	v_and_b32_e32 v60, 0xffff0000, v118
	v_and_b32_e32 v63, 0xffff0000, v119
	v_lshlrev_b32_e32 v62, 16, v118
	v_mul_f32_e32 v51, v60, v60
	v_lshlrev_b32_e32 v64, 16, v119
	v_mul_f32_e32 v65, v63, v63
	v_fmac_f32_e32 v51, v62, v62
	v_fmac_f32_e32 v65, v64, v64
	v_add_f32_e32 v51, v65, v51
	v_and_b32_e32 v65, 0xffff0000, v120
	v_lshlrev_b32_e32 v114, 16, v120
	v_mul_f32_e32 v115, v65, v65
	v_fmac_f32_e32 v115, v114, v114
	v_add_f32_e32 v51, v115, v51
	v_lshlrev_b32_e32 v123, 16, v121
	v_and_b32_e32 v115, 0xffff0000, v121
	ds_read_b128 v[118:121], v0 offset:16640
	v_mul_f32_e32 v117, v115, v115
	v_fmac_f32_e32 v117, v123, v123
	v_add_f32_e32 v117, v117, v51
	s_waitcnt lgkmcnt(1)
	v_and_b32_e32 v153, 0xffff0000, v144
	s_waitcnt lgkmcnt(0)
	v_and_b32_e32 v122, 0xffff0000, v118
	v_and_b32_e32 v124, 0xffff0000, v119
	v_lshlrev_b32_e32 v125, 16, v118
	v_mul_f32_e32 v51, v122, v122
	v_lshlrev_b32_e32 v126, 16, v119
	v_mul_f32_e32 v118, v124, v124
	v_fmac_f32_e32 v51, v125, v125
	v_fmac_f32_e32 v118, v126, v126
	v_and_b32_e32 v127, 0xffff0000, v120
	v_add_f32_e32 v51, v118, v51
	v_lshlrev_b32_e32 v128, 16, v120
	v_mul_f32_e32 v118, v127, v127
	v_fmac_f32_e32 v118, v128, v128
	v_and_b32_e32 v129, 0xffff0000, v121
	v_add_f32_e32 v51, v118, v51
	v_lshlrev_b32_e32 v131, 16, v121
	v_mul_f32_e32 v118, v129, v129
	v_fmac_f32_e32 v118, v131, v131
	v_add_f32_e32 v118, v118, v51
	v_mul_f32_e32 v51, v130, v130
	v_mul_f32_e32 v119, v133, v133
	v_fmac_f32_e32 v51, v132, v132
	v_fmac_f32_e32 v119, v134, v134
	v_add_f32_e32 v51, v119, v51
	v_mul_f32_e32 v119, v135, v135
	v_fmac_f32_e32 v119, v136, v136
	v_add_f32_e32 v51, v119, v51
	v_mul_f32_e32 v119, v137, v137
	v_fmac_f32_e32 v119, v139, v139
	v_add_f32_e32 v119, v119, v51
	v_mul_f32_e32 v51, v138, v138
	v_mul_f32_e32 v120, v140, v140
	v_fmac_f32_e32 v51, v141, v141
	v_fmac_f32_e32 v120, v142, v142
	v_add_f32_e32 v51, v120, v51
	v_mul_f32_e32 v120, v143, v143
	v_fmac_f32_e32 v120, v150, v150
	v_add_f32_e32 v51, v120, v51
	v_mul_f32_e32 v120, v151, v151
	v_fmac_f32_e32 v120, v161, v161
	v_add_f32_e32 v120, v120, v51
	v_mul_f32_e32 v51, v152, v152
	v_mul_f32_e32 v121, v163, v163
	v_fmac_f32_e32 v51, v162, v162
	v_fmac_f32_e32 v121, v164, v164
	v_add_f32_e32 v51, v121, v51
	v_mul_f32_e32 v121, v165, v165
	v_fmac_f32_e32 v121, v166, v166
	v_add_f32_e32 v51, v121, v51
	v_mul_f32_e32 v121, v167, v167
	v_fmac_f32_e32 v121, v168, v168
	v_and_b32_e32 v154, 0xffff0000, v145
	v_add_f32_e32 v169, v121, v51
	v_lshlrev_b32_e32 v155, 16, v144
	v_mul_f32_e32 v51, v153, v153
	v_lshlrev_b32_e32 v156, 16, v145
	v_mul_f32_e32 v121, v154, v154
	v_fmac_f32_e32 v51, v155, v155
	v_fmac_f32_e32 v121, v156, v156
	v_and_b32_e32 v157, 0xffff0000, v146
	v_add_f32_e32 v51, v121, v51
	v_lshlrev_b32_e32 v158, 16, v146
	v_mul_f32_e32 v121, v157, v157
	v_fmac_f32_e32 v121, v158, v158
	v_and_b32_e32 v159, 0xffff0000, v147
	v_add_f32_e32 v51, v121, v51
	v_lshlrev_b32_e32 v160, 16, v147
	v_mul_f32_e32 v121, v159, v159
	v_fmac_f32_e32 v121, v160, v160
	v_and_b32_e32 v0, 0xffff0000, v170
	v_and_b32_e32 v144, 0xffff0000, v171
	v_add_f32_e32 v174, v121, v51
	v_lshlrev_b32_e32 v51, 16, v170
	v_mul_f32_e32 v121, v0, v0
	v_lshlrev_b32_e32 v145, 16, v171
	v_mul_f32_e32 v146, v144, v144
	v_fmac_f32_e32 v121, v51, v51
	v_fmac_f32_e32 v146, v145, v145
	v_add_f32_e32 v121, v146, v121
	v_and_b32_e32 v146, 0xffff0000, v172
	v_lshlrev_b32_e32 v147, 16, v172
	v_mul_f32_e32 v148, v146, v146
	v_fmac_f32_e32 v148, v147, v147
	v_add_f32_e32 v121, v148, v121
	v_and_b32_e32 v148, 0xffff0000, v173
	v_lshlrev_b32_e32 v149, 16, v173
	v_mul_f32_e32 v170, v148, v148
	v_fmac_f32_e32 v170, v149, v149
	v_add_f32_e32 v170, v170, v121
	v_and_b32_e32 v121, 64, v234
	v_add_u32_e32 v171, 64, v121
	v_xor_b32_e32 v121, 1, v234
	v_cmp_lt_i32_e32 vcc, v121, v171
	s_addc_u32 s31, s29, 0
	v_cmp_eq_u32_e64 s[26:27], 0, v52
	v_cndmask_b32_e32 v121, v234, v121, vcc
	v_lshlrev_b32_e32 v121, 2, v121
	s_nop 1
	v_add_f32_dpp v116, v116, v116 quad_perm:[1,0,3,2] row_mask:0xf bank_mask:0xf
	s_nop 1
	v_add_f32_dpp v116, v116, v116 quad_perm:[2,3,0,1] row_mask:0xf bank_mask:0xf
	s_nop 1
	v_add_f32_dpp v116, v116, v116 row_half_mirror row_mask:0xf bank_mask:0xf
	s_nop 1
	v_add_f32_dpp v116, v116, v116 row_ror:8 row_mask:0xf bank_mask:0xf
	v_mov_b32_e32 v172, v116
	s_nop 1
	v_permlane16_swap_b32_e32 v116, v172
	s_nop 0
	v_add_f32_e32 v116, v116, v172
	v_mov_b32_e32 v172, v116
	s_nop 1
	v_permlane32_swap_b32_e32 v116, v172
	s_nop 0
	v_add_f32_e32 v116, v116, v172
	v_mov_b32_e32 v172, 0
	s_waitcnt lgkmcnt(0)
	v_add_f32_e32 v116, v116, v172
	s_nop 1
	v_add_f32_dpp v117, v117, v117 quad_perm:[1,0,3,2] row_mask:0xf bank_mask:0xf
	s_nop 1
	v_add_f32_dpp v117, v117, v117 quad_perm:[2,3,0,1] row_mask:0xf bank_mask:0xf
	s_nop 1
	v_add_f32_dpp v117, v117, v117 row_half_mirror row_mask:0xf bank_mask:0xf
	s_nop 1
	v_add_f32_dpp v117, v117, v117 row_ror:8 row_mask:0xf bank_mask:0xf
	v_mov_b32_e32 v172, v117
	s_nop 1
	v_permlane16_swap_b32_e32 v117, v172
	s_nop 0
	v_add_f32_e32 v117, v117, v172
	v_mov_b32_e32 v172, v117
	s_nop 1
	v_permlane32_swap_b32_e32 v117, v172
	s_nop 0
	v_add_f32_e32 v117, v117, v172
	v_mov_b32_e32 v172, 0
	s_waitcnt lgkmcnt(0)
	v_add_f32_e32 v117, v117, v172
	s_nop 1
	v_add_f32_dpp v118, v118, v118 quad_perm:[1,0,3,2] row_mask:0xf bank_mask:0xf
	s_nop 1
	v_add_f32_dpp v118, v118, v118 quad_perm:[2,3,0,1] row_mask:0xf bank_mask:0xf
	s_nop 1
	v_add_f32_dpp v118, v118, v118 row_half_mirror row_mask:0xf bank_mask:0xf
	s_nop 1
	v_add_f32_dpp v118, v118, v118 row_ror:8 row_mask:0xf bank_mask:0xf
	v_mov_b32_e32 v172, v118
	s_nop 1
	v_permlane16_swap_b32_e32 v118, v172
	s_nop 0
	v_add_f32_e32 v118, v118, v172
	v_mov_b32_e32 v172, v118
	s_nop 1
	v_permlane32_swap_b32_e32 v118, v172
	s_nop 0
	v_add_f32_e32 v118, v118, v172
	v_mov_b32_e32 v172, 0
	s_waitcnt lgkmcnt(0)
	v_add_f32_e32 v118, v118, v172
	s_nop 1
	v_add_f32_dpp v119, v119, v119 quad_perm:[1,0,3,2] row_mask:0xf bank_mask:0xf
	s_nop 1
	v_add_f32_dpp v119, v119, v119 quad_perm:[2,3,0,1] row_mask:0xf bank_mask:0xf
	s_nop 1
	v_add_f32_dpp v119, v119, v119 row_half_mirror row_mask:0xf bank_mask:0xf
	s_nop 1
	v_add_f32_dpp v119, v119, v119 row_ror:8 row_mask:0xf bank_mask:0xf
	v_mov_b32_e32 v172, v119
	s_nop 1
	v_permlane16_swap_b32_e32 v119, v172
	s_nop 0
	v_add_f32_e32 v119, v119, v172
	v_mov_b32_e32 v172, v119
	s_nop 1
	v_permlane32_swap_b32_e32 v119, v172
	s_nop 0
	v_add_f32_e32 v119, v119, v172
	v_mov_b32_e32 v172, 0
	s_waitcnt lgkmcnt(0)
	v_add_f32_e32 v119, v119, v172
	s_nop 1
	v_add_f32_dpp v120, v120, v120 quad_perm:[1,0,3,2] row_mask:0xf bank_mask:0xf
	s_nop 1
	v_add_f32_dpp v120, v120, v120 quad_perm:[2,3,0,1] row_mask:0xf bank_mask:0xf
	s_nop 1
	v_add_f32_dpp v120, v120, v120 row_half_mirror row_mask:0xf bank_mask:0xf
	s_nop 1
	v_add_f32_dpp v120, v120, v120 row_ror:8 row_mask:0xf bank_mask:0xf
	v_mov_b32_e32 v172, v120
	s_nop 1
	v_permlane16_swap_b32_e32 v120, v172
	s_nop 0
	v_add_f32_e32 v120, v120, v172
	v_mov_b32_e32 v172, v120
	s_nop 1
	v_permlane32_swap_b32_e32 v120, v172
	s_nop 0
	v_add_f32_e32 v120, v120, v172
	v_mov_b32_e32 v172, 0
	s_waitcnt lgkmcnt(0)
	v_add_f32_e32 v172, v120, v172
	s_nop 1
	v_add_f32_dpp v169, v169, v169 quad_perm:[1,0,3,2] row_mask:0xf bank_mask:0xf
	s_nop 1
	v_add_f32_dpp v169, v169, v169 quad_perm:[2,3,0,1] row_mask:0xf bank_mask:0xf
	s_nop 1
	v_add_f32_dpp v169, v169, v169 row_half_mirror row_mask:0xf bank_mask:0xf
	s_nop 1
	v_add_f32_dpp v169, v169, v169 row_ror:8 row_mask:0xf bank_mask:0xf
	v_mov_b32_e32 v120, v169
	s_nop 1
	v_permlane16_swap_b32_e32 v169, v120
	s_nop 0
	v_add_f32_e32 v169, v169, v120
	v_mov_b32_e32 v120, v169
	s_nop 1
	v_permlane32_swap_b32_e32 v169, v120
	s_nop 0
	v_add_f32_e32 v169, v169, v120
	v_mov_b32_e32 v120, 0
	s_waitcnt lgkmcnt(0)
	v_add_f32_e32 v169, v169, v120
	s_nop 1
	v_add_f32_dpp v174, v174, v174 quad_perm:[1,0,3,2] row_mask:0xf bank_mask:0xf
	s_nop 1
	v_add_f32_dpp v174, v174, v174 quad_perm:[2,3,0,1] row_mask:0xf bank_mask:0xf
	s_nop 1
	v_add_f32_dpp v174, v174, v174 row_half_mirror row_mask:0xf bank_mask:0xf
	s_nop 1
	v_add_f32_dpp v174, v174, v174 row_ror:8 row_mask:0xf bank_mask:0xf
	v_mov_b32_e32 v120, v174
	s_nop 1
	v_permlane16_swap_b32_e32 v174, v120
	s_nop 0
	v_add_f32_e32 v174, v174, v120
	v_mov_b32_e32 v120, v174
	s_nop 1
	v_permlane32_swap_b32_e32 v174, v120
	s_nop 0
	v_add_f32_e32 v174, v174, v120
	v_mov_b32_e32 v120, 0
	s_waitcnt lgkmcnt(0)
	v_add_f32_e32 v173, v174, v120
	s_nop 1
	v_add_f32_dpp v170, v170, v170 quad_perm:[1,0,3,2] row_mask:0xf bank_mask:0xf
	s_nop 1
	v_add_f32_dpp v170, v170, v170 quad_perm:[2,3,0,1] row_mask:0xf bank_mask:0xf
	s_nop 1
	v_add_f32_dpp v170, v170, v170 row_half_mirror row_mask:0xf bank_mask:0xf
	s_nop 1
	v_add_f32_dpp v170, v170, v170 row_ror:8 row_mask:0xf bank_mask:0xf
	v_mov_b32_e32 v120, v170
	s_nop 1
	v_permlane16_swap_b32_e32 v170, v120
	s_nop 0
	v_add_f32_e32 v170, v170, v120
	v_mov_b32_e32 v120, v170
	s_nop 1
	v_permlane32_swap_b32_e32 v170, v120
	s_nop 0
	v_add_f32_e32 v170, v170, v120
	v_mov_b32_e32 v120, 0
	s_waitcnt lgkmcnt(0)
	v_add_f32_e32 v170, v170, v120
	v_xor_b32_e32 v120, 2, v234
	v_cmp_lt_i32_e32 vcc, v120, v171
	s_nop 1
	v_cndmask_b32_e32 v120, v234, v120, vcc
	v_lshlrev_b32_e32 v120, 2, v120
	v_mov_b32_e32 v174, 0
	s_waitcnt lgkmcnt(0)
	v_add_f32_e32 v116, v116, v174
	v_mov_b32_e32 v174, 0
	s_waitcnt lgkmcnt(0)
	v_add_f32_e32 v117, v117, v174
	v_mov_b32_e32 v174, 0
	s_waitcnt lgkmcnt(0)
	v_add_f32_e32 v118, v118, v174
	v_mov_b32_e32 v174, 0
	s_waitcnt lgkmcnt(0)
	v_add_f32_e32 v174, v119, v174
	v_mov_b32_e32 v119, 0
	s_waitcnt lgkmcnt(0)
	v_add_f32_e32 v172, v172, v119
	v_mov_b32_e32 v119, 0
	s_waitcnt lgkmcnt(0)
	v_add_f32_e32 v169, v169, v119
	v_mov_b32_e32 v119, 0
	s_waitcnt lgkmcnt(0)
	v_add_f32_e32 v173, v173, v119
	v_mov_b32_e32 v119, 0
	s_waitcnt lgkmcnt(0)
	v_add_f32_e32 v170, v170, v119
	v_xor_b32_e32 v119, 4, v234
	v_cmp_lt_i32_e32 vcc, v119, v171
	s_nop 1
	v_cndmask_b32_e32 v119, v234, v119, vcc
	v_lshlrev_b32_e32 v119, 2, v119
	v_mov_b32_e32 v175, 0
	s_waitcnt lgkmcnt(0)
	v_add_f32_e32 v116, v116, v175
	v_mov_b32_e32 v175, 0
	s_waitcnt lgkmcnt(0)
	v_add_f32_e32 v117, v117, v175
	v_mov_b32_e32 v175, 0
	s_waitcnt lgkmcnt(0)
	v_add_f32_e32 v175, v118, v175
	v_mov_b32_e32 v118, 0
	s_waitcnt lgkmcnt(0)
	v_add_f32_e32 v174, v174, v118
	v_mov_b32_e32 v118, 0
	s_waitcnt lgkmcnt(0)
	v_add_f32_e32 v172, v172, v118
	v_mov_b32_e32 v118, 0
	s_waitcnt lgkmcnt(0)
	v_add_f32_e32 v169, v169, v118
	v_mov_b32_e32 v118, 0
	s_waitcnt lgkmcnt(0)
	v_add_f32_e32 v173, v173, v118
	v_mov_b32_e32 v118, 0
	s_waitcnt lgkmcnt(0)
	v_add_f32_e32 v170, v170, v118
	v_xor_b32_e32 v118, 8, v234
	v_cmp_lt_i32_e32 vcc, v118, v171
	s_nop 1
	v_cndmask_b32_e32 v118, v234, v118, vcc
	v_lshlrev_b32_e32 v118, 2, v118
	v_mov_b32_e32 v176, 0
	s_waitcnt lgkmcnt(0)
	v_add_f32_e32 v176, v116, v176
	v_mov_b32_e32 v116, 0
	s_waitcnt lgkmcnt(0)
	v_add_f32_e32 v117, v117, v116
	v_mov_b32_e32 v116, 0
	s_waitcnt lgkmcnt(0)
	v_add_f32_e32 v175, v175, v116
	v_mov_b32_e32 v116, 0
	s_waitcnt lgkmcnt(0)
	v_add_f32_e32 v174, v174, v116
	v_mov_b32_e32 v116, 0
	s_waitcnt lgkmcnt(0)
	v_add_f32_e32 v172, v172, v116
	v_mov_b32_e32 v116, 0
	s_waitcnt lgkmcnt(0)
	v_add_f32_e32 v169, v169, v116
	v_mov_b32_e32 v116, 0
	s_waitcnt lgkmcnt(0)
	v_add_f32_e32 v173, v173, v116
	v_mov_b32_e32 v116, 0
	s_waitcnt lgkmcnt(0)
	v_add_f32_e32 v170, v170, v116
	v_xor_b32_e32 v116, 16, v234
	v_cmp_lt_i32_e32 vcc, v116, v171
	s_nop 1
	v_cndmask_b32_e32 v116, v234, v116, vcc
	v_lshlrev_b32_e32 v116, 2, v116
	v_mov_b32_e32 v177, 0
	s_waitcnt lgkmcnt(0)
	v_add_f32_e32 v176, v176, v177
	v_mov_b32_e32 v177, 0
	s_waitcnt lgkmcnt(0)
	v_add_f32_e32 v177, v117, v177
	v_mov_b32_e32 v117, 0
	s_waitcnt lgkmcnt(0)
	v_add_f32_e32 v175, v175, v117
	v_mov_b32_e32 v117, 0
	s_waitcnt lgkmcnt(0)
	v_add_f32_e32 v174, v174, v117
	v_mov_b32_e32 v117, 0
	s_waitcnt lgkmcnt(0)
	v_add_f32_e32 v172, v172, v117
	v_mov_b32_e32 v117, 0
	s_waitcnt lgkmcnt(0)
	v_add_f32_e32 v169, v169, v117
	v_mov_b32_e32 v117, 0
	s_waitcnt lgkmcnt(0)
	v_add_f32_e32 v178, v173, v117
	v_mov_b32_e32 v117, 0
	s_waitcnt lgkmcnt(0)
	v_add_f32_e32 v179, v170, v117
	v_xor_b32_e32 v117, 32, v234
	v_cmp_lt_i32_e32 vcc, v117, v171
	s_nop 1
	v_cndmask_b32_e32 v117, v234, v117, vcc
	v_lshlrev_b32_e32 v117, 2, v117
	v_mov_b32_e32 v170, 0
	s_waitcnt lgkmcnt(0)
	v_add_f32_e32 v176, v176, v170
	v_mov_b32_e32 v170, 0
	s_waitcnt lgkmcnt(0)
	v_add_f32_e32 v177, v177, v170
	v_mov_b32_e32 v170, 0
	s_waitcnt lgkmcnt(0)
	v_add_f32_e32 v175, v175, v170
	v_mov_b32_e32 v170, 0
	s_waitcnt lgkmcnt(0)
	v_add_f32_e32 v173, v174, v170
	v_mov_b32_e32 v170, 0
	v_fmamk_f32 v174, v176, 0x3b000000, v235
	v_rsq_f32_e32 v174, v174
	v_fmamk_f32 v173, v173, 0x3b000000, v235
	v_rsq_f32_e32 v173, v173
	s_waitcnt lgkmcnt(0)
	v_add_f32_e32 v172, v172, v170
	v_mov_b32_e32 v170, 0
	v_mul_f32_e32 v53, v174, v53
	s_waitcnt vmcnt(0)
	v_mul_f32_e32 v176, v47, v53
	v_mul_f32_e32 v53, v174, v56
	v_mul_f32_e32 v56, v48, v53
	s_waitcnt lgkmcnt(0)
	v_add_f32_e32 v171, v169, v170
	v_mov_b32_e32 v169, 0
	v_mul_f32_e32 v53, v174, v54
	v_mul_f32_e32 v55, v174, v55
	v_mul_f32_e32 v55, v46, v55
	v_mul_f32_e32 v54, 0xbfb8aa3b, v176
	s_waitcnt lgkmcnt(0)
	v_add_f32_e32 v170, v178, v169
	v_mov_b32_e32 v169, 0
	v_mul_f32_e32 v178, v49, v53
	v_mul_f32_e32 v53, v174, v58
	v_mul_f32_e32 v58, v42, v53
	v_mul_f32_e32 v53, v174, v57
	s_waitcnt lgkmcnt(0)
	v_add_f32_e32 v169, v179, v169
	v_mul_f32_e32 v179, v43, v53
	v_mul_f32_e32 v53, v174, v61
	v_mul_f32_e32 v61, v44, v53
	v_mul_f32_e32 v53, v174, v59
	v_mul_f32_e32 v174, v45, v53
	v_mul_f32_e32 v53, 0xbfb8aa3b, v55
	v_mul_f32_e32 v59, 0xbfb8aa3b, v61
	v_exp_f32_e32 v53, v53
	v_exp_f32_e32 v59, v59
	v_exp_f32_e32 v54, v54
	v_mul_f32_e32 v130, v173, v130
	v_add_f32_e32 v53, 1.0, v53
	v_add_f32_e32 v59, 1.0, v59
	v_rcp_f32_e32 v53, v53
	v_rcp_f32_e32 v59, v59
	v_add_f32_e32 v54, 1.0, v54
	v_rcp_f32_e32 v54, v54
	v_mul_f32_e32 v53, v55, v53
	v_mul_f32_e32 v55, 0xbfb8aa3b, v56
	v_mul_f32_e32 v59, v61, v59
	v_mul_f32_e32 v61, 0xbfb8aa3b, v174
	v_exp_f32_e32 v55, v55
	v_exp_f32_e32 v61, v61
	v_mul_f32_e32 v54, v176, v54
	v_mul_f32_e32 v132, v173, v132
	v_add_f32_e32 v55, 1.0, v55
	v_add_f32_e32 v61, 1.0, v61
	v_rcp_f32_e32 v55, v55
	v_rcp_f32_e32 v61, v61
	v_mul_f32_e32 v132, v46, v132
	v_fmamk_f32 v172, v172, 0x3b000000, v235
	v_mul_f32_e32 v55, v56, v55
	v_mul_f32_e32 v56, 0xbfb8aa3b, v178
	v_mul_f32_e32 v61, v174, v61
	v_fmamk_f32 v174, v177, 0x3b000000, v235
	v_exp_f32_e32 v56, v56
	v_rsq_f32_e32 v174, v174
	v_rsq_f32_e32 v172, v172
	v_fmamk_f32 v171, v171, 0x3b000000, v235
	v_add_f32_e32 v56, 1.0, v56
	v_mul_f32_e32 v60, v174, v60
	v_rcp_f32_e32 v56, v56
	v_mul_f32_e32 v176, v47, v60
	v_mul_f32_e32 v60, v174, v64
	v_mul_f32_e32 v64, v48, v60
	v_mul_f32_e32 v60, v174, v63
	v_mul_f32_e32 v177, v49, v60
	v_mul_f32_e32 v60, v174, v114
	v_mul_f32_e32 v114, v42, v60
	v_mul_f32_e32 v60, v174, v65
	v_mul_f32_e32 v56, v178, v56
	v_mul_f32_e32 v178, v43, v60
	v_mul_f32_e32 v60, v174, v123
	v_mul_f32_e32 v123, v44, v60
	v_mul_f32_e32 v60, v174, v115
	v_mul_f32_e32 v115, 0xbfb8aa3b, v123
	v_exp_f32_e32 v115, v115
	v_mul_f32_e32 v62, v174, v62
	v_mul_f32_e32 v62, v46, v62
	v_mul_f32_e32 v174, v45, v60
	v_add_f32_e32 v115, 1.0, v115
	v_rcp_f32_e32 v115, v115
	v_mul_f32_e32 v60, 0xbfb8aa3b, v62
	v_exp_f32_e32 v60, v60
	v_mul_f32_e32 v63, 0xbfb8aa3b, v64
	v_mul_f32_e32 v115, v123, v115
	v_mul_f32_e32 v123, 0xbfb8aa3b, v174
	v_exp_f32_e32 v63, v63
	v_exp_f32_e32 v123, v123
	v_add_f32_e32 v60, 1.0, v60
	v_rcp_f32_e32 v60, v60
	v_add_f32_e32 v63, 1.0, v63
	v_add_f32_e32 v123, 1.0, v123
	v_rcp_f32_e32 v63, v63
	v_rcp_f32_e32 v123, v123
	v_mul_f32_e32 v60, v62, v60
	v_mul_f32_e32 v62, 0xbfb8aa3b, v176
	v_exp_f32_e32 v62, v62
	v_mul_f32_e32 v63, v64, v63
	v_mul_f32_e32 v64, 0xbfb8aa3b, v177
	v_mul_f32_e32 v123, v174, v123
	v_fmamk_f32 v174, v175, 0x3b000000, v235
	v_exp_f32_e32 v64, v64
	v_rsq_f32_e32 v174, v174
	v_add_f32_e32 v62, 1.0, v62
	v_rcp_f32_e32 v62, v62
	v_add_f32_e32 v64, 1.0, v64
	v_mul_f32_e32 v122, v174, v122
	v_rcp_f32_e32 v64, v64
	v_mul_f32_e32 v175, v47, v122
	v_mul_f32_e32 v122, v174, v126
	v_mul_f32_e32 v126, v48, v122
	v_mul_f32_e32 v122, v174, v124
	v_mul_f32_e32 v62, v176, v62
	v_mul_f32_e32 v176, v49, v122
	v_mul_f32_e32 v122, v174, v128
	v_mul_f32_e32 v128, v42, v122
	v_mul_f32_e32 v122, v174, v127
	v_mul_f32_e32 v64, v177, v64
	v_mul_f32_e32 v125, v174, v125
	v_mul_f32_e32 v177, v43, v122
	v_mul_f32_e32 v122, v174, v131
	v_mul_f32_e32 v125, v46, v125
	v_mul_f32_e32 v131, v44, v122
	v_mul_f32_e32 v122, v174, v129
	v_mul_f32_e32 v174, v45, v122
	v_mul_f32_e32 v122, 0xbfb8aa3b, v125
	v_exp_f32_e32 v122, v122
	v_mul_f32_e32 v129, 0xbfb8aa3b, v131
	v_exp_f32_e32 v129, v129
	v_mul_f32_e32 v124, 0xbfb8aa3b, v175
	v_add_f32_e32 v122, 1.0, v122
	v_rcp_f32_e32 v122, v122
	v_add_f32_e32 v129, 1.0, v129
	v_rcp_f32_e32 v129, v129
	v_exp_f32_e32 v124, v124
	v_mul_f32_e32 v122, v125, v122
	v_mul_f32_e32 v125, 0xbfb8aa3b, v126
	v_exp_f32_e32 v125, v125
	v_mul_f32_e32 v129, v131, v129
	v_mul_f32_e32 v131, 0xbfb8aa3b, v174
	v_exp_f32_e32 v131, v131
	v_add_f32_e32 v125, 1.0, v125
	v_rcp_f32_e32 v125, v125
	v_add_f32_e32 v124, 1.0, v124
	v_add_f32_e32 v131, 1.0, v131
	v_rcp_f32_e32 v131, v131
	v_mul_f32_e32 v125, v126, v125
	v_mul_f32_e32 v126, 0xbfb8aa3b, v176
	v_exp_f32_e32 v126, v126
	v_rcp_f32_e32 v124, v124
	v_mul_f32_e32 v131, v174, v131
	v_mul_f32_e32 v174, v47, v130
	v_add_f32_e32 v126, 1.0, v126
	v_rcp_f32_e32 v126, v126
	v_mul_f32_e32 v130, v173, v134
	v_mul_f32_e32 v134, v48, v130
	v_mul_f32_e32 v130, v173, v133
	v_mul_f32_e32 v124, v175, v124
	v_mul_f32_e32 v175, v49, v130
	v_mul_f32_e32 v130, v173, v136
	v_mul_f32_e32 v136, v42, v130
	v_mul_f32_e32 v130, v173, v135
	v_mul_f32_e32 v126, v176, v126
	v_mul_f32_e32 v176, v43, v130
	v_mul_f32_e32 v130, v173, v139
	v_mul_f32_e32 v139, v44, v130
	v_mul_f32_e32 v130, v173, v137
	v_mul_f32_e32 v137, 0xbfb8aa3b, v139
	v_exp_f32_e32 v137, v137
	v_mul_f32_e32 v173, v45, v130
	v_mul_f32_e32 v130, 0xbfb8aa3b, v132
	v_exp_f32_e32 v130, v130
	v_mul_f32_e32 v133, 0xbfb8aa3b, v134
	v_exp_f32_e32 v133, v133
	v_add_f32_e32 v137, 1.0, v137
	v_rcp_f32_e32 v137, v137
	v_add_f32_e32 v130, 1.0, v130
	v_rcp_f32_e32 v130, v130
	v_add_f32_e32 v133, 1.0, v133
	v_rcp_f32_e32 v133, v133
	v_mul_f32_e32 v137, v139, v137
	v_mul_f32_e32 v139, 0xbfb8aa3b, v173
	v_exp_f32_e32 v139, v139
	v_mul_f32_e32 v130, v132, v130
	v_mul_f32_e32 v132, 0xbfb8aa3b, v174
	v_exp_f32_e32 v132, v132
	v_mul_f32_e32 v133, v134, v133
	v_mul_f32_e32 v134, 0xbfb8aa3b, v175
	v_exp_f32_e32 v134, v134
	v_add_f32_e32 v139, 1.0, v139
	v_rcp_f32_e32 v139, v139
	v_add_f32_e32 v132, 1.0, v132
	v_rcp_f32_e32 v132, v132
	v_add_f32_e32 v134, 1.0, v134
	v_mul_f32_e32 v138, v172, v138
	v_rcp_f32_e32 v134, v134
	v_mul_f32_e32 v139, v173, v139
	v_mul_f32_e32 v173, v47, v138
	v_mul_f32_e32 v138, v172, v142
	v_mul_f32_e32 v142, v48, v138
	v_mul_f32_e32 v138, v172, v140
	v_mul_f32_e32 v132, v174, v132
	v_mul_f32_e32 v174, v49, v138
	v_mul_f32_e32 v138, v172, v150
	v_mul_f32_e32 v150, v42, v138
	v_mul_f32_e32 v138, v172, v143
	v_mul_f32_e32 v134, v175, v134
	v_mul_f32_e32 v141, v172, v141
	v_mul_f32_e32 v175, v43, v138
	v_mul_f32_e32 v138, v172, v161
	v_mul_f32_e32 v141, v46, v141
	v_mul_f32_e32 v161, v44, v138
	v_mul_f32_e32 v138, v172, v151
	v_mul_f32_e32 v172, v45, v138
	v_mul_f32_e32 v138, 0xbfb8aa3b, v141
	v_exp_f32_e32 v138, v138
	v_mul_f32_e32 v151, 0xbfb8aa3b, v161
	v_exp_f32_e32 v151, v151
	v_mul_f32_e32 v140, 0xbfb8aa3b, v173
	v_add_f32_e32 v138, 1.0, v138
	v_rcp_f32_e32 v138, v138
	v_add_f32_e32 v151, 1.0, v151
	v_rcp_f32_e32 v151, v151
	v_exp_f32_e32 v140, v140
	v_mul_f32_e32 v138, v141, v138
	v_mul_f32_e32 v141, 0xbfb8aa3b, v142
	v_exp_f32_e32 v141, v141
	v_mul_f32_e32 v151, v161, v151
	v_mul_f32_e32 v161, 0xbfb8aa3b, v172
	v_exp_f32_e32 v161, v161
	v_add_f32_e32 v141, 1.0, v141
	v_rcp_f32_e32 v141, v141
	v_rsq_f32_e32 v171, v171
	v_add_f32_e32 v161, 1.0, v161
	v_rcp_f32_e32 v161, v161
	v_mul_f32_e32 v141, v142, v141
	v_mul_f32_e32 v142, 0xbfb8aa3b, v174
	v_exp_f32_e32 v142, v142
	v_add_f32_e32 v140, 1.0, v140
	v_rcp_f32_e32 v140, v140
	v_mul_f32_e32 v152, v171, v152
	v_add_f32_e32 v142, 1.0, v142
	v_rcp_f32_e32 v142, v142
	v_mul_f32_e32 v161, v172, v161
	v_mul_f32_e32 v172, v47, v152
	v_mul_f32_e32 v152, v171, v164
	v_mul_f32_e32 v164, v48, v152
	v_mul_f32_e32 v152, v171, v163
	v_mul_f32_e32 v140, v173, v140
	v_mul_f32_e32 v173, v49, v152
	v_mul_f32_e32 v152, v171, v166
	v_mul_f32_e32 v166, v42, v152
	v_mul_f32_e32 v152, v171, v165
	v_mul_f32_e32 v142, v174, v142
	v_mul_f32_e32 v174, v43, v152
	v_mul_f32_e32 v152, v171, v168
	v_mul_f32_e32 v168, v44, v152
	v_mul_f32_e32 v162, v171, v162
	v_mul_f32_e32 v152, v171, v167
	v_mul_f32_e32 v167, 0xbfb8aa3b, v168
	v_mul_f32_e32 v162, v46, v162
	v_exp_f32_e32 v167, v167
	v_mul_f32_e32 v171, v45, v152
	v_mul_f32_e32 v152, 0xbfb8aa3b, v162
	v_exp_f32_e32 v152, v152
	v_mul_f32_e32 v163, 0xbfb8aa3b, v164
	v_exp_f32_e32 v163, v163
	v_add_f32_e32 v167, 1.0, v167
	v_rcp_f32_e32 v167, v167
	v_add_f32_e32 v152, 1.0, v152
	v_rcp_f32_e32 v152, v152
	v_add_f32_e32 v163, 1.0, v163
	v_rcp_f32_e32 v163, v163
	v_mul_f32_e32 v167, v168, v167
	v_mul_f32_e32 v168, 0xbfb8aa3b, v171
	v_exp_f32_e32 v168, v168
	v_mul_f32_e32 v152, v162, v152
	v_mul_f32_e32 v162, 0xbfb8aa3b, v172
	v_exp_f32_e32 v162, v162
	v_mul_f32_e32 v163, v164, v163
	v_mul_f32_e32 v164, 0xbfb8aa3b, v173
	v_fmamk_f32 v170, v170, 0x3b000000, v235
	v_fmamk_f32 v169, v169, 0x3b000000, v235
	v_exp_f32_e32 v164, v164
	v_add_f32_e32 v168, 1.0, v168
	v_rsq_f32_e32 v170, v170
	v_rsq_f32_e32 v169, v169
	v_rcp_f32_e32 v168, v168
	v_add_f32_e32 v162, 1.0, v162
	v_rcp_f32_e32 v162, v162
	v_add_f32_e32 v164, 1.0, v164
	v_mul_f32_e32 v153, v170, v153
	v_mul_f32_e32 v0, v169, v0
	v_rcp_f32_e32 v164, v164
	v_mul_f32_e32 v168, v171, v168
	v_mul_f32_e32 v171, v47, v153
	v_mul_f32_e32 v153, v170, v156
	v_mul_f32_e32 v0, v47, v0
	v_mul_f32_e32 v47, v169, v145
	v_mul_f32_e32 v155, v170, v155
	v_mul_f32_e32 v156, v48, v153
	v_mul_f32_e32 v153, v170, v154
	v_mul_f32_e32 v51, v169, v51
	v_mul_f32_e32 v47, v48, v47
	v_mul_f32_e32 v48, v169, v144
	v_mul_f32_e32 v162, v172, v162
	v_mul_f32_e32 v155, v46, v155
	v_mul_f32_e32 v172, v49, v153
	v_mul_f32_e32 v153, v170, v158
	v_mul_f32_e32 v46, v46, v51
	v_mul_f32_e32 v51, v49, v48
	v_mul_f32_e32 v48, v169, v147
	v_mul_f32_e32 v158, v42, v153
	v_mul_f32_e32 v153, v170, v157
	v_mul_f32_e32 v42, v42, v48
	v_mul_f32_e32 v48, v169, v146
	v_mul_f32_e32 v164, v173, v164
	v_mul_f32_e32 v173, v43, v153
	v_mul_f32_e32 v153, v170, v160
	v_mul_f32_e32 v43, v43, v48
	v_mul_f32_e32 v48, v169, v149
	v_mul_f32_e32 v160, v44, v153
	v_mul_f32_e32 v153, v170, v159
	v_mul_f32_e32 v44, v44, v48
	v_mul_f32_e32 v48, v169, v148
	v_mul_f32_e32 v170, v45, v153
	v_mul_f32_e32 v45, v45, v48
	v_mul_f32_e32 v48, 0xbfb8aa3b, v46
	v_exp_f32_e32 v48, v48
	v_mul_f32_e32 v57, 0xbfb8aa3b, v58
	v_exp_f32_e32 v57, v57
	v_mul_f32_e32 v65, 0xbfb8aa3b, v114
	v_add_f32_e32 v48, 1.0, v48
	v_rcp_f32_e32 v48, v48
	v_add_f32_e32 v57, 1.0, v57
	v_rcp_f32_e32 v57, v57
	v_exp_f32_e32 v65, v65
	v_mul_f32_e32 v48, v46, v48
	v_mul_f32_e32 v46, 0xbfb8aa3b, v0
	v_exp_f32_e32 v46, v46
	v_mul_f32_e32 v57, v58, v57
	v_mul_f32_e32 v58, 0xbfb8aa3b, v179
	v_exp_f32_e32 v58, v58
	v_add_f32_e32 v46, 1.0, v46
	v_rcp_f32_e32 v46, v46
	v_add_f32_e32 v65, 1.0, v65
	v_rcp_f32_e32 v65, v65
	v_mul_f32_e32 v127, 0xbfb8aa3b, v128
	v_mul_f32_e32 v49, v0, v46
	v_mul_f32_e32 v0, 0xbfb8aa3b, v47
	v_exp_f32_e32 v0, v0
	v_exp_f32_e32 v127, v127
	v_add_f32_e32 v58, 1.0, v58
	v_rcp_f32_e32 v58, v58
	v_add_f32_e32 v0, 1.0, v0
	v_rcp_f32_e32 v0, v0
	v_mul_f32_e32 v65, v114, v65
	v_mul_f32_e32 v114, 0xbfb8aa3b, v178
	v_exp_f32_e32 v114, v114
	v_mul_f32_e32 v144, v47, v0
	v_mul_f32_e32 v0, 0xbfb8aa3b, v51
	v_exp_f32_e32 v0, v0
	v_add_f32_e32 v127, 1.0, v127
	v_rcp_f32_e32 v127, v127
	v_mul_f32_e32 v135, 0xbfb8aa3b, v136
	v_add_f32_e32 v0, 1.0, v0
	v_rcp_f32_e32 v0, v0
	v_exp_f32_e32 v135, v135
	v_mul_f32_e32 v58, v179, v58
	v_add_f32_e32 v114, 1.0, v114
	v_mul_f32_e32 v146, v51, v0
	v_mul_f32_e32 v0, 0xbfb8aa3b, v42
	v_exp_f32_e32 v0, v0
	v_rcp_f32_e32 v114, v114
	v_mul_f32_e32 v127, v128, v127
	v_mul_f32_e32 v128, 0xbfb8aa3b, v177
	v_add_f32_e32 v0, 1.0, v0
	v_rcp_f32_e32 v0, v0
	v_exp_f32_e32 v128, v128
	v_add_f32_e32 v135, 1.0, v135
	v_rcp_f32_e32 v135, v135
	v_mul_f32_e32 v145, v42, v0
	v_mul_f32_e32 v0, 0xbfb8aa3b, v43
	v_exp_f32_e32 v0, v0
	v_mul_f32_e32 v143, 0xbfb8aa3b, v150
	v_exp_f32_e32 v143, v143
	v_mul_f32_e32 v153, 0xbfb8aa3b, v155
	v_add_f32_e32 v0, 1.0, v0
	v_rcp_f32_e32 v0, v0
	v_max3_f32 v42, |v60|, 0, |v62|
	v_mul_f32_e32 v114, v178, v114
	v_exp_f32_e32 v153, v153
	v_mul_f32_e32 v147, v43, v0
	v_mul_f32_e32 v0, 0xbfb8aa3b, v44
	v_exp_f32_e32 v0, v0
	v_max3_f32 v42, v42, |v63|, |v64|
	v_add_f32_e32 v128, 1.0, v128
	v_max3_f32 v42, v42, |v65|, |v114|
	v_add_f32_e32 v0, 1.0, v0
	v_rcp_f32_e32 v0, v0
	v_rcp_f32_e32 v128, v128
	v_mul_f32_e32 v135, v136, v135
	v_mul_f32_e32 v136, 0xbfb8aa3b, v176
	v_mul_f32_e32 v148, v44, v0
	v_mul_f32_e32 v0, 0xbfb8aa3b, v45
	v_exp_f32_e32 v0, v0
	v_max3_f32 v42, v42, |v115|, |v123|
	v_exp_f32_e32 v136, v136
	v_add_f32_e32 v143, 1.0, v143
	v_add_f32_e32 v0, 1.0, v0
	v_rcp_f32_e32 v0, v0
	v_rcp_f32_e32 v143, v143
	v_mul_f32_e32 v165, 0xbfb8aa3b, v166
	v_add_f32_e32 v153, 1.0, v153
	v_mul_f32_e32 v149, v45, v0
	v_max3_f32 v0, |v53|, 0, |v54|
	v_max3_f32 v0, v0, |v55|, |v56|
	v_max3_f32 v0, v0, |v57|, |v58|
	v_max3_f32 v0, v0, |v59|, |v61|
	s_nop 1
	v_max_f32_dpp v0, v0, v0 quad_perm:[1,0,3,2] row_mask:0xf bank_mask:0xf
	s_nop 1
	v_max_f32_dpp v0, v0, v0 quad_perm:[2,3,0,1] row_mask:0xf bank_mask:0xf
	s_nop 1
	v_max_f32_dpp v0, v0, v0 row_half_mirror row_mask:0xf bank_mask:0xf
	s_nop 1
	v_max_f32_dpp v0, v0, v0 row_ror:8 row_mask:0xf bank_mask:0xf
	v_mov_b32_e32 v169, v0
	s_nop 1
	v_permlane16_swap_b32_e32 v0, v169
	s_nop 0
	v_max_f32_e32 v0, v0, v169
	v_mov_b32_e32 v169, v0
	s_nop 1
	v_permlane32_swap_b32_e32 v0, v169
	s_nop 0
	v_max_f32_e32 v0, v0, v169
	v_mov_b32_e32 v169, v0
	v_exp_f32_e32 v165, v165
	v_rcp_f32_e32 v153, v153
	v_max3_f32 v43, |v122|, 0, |v124|
	v_mul_f32_e32 v128, v177, v128
	s_waitcnt lgkmcnt(0)
	v_max_f32_e32 v169, v169, v169
	v_max_f32_e32 v0, v0, v169
	s_nop 1
	v_max_f32_dpp v42, v42, v42 quad_perm:[1,0,3,2] row_mask:0xf bank_mask:0xf
	s_nop 1
	v_max_f32_dpp v42, v42, v42 quad_perm:[2,3,0,1] row_mask:0xf bank_mask:0xf
	s_nop 1
	v_max_f32_dpp v42, v42, v42 row_half_mirror row_mask:0xf bank_mask:0xf
	s_nop 1
	v_max_f32_dpp v42, v42, v42 row_ror:8 row_mask:0xf bank_mask:0xf
	v_mov_b32_e32 v169, v42
	s_nop 1
	v_permlane16_swap_b32_e32 v42, v169
	s_nop 0
	v_max_f32_e32 v42, v42, v169
	v_mov_b32_e32 v169, v42
	s_nop 1
	v_permlane32_swap_b32_e32 v42, v169
	s_nop 0
	v_max_f32_e32 v42, v42, v169
	v_mov_b32_e32 v169, v42
	v_max3_f32 v43, v43, |v125|, |v126|
	v_add_f32_e32 v136, 1.0, v136
	v_max3_f32 v43, v43, |v127|, |v128|
	v_rcp_f32_e32 v136, v136
	v_mul_f32_e32 v143, v150, v143
	v_mul_f32_e32 v150, 0xbfb8aa3b, v175
	v_max3_f32 v43, v43, |v129|, |v131|
	s_waitcnt lgkmcnt(0)
	v_max_f32_e32 v169, v169, v169
	v_exp_f32_e32 v150, v150
	v_add_f32_e32 v165, 1.0, v165
	v_mul_f32_e32 v153, v155, v153
	v_mul_f32_e32 v155, 0xbfb8aa3b, v156
	v_max_f32_e32 v42, v42, v169
	s_nop 1
	v_max_f32_dpp v43, v43, v43 quad_perm:[1,0,3,2] row_mask:0xf bank_mask:0xf
	s_nop 1
	v_max_f32_dpp v43, v43, v43 quad_perm:[2,3,0,1] row_mask:0xf bank_mask:0xf
	s_nop 1
	v_max_f32_dpp v43, v43, v43 row_half_mirror row_mask:0xf bank_mask:0xf
	s_nop 1
	v_max_f32_dpp v43, v43, v43 row_ror:8 row_mask:0xf bank_mask:0xf
	v_mov_b32_e32 v169, v43
	s_nop 1
	v_permlane16_swap_b32_e32 v43, v169
	s_nop 0
	v_max_f32_e32 v43, v43, v169
	v_mov_b32_e32 v169, v43
	s_nop 1
	v_permlane32_swap_b32_e32 v43, v169
	s_nop 0
	v_max_f32_e32 v43, v43, v169
	v_mov_b32_e32 v169, v43
	v_rcp_f32_e32 v165, v165
	v_exp_f32_e32 v155, v155
	v_mul_f32_e32 v157, 0xbfb8aa3b, v158
	v_exp_f32_e32 v157, v157
	v_mul_f32_e32 v159, 0xbfb8aa3b, v160
	v_max3_f32 v44, |v130|, 0, |v132|
	v_mul_f32_e32 v136, v176, v136
	v_exp_f32_e32 v159, v159
	v_max3_f32 v44, v44, |v133|, |v134|
	v_add_f32_e32 v150, 1.0, v150
	v_max3_f32 v44, v44, |v135|, |v136|
	v_rcp_f32_e32 v150, v150
	v_mul_f32_e32 v165, v166, v165
	v_mul_f32_e32 v166, 0xbfb8aa3b, v174
	v_add_f32_e32 v155, 1.0, v155
	v_max3_f32 v44, v44, |v137|, |v139|
	s_waitcnt lgkmcnt(0)
	v_max_f32_e32 v169, v169, v169
	v_exp_f32_e32 v166, v166
	v_rcp_f32_e32 v155, v155
	v_add_f32_e32 v157, 1.0, v157
	v_max_f32_e32 v43, v43, v169
	s_nop 1
	v_max_f32_dpp v44, v44, v44 quad_perm:[1,0,3,2] row_mask:0xf bank_mask:0xf
	s_nop 1
	v_max_f32_dpp v44, v44, v44 quad_perm:[2,3,0,1] row_mask:0xf bank_mask:0xf
	s_nop 1
	v_max_f32_dpp v44, v44, v44 row_half_mirror row_mask:0xf bank_mask:0xf
	s_nop 1
	v_max_f32_dpp v44, v44, v44 row_ror:8 row_mask:0xf bank_mask:0xf
	v_mov_b32_e32 v169, v44
	s_nop 1
	v_permlane16_swap_b32_e32 v44, v169
	s_nop 0
	v_max_f32_e32 v44, v44, v169
	v_mov_b32_e32 v169, v44
	s_nop 1
	v_permlane32_swap_b32_e32 v44, v169
	s_nop 0
	v_max_f32_e32 v44, v44, v169
	v_mov_b32_e32 v169, v44
	v_rcp_f32_e32 v157, v157
	v_add_f32_e32 v159, 1.0, v159
	v_rcp_f32_e32 v159, v159
	v_max3_f32 v45, |v138|, 0, |v140|
	v_mul_f32_e32 v150, v175, v150
	v_mul_f32_e32 v154, 0xbfb8aa3b, v171
	v_max3_f32 v45, v45, |v141|, |v142|
	v_add_f32_e32 v166, 1.0, v166
	v_exp_f32_e32 v154, v154
	v_mul_f32_e32 v155, v156, v155
	v_mul_f32_e32 v156, 0xbfb8aa3b, v172
	v_max3_f32 v45, v45, |v143|, |v150|
	v_rcp_f32_e32 v166, v166
	v_exp_f32_e32 v156, v156
	v_mul_f32_e32 v157, v158, v157
	v_mul_f32_e32 v158, 0xbfb8aa3b, v173
	v_max3_f32 v45, v45, |v151|, |v161|
	s_waitcnt lgkmcnt(0)
	v_max_f32_e32 v169, v169, v169
	v_exp_f32_e32 v158, v158
	v_mul_f32_e32 v159, v160, v159
	v_mul_f32_e32 v160, 0xbfb8aa3b, v170
	v_max_f32_e32 v44, v44, v169
	s_nop 1
	v_max_f32_dpp v45, v45, v45 quad_perm:[1,0,3,2] row_mask:0xf bank_mask:0xf
	s_nop 1
	v_max_f32_dpp v45, v45, v45 quad_perm:[2,3,0,1] row_mask:0xf bank_mask:0xf
	s_nop 1
	v_max_f32_dpp v45, v45, v45 row_half_mirror row_mask:0xf bank_mask:0xf
	s_nop 1
	v_max_f32_dpp v45, v45, v45 row_ror:8 row_mask:0xf bank_mask:0xf
	v_mov_b32_e32 v169, v45
	s_nop 1
	v_permlane16_swap_b32_e32 v45, v169
	s_nop 0
	v_max_f32_e32 v45, v45, v169
	v_mov_b32_e32 v169, v45
	s_nop 1
	v_permlane32_swap_b32_e32 v45, v169
	s_nop 0
	v_max_f32_e32 v45, v45, v169
	v_mov_b32_e32 v169, v45
	v_exp_f32_e32 v160, v160
	v_add_f32_e32 v154, 1.0, v154
	v_max3_f32 v46, |v152|, 0, |v162|
	v_mul_f32_e32 v166, v174, v166
	v_rcp_f32_e32 v154, v154
	v_add_f32_e32 v156, 1.0, v156
	v_max3_f32 v46, v46, |v163|, |v164|
	v_rcp_f32_e32 v156, v156
	v_add_f32_e32 v158, 1.0, v158
	v_max3_f32 v46, v46, |v165|, |v166|
	v_rcp_f32_e32 v158, v158
	v_add_f32_e32 v160, 1.0, v160
	v_max3_f32 v46, v46, |v167|, |v168|
	s_waitcnt lgkmcnt(0)
	v_max_f32_e32 v169, v169, v169
	v_rcp_f32_e32 v160, v160
	v_max_f32_e32 v45, v45, v169
	s_nop 1
	v_max_f32_dpp v46, v46, v46 quad_perm:[1,0,3,2] row_mask:0xf bank_mask:0xf
	s_nop 1
	v_max_f32_dpp v46, v46, v46 quad_perm:[2,3,0,1] row_mask:0xf bank_mask:0xf
	s_nop 1
	v_max_f32_dpp v46, v46, v46 row_half_mirror row_mask:0xf bank_mask:0xf
	s_nop 1
	v_max_f32_dpp v46, v46, v46 row_ror:8 row_mask:0xf bank_mask:0xf
	v_mov_b32_e32 v169, v46
	s_nop 1
	v_permlane16_swap_b32_e32 v46, v169
	s_nop 0
	v_max_f32_e32 v46, v46, v169
	v_mov_b32_e32 v169, v46
	s_nop 1
	v_permlane32_swap_b32_e32 v46, v169
	s_nop 0
	v_max_f32_e32 v46, v46, v169
	v_mov_b32_e32 v169, v46
	v_mul_f32_e32 v154, v171, v154
	v_mul_f32_e32 v156, v172, v156
	v_max3_f32 v47, |v153|, 0, |v154|
	v_mul_f32_e32 v158, v173, v158
	v_max3_f32 v47, v47, |v155|, |v156|
	v_mul_f32_e32 v160, v170, v160
	v_max3_f32 v47, v47, |v157|, |v158|
	v_max3_f32 v47, v47, |v159|, |v160|
	s_waitcnt lgkmcnt(0)
	v_max_f32_e32 v169, v169, v169
	v_max_f32_e32 v46, v46, v169
	s_nop 1
	v_max_f32_dpp v47, v47, v47 quad_perm:[1,0,3,2] row_mask:0xf bank_mask:0xf
	s_nop 1
	v_max_f32_dpp v47, v47, v47 quad_perm:[2,3,0,1] row_mask:0xf bank_mask:0xf
	s_nop 1
	v_max_f32_dpp v47, v47, v47 row_half_mirror row_mask:0xf bank_mask:0xf
	s_nop 1
	v_max_f32_dpp v47, v47, v47 row_ror:8 row_mask:0xf bank_mask:0xf
	v_mov_b32_e32 v169, v47
	s_nop 1
	v_permlane16_swap_b32_e32 v47, v169
	s_nop 0
	v_max_f32_e32 v47, v47, v169
	v_mov_b32_e32 v169, v47
	s_nop 1
	v_permlane32_swap_b32_e32 v47, v169
	s_nop 0
	v_max_f32_e32 v47, v47, v169
	v_mov_b32_e32 v169, v47
	v_max3_f32 v51, |v48|, 0, |v49|
	v_max3_f32 v51, v51, |v144|, |v146|
	v_max3_f32 v51, v51, |v145|, |v147|
	v_max3_f32 v51, v51, |v148|, |v149|
	s_waitcnt lgkmcnt(0)
	v_max_f32_e32 v169, v169, v169
	v_max_f32_e32 v47, v47, v169
	s_nop 1
	v_max_f32_dpp v51, v51, v51 quad_perm:[1,0,3,2] row_mask:0xf bank_mask:0xf
	s_nop 1
	v_max_f32_dpp v51, v51, v51 quad_perm:[2,3,0,1] row_mask:0xf bank_mask:0xf
	s_nop 1
	v_max_f32_dpp v51, v51, v51 row_half_mirror row_mask:0xf bank_mask:0xf
	s_nop 1
	v_max_f32_dpp v51, v51, v51 row_ror:8 row_mask:0xf bank_mask:0xf
	v_mov_b32_e32 v169, v51
	s_nop 1
	v_permlane16_swap_b32_e32 v51, v169
	s_nop 0
	v_max_f32_e32 v51, v51, v169
	v_mov_b32_e32 v169, v51
	s_nop 1
	v_permlane32_swap_b32_e32 v51, v169
	s_nop 0
	v_max_f32_e32 v51, v51, v169
	v_mov_b32_e32 v169, v51
	s_waitcnt lgkmcnt(0)
	v_max_f32_e32 v169, v169, v169
	v_max_f32_e32 v51, v51, v169
	v_mov_b32_e32 v169, v0
	s_waitcnt lgkmcnt(0)
	v_max_f32_e32 v169, v169, v169
	v_max_f32_e32 v0, v0, v169
	v_mov_b32_e32 v169, v42
	s_waitcnt lgkmcnt(0)
	v_max_f32_e32 v169, v169, v169
	v_max_f32_e32 v42, v42, v169
	v_mov_b32_e32 v169, v43
	s_waitcnt lgkmcnt(0)
	v_max_f32_e32 v169, v169, v169
	v_max_f32_e32 v43, v43, v169
	v_mov_b32_e32 v169, v44
	s_waitcnt lgkmcnt(0)
	v_max_f32_e32 v169, v169, v169
	v_max_f32_e32 v44, v44, v169
	v_mov_b32_e32 v169, v45
	s_waitcnt lgkmcnt(0)
	v_max_f32_e32 v169, v169, v169
	v_max_f32_e32 v45, v45, v169
	v_mov_b32_e32 v169, v46
	s_waitcnt lgkmcnt(0)
	v_max_f32_e32 v169, v169, v169
	v_max_f32_e32 v46, v46, v169
	v_mov_b32_e32 v169, v47
	s_waitcnt lgkmcnt(0)
	v_max_f32_e32 v169, v169, v169
	v_max_f32_e32 v47, v47, v169
	v_mov_b32_e32 v169, v51
	s_waitcnt lgkmcnt(0)
	v_max_f32_e32 v169, v169, v169
	v_max_f32_e32 v51, v51, v169
	v_mov_b32_e32 v169, v0
	s_waitcnt lgkmcnt(0)
	v_max_f32_e32 v169, v169, v169
	v_max_f32_e32 v0, v0, v169
	v_mov_b32_e32 v169, v42
	s_waitcnt lgkmcnt(0)
	v_max_f32_e32 v169, v169, v169
	v_max_f32_e32 v42, v42, v169
	v_mov_b32_e32 v169, v43
	s_waitcnt lgkmcnt(0)
	v_max_f32_e32 v169, v169, v169
	v_max_f32_e32 v43, v43, v169
	v_mov_b32_e32 v169, v44
	s_waitcnt lgkmcnt(0)
	v_max_f32_e32 v169, v169, v169
	v_max_f32_e32 v44, v44, v169
	v_mov_b32_e32 v169, v45
	s_waitcnt lgkmcnt(0)
	v_max_f32_e32 v169, v169, v169
	v_max_f32_e32 v45, v45, v169
	v_mov_b32_e32 v169, v46
	s_waitcnt lgkmcnt(0)
	v_max_f32_e32 v169, v169, v169
	v_max_f32_e32 v46, v46, v169
	v_mov_b32_e32 v169, v47
	s_waitcnt lgkmcnt(0)
	v_max_f32_e32 v169, v169, v169
	v_max_f32_e32 v47, v47, v169
	v_mov_b32_e32 v169, v51
	s_waitcnt lgkmcnt(0)
	v_max_f32_e32 v169, v169, v169
	v_max_f32_e32 v51, v51, v169
	v_mov_b32_e32 v169, v0
	s_waitcnt lgkmcnt(0)
	v_max_f32_e32 v169, v169, v169
	v_max_f32_e32 v0, v0, v169
	v_mov_b32_e32 v169, v42
	s_waitcnt lgkmcnt(0)
	v_max_f32_e32 v169, v169, v169
	v_max_f32_e32 v42, v42, v169
	v_mov_b32_e32 v169, v43
	s_waitcnt lgkmcnt(0)
	v_max_f32_e32 v169, v169, v169
	v_max_f32_e32 v43, v43, v169
	v_mov_b32_e32 v169, v44
	s_waitcnt lgkmcnt(0)
	v_max_f32_e32 v169, v169, v169
	v_max_f32_e32 v44, v44, v169
	v_mov_b32_e32 v169, v45
	s_waitcnt lgkmcnt(0)
	v_max_f32_e32 v169, v169, v169
	v_max_f32_e32 v45, v45, v169
	v_mov_b32_e32 v169, v46
	s_waitcnt lgkmcnt(0)
	v_max_f32_e32 v169, v169, v169
	v_max_f32_e32 v169, v46, v169
	v_mov_b32_e32 v46, v47
	s_waitcnt lgkmcnt(0)
	v_max_f32_e32 v46, v46, v46
	v_max_f32_e32 v47, v47, v46
	v_mov_b32_e32 v46, v51
	s_waitcnt lgkmcnt(0)
	v_max_f32_e32 v46, v46, v46
	v_max_f32_e32 v51, v51, v46
	v_mov_b32_e32 v46, v0
	s_waitcnt lgkmcnt(0)
	v_max_f32_e32 v46, v46, v46
	v_max_f32_e32 v0, v0, v46
	v_mov_b32_e32 v46, v42
	s_waitcnt lgkmcnt(0)
	v_max_f32_e32 v46, v46, v46
	v_max_f32_e32 v46, v42, v46
	v_mov_b32_e32 v42, v43
	s_waitcnt lgkmcnt(0)
	v_max_f32_e32 v42, v42, v42
	v_max_f32_e32 v178, v43, v42
	v_mov_b32_e32 v42, v44
	v_mov_b32_e32 v180, v178
	s_waitcnt lgkmcnt(0)
	v_max_f32_e32 v42, v42, v42
	v_max_f32_e32 v176, v44, v42
	v_mov_b32_e32 v42, v45
	v_mov_b32_e32 v179, v176
	s_waitcnt lgkmcnt(0)
	v_max_f32_e32 v42, v42, v42
	v_max_f32_e32 v175, v45, v42
	v_mov_b32_e32 v42, v169
	v_mov_b32_e32 v177, v175
	s_waitcnt lgkmcnt(0)
	v_max_f32_e32 v42, v42, v42
	v_max_f32_e32 v173, v169, v42
	v_mov_b32_e32 v42, v47
	v_mov_b32_e32 v174, v173
	s_waitcnt lgkmcnt(0)
	v_max_f32_e32 v42, v42, v42
	v_max_f32_e32 v171, v47, v42
	v_mov_b32_e32 v42, v51
	v_mov_b32_e32 v47, v46
	v_mov_b32_e32 v172, v171
	s_waitcnt lgkmcnt(0)
	v_max_f32_e32 v42, v42, v42
	v_max_f32_e32 v169, v51, v42
	v_mov_b32_e32 v42, v0
	v_mov_b32_e32 v170, v169
	v_ashrrev_i32_e32 v51, 31, v50
	v_lshl_add_u64 v[44:45], s[36:37], 0, v[50:51]
	s_waitcnt lgkmcnt(0)
	v_max3_f32 v50, v0, v42, s72
	s_and_saveexec_b64 s[40:41], s[26:27]
	s_cbranch_execz .LBB0_549
	v_lshl_add_u64 v[42:43], v[44:45], 2, s[30:31]
	v_mul_f32_e32 v0, 0x3c010204, v50
	global_store_dword v[42:43], v0, off

.LBB0_599:
	s_mov_b64 s[4:5], s[0:1]
	s_load_dwordx2 s[10:11], s[4:5], 0xd0
	v_mbcnt_lo_u32_b32 v0, -1, 0
	v_mbcnt_hi_u32_b32 v0, -1, v0
	s_waitcnt lgkmcnt(0)
	s_add_u32 s8, s10, 0x27c60000
	v_add_u32_e32 v2, s67, v0
	s_addc_u32 s9, s11, 0
	v_and_b32_e32 v0, 63, v2
	v_ashrrev_i32_e32 v2, 6, v2
	v_lshlrev_b32_e32 v3, 4, v0
	v_mul_lo_u32 v4, v2, s44
	v_add3_u32 v3, 0, v3, v4
	ds_read_b128 v[6:9], v3
	v_cmp_eq_u32_e64 s[6:7], 0, v0
	ds_read_b128 v[12:15], v3 offset:58240
	s_waitcnt lgkmcnt(1)
	v_lshlrev_b32_e32 v114, 16, v6
	v_and_b32_e32 v115, 0xffff0000, v6
	v_lshlrev_b32_e32 v122, 16, v7
	v_and_b32_e32 v123, 0xffff0000, v7
	v_lshlrev_b32_e32 v6, 16, v8
	v_and_b32_e32 v7, 0xffff0000, v8
	v_lshlrev_b32_e32 v60, 16, v9
	v_and_b32_e32 v61, 0xffff0000, v9
	ds_read_b128 v[8:11], v3 offset:8320
	s_waitcnt lgkmcnt(1)
	v_lshlrev_b32_e32 v20, 16, v12
	v_and_b32_e32 v21, 0xffff0000, v12
	v_lshlrev_b32_e32 v22, 16, v13
	v_and_b32_e32 v23, 0xffff0000, v13
	s_waitcnt lgkmcnt(0)
	v_lshlrev_b32_e32 v62, 16, v8
	v_and_b32_e32 v63, 0xffff0000, v8
	v_lshlrev_b32_e32 v64, 16, v9
	v_and_b32_e32 v65, 0xffff0000, v9
	v_lshlrev_b32_e32 v56, 16, v10
	v_and_b32_e32 v57, 0xffff0000, v10
	v_lshlrev_b32_e32 v58, 16, v11
	v_and_b32_e32 v59, 0xffff0000, v11
	ds_read_b128 v[8:11], v3 offset:16640
	v_max3_f32 v4, |v62|, 0, |v63|
	v_max3_f32 v4, v4, |v64|, |v65|
	v_max3_f32 v4, v4, |v56|, |v57|
	v_max3_f32 v4, v4, |v58|, |v59|
	s_waitcnt lgkmcnt(0)
	v_lshlrev_b32_e32 v48, 16, v8
	v_and_b32_e32 v49, 0xffff0000, v8
	v_lshlrev_b32_e32 v50, 16, v9
	v_and_b32_e32 v51, 0xffff0000, v9
	v_lshlrev_b32_e32 v40, 16, v10
	v_and_b32_e32 v41, 0xffff0000, v10
	v_lshlrev_b32_e32 v42, 16, v11
	v_and_b32_e32 v43, 0xffff0000, v11
	ds_read_b128 v[8:11], v3 offset:24960
	v_max3_f32 v5, |v48|, 0, |v49|
	v_max3_f32 v5, v5, |v50|, |v51|
	v_max3_f32 v5, v5, |v40|, |v41|
	v_max3_f32 v5, v5, |v42|, |v43|
	s_waitcnt lgkmcnt(0)
	v_lshlrev_b32_e32 v52, 16, v8
	v_and_b32_e32 v53, 0xffff0000, v8
	v_lshlrev_b32_e32 v54, 16, v9
	v_and_b32_e32 v55, 0xffff0000, v9
	v_lshlrev_b32_e32 v44, 16, v10
	v_and_b32_e32 v45, 0xffff0000, v10
	v_lshlrev_b32_e32 v46, 16, v11
	v_and_b32_e32 v47, 0xffff0000, v11
	ds_read_b128 v[8:11], v3 offset:33280
	v_max3_f32 v124, |v52|, 0, |v53|
	v_max3_f32 v124, v124, |v54|, |v55|
	v_max3_f32 v124, v124, |v44|, |v45|
	v_max3_f32 v124, v124, |v46|, |v47|
	s_waitcnt lgkmcnt(0)
	v_lshlrev_b32_e32 v32, 16, v8
	v_and_b32_e32 v33, 0xffff0000, v8
	v_lshlrev_b32_e32 v34, 16, v9
	v_and_b32_e32 v35, 0xffff0000, v9
	v_lshlrev_b32_e32 v24, 16, v10
	v_and_b32_e32 v25, 0xffff0000, v10
	v_lshlrev_b32_e32 v26, 16, v11
	v_and_b32_e32 v27, 0xffff0000, v11
	ds_read_b128 v[8:11], v3 offset:41600
	v_max3_f32 v125, |v32|, 0, |v33|
	v_max3_f32 v125, v125, |v34|, |v35|
	v_max3_f32 v125, v125, |v24|, |v25|
	v_max3_f32 v125, v125, |v26|, |v27|
	s_waitcnt lgkmcnt(0)
	v_lshlrev_b32_e32 v36, 16, v8
	v_and_b32_e32 v37, 0xffff0000, v8
	v_lshlrev_b32_e32 v38, 16, v9
	v_and_b32_e32 v39, 0xffff0000, v9
	v_lshlrev_b32_e32 v28, 16, v10
	v_and_b32_e32 v29, 0xffff0000, v10
	v_lshlrev_b32_e32 v30, 16, v11
	v_and_b32_e32 v31, 0xffff0000, v11
	ds_read_b128 v[8:11], v3 offset:49920
	v_max3_f32 v3, |v114|, 0, |v115|
	v_max3_f32 v3, v3, |v122|, |v123|
	v_max3_f32 v3, v3, |v6|, |v7|
	v_max3_f32 v3, v3, |v60|, |v61|
	s_nop 1
	v_max_f32_dpp v3, v3, v3 quad_perm:[1,0,3,2] row_mask:0xf bank_mask:0xf
	s_nop 1
	v_max_f32_dpp v3, v3, v3 quad_perm:[2,3,0,1] row_mask:0xf bank_mask:0xf
	s_nop 1
	v_max_f32_dpp v3, v3, v3 row_half_mirror row_mask:0xf bank_mask:0xf
	s_nop 1
	v_max_f32_dpp v3, v3, v3 row_ror:8 row_mask:0xf bank_mask:0xf
	v_mov_b32_e32 v129, v3
	s_nop 1
	v_permlane16_swap_b32_e32 v3, v129
	s_nop 0
	v_max_f32_e32 v3, v3, v129
	v_mov_b32_e32 v129, v3
	s_nop 1
	v_permlane32_swap_b32_e32 v3, v129
	s_nop 0
	v_max_f32_e32 v3, v3, v129
	v_mov_b32_e32 v129, v3
	v_max3_f32 v126, |v36|, 0, |v37|
	v_max3_f32 v126, v126, |v38|, |v39|
	v_max3_f32 v126, v126, |v28|, |v29|
	v_max3_f32 v126, v126, |v30|, |v31|
	s_waitcnt lgkmcnt(0)
	v_max_f32_e32 v129, v129, v129
	v_max_f32_e32 v3, v3, v129
	s_nop 1
	v_max_f32_dpp v4, v4, v4 quad_perm:[1,0,3,2] row_mask:0xf bank_mask:0xf
	s_nop 1
	v_max_f32_dpp v4, v4, v4 quad_perm:[2,3,0,1] row_mask:0xf bank_mask:0xf
	s_nop 1
	v_max_f32_dpp v4, v4, v4 row_half_mirror row_mask:0xf bank_mask:0xf
	s_nop 1
	v_max_f32_dpp v4, v4, v4 row_ror:8 row_mask:0xf bank_mask:0xf
	v_mov_b32_e32 v129, v4
	s_nop 1
	v_permlane16_swap_b32_e32 v4, v129
	s_nop 0
	v_max_f32_e32 v4, v4, v129
	v_mov_b32_e32 v129, v4
	s_nop 1
	v_permlane32_swap_b32_e32 v4, v129
	s_nop 0
	v_max_f32_e32 v4, v4, v129
	v_mov_b32_e32 v129, v4
	v_lshlrev_b32_e32 v16, 16, v8
	v_and_b32_e32 v17, 0xffff0000, v8
	v_lshlrev_b32_e32 v18, 16, v9
	v_and_b32_e32 v19, 0xffff0000, v9
	s_waitcnt lgkmcnt(0)
	v_max_f32_e32 v129, v129, v129
	v_max_f32_e32 v4, v4, v129
	s_nop 1
	v_max_f32_dpp v5, v5, v5 quad_perm:[1,0,3,2] row_mask:0xf bank_mask:0xf
	s_nop 1
	v_max_f32_dpp v5, v5, v5 quad_perm:[2,3,0,1] row_mask:0xf bank_mask:0xf
	s_nop 1
	v_max_f32_dpp v5, v5, v5 row_half_mirror row_mask:0xf bank_mask:0xf
	s_nop 1
	v_max_f32_dpp v5, v5, v5 row_ror:8 row_mask:0xf bank_mask:0xf
	v_mov_b32_e32 v129, v5
	s_nop 1
	v_permlane16_swap_b32_e32 v5, v129
	s_nop 0
	v_max_f32_e32 v5, v5, v129
	v_mov_b32_e32 v129, v5
	s_nop 1
	v_permlane32_swap_b32_e32 v5, v129
	s_nop 0
	v_max_f32_e32 v5, v5, v129
	v_mov_b32_e32 v129, v5
	v_max3_f32 v127, |v16|, 0, |v17|
	v_max3_f32 v128, |v20|, 0, |v21|
	v_lshlrev_b32_e32 v8, 16, v10
	v_and_b32_e32 v9, 0xffff0000, v10
	s_waitcnt lgkmcnt(0)
	v_max_f32_e32 v129, v129, v129
	v_max_f32_e32 v5, v5, v129
	s_nop 1
	v_max_f32_dpp v124, v124, v124 quad_perm:[1,0,3,2] row_mask:0xf bank_mask:0xf
	s_nop 1
	v_max_f32_dpp v124, v124, v124 quad_perm:[2,3,0,1] row_mask:0xf bank_mask:0xf
	s_nop 1
	v_max_f32_dpp v124, v124, v124 row_half_mirror row_mask:0xf bank_mask:0xf
	s_nop 1
	v_max_f32_dpp v124, v124, v124 row_ror:8 row_mask:0xf bank_mask:0xf
	v_mov_b32_e32 v129, v124
	s_nop 1
	v_permlane16_swap_b32_e32 v124, v129
	s_nop 0
	v_max_f32_e32 v124, v124, v129
	v_mov_b32_e32 v129, v124
	s_nop 1
	v_permlane32_swap_b32_e32 v124, v129
	s_nop 0
	v_max_f32_e32 v124, v124, v129
	v_mov_b32_e32 v129, v124
	v_lshlrev_b32_e32 v12, 16, v14
	v_and_b32_e32 v13, 0xffff0000, v14
	v_max3_f32 v127, v127, |v18|, |v19|
	v_max3_f32 v128, v128, |v22|, |v23|
	s_waitcnt lgkmcnt(0)
	v_max_f32_e32 v129, v129, v129
	v_max_f32_e32 v124, v124, v129
	s_nop 1
	v_max_f32_dpp v125, v125, v125 quad_perm:[1,0,3,2] row_mask:0xf bank_mask:0xf
	s_nop 1
	v_max_f32_dpp v125, v125, v125 quad_perm:[2,3,0,1] row_mask:0xf bank_mask:0xf
	s_nop 1
	v_max_f32_dpp v125, v125, v125 row_half_mirror row_mask:0xf bank_mask:0xf
	s_nop 1
	v_max_f32_dpp v125, v125, v125 row_ror:8 row_mask:0xf bank_mask:0xf
	v_mov_b32_e32 v129, v125
	s_nop 1
	v_permlane16_swap_b32_e32 v125, v129
	s_nop 0
	v_max_f32_e32 v125, v125, v129
	v_mov_b32_e32 v129, v125
	s_nop 1
	v_permlane32_swap_b32_e32 v125, v129
	s_nop 0
	v_max_f32_e32 v125, v125, v129
	v_mov_b32_e32 v129, v125
	v_lshlrev_b32_e32 v10, 16, v11
	v_and_b32_e32 v11, 0xffff0000, v11
	v_lshlrev_b32_e32 v14, 16, v15
	v_and_b32_e32 v15, 0xffff0000, v15
	s_waitcnt lgkmcnt(0)
	v_max_f32_e32 v129, v129, v129
	v_max_f32_e32 v125, v125, v129
	s_nop 1
	v_max_f32_dpp v126, v126, v126 quad_perm:[1,0,3,2] row_mask:0xf bank_mask:0xf
	s_nop 1
	v_max_f32_dpp v126, v126, v126 quad_perm:[2,3,0,1] row_mask:0xf bank_mask:0xf
	s_nop 1
	v_max_f32_dpp v126, v126, v126 row_half_mirror row_mask:0xf bank_mask:0xf
	s_nop 1
	v_max_f32_dpp v126, v126, v126 row_ror:8 row_mask:0xf bank_mask:0xf
	v_mov_b32_e32 v129, v126
	s_nop 1
	v_permlane16_swap_b32_e32 v126, v129
	s_nop 0
	v_max_f32_e32 v126, v126, v129
	v_mov_b32_e32 v129, v126
	s_nop 1
	v_permlane32_swap_b32_e32 v126, v129
	s_nop 0
	v_max_f32_e32 v126, v126, v129
	v_mov_b32_e32 v129, v126
	v_max3_f32 v127, v127, |v8|, |v9|
	v_max3_f32 v128, v128, |v12|, |v13|
	v_max3_f32 v127, v127, |v10|, |v11|
	v_max3_f32 v128, v128, |v14|, |v15|
	s_waitcnt lgkmcnt(0)
	v_max_f32_e32 v129, v129, v129
	v_max_f32_e32 v126, v126, v129
	s_nop 1
	v_max_f32_dpp v127, v127, v127 quad_perm:[1,0,3,2] row_mask:0xf bank_mask:0xf
	s_nop 1
	v_max_f32_dpp v127, v127, v127 quad_perm:[2,3,0,1] row_mask:0xf bank_mask:0xf
	s_nop 1
	v_max_f32_dpp v127, v127, v127 row_half_mirror row_mask:0xf bank_mask:0xf
	s_nop 1
	v_max_f32_dpp v127, v127, v127 row_ror:8 row_mask:0xf bank_mask:0xf
	v_mov_b32_e32 v129, v127
	s_nop 1
	v_permlane16_swap_b32_e32 v127, v129
	s_nop 0
	v_max_f32_e32 v127, v127, v129
	v_mov_b32_e32 v129, v127
	s_nop 1
	v_permlane32_swap_b32_e32 v127, v129
	s_nop 0
	v_max_f32_e32 v127, v127, v129
	v_mov_b32_e32 v129, v127
	s_nop 1
	v_max_f32_dpp v128, v128, v128 quad_perm:[1,0,3,2] row_mask:0xf bank_mask:0xf
	s_nop 1
	v_max_f32_dpp v128, v128, v128 quad_perm:[2,3,0,1] row_mask:0xf bank_mask:0xf
	s_nop 1
	v_max_f32_dpp v128, v128, v128 row_half_mirror row_mask:0xf bank_mask:0xf
	s_nop 1
	v_max_f32_dpp v128, v128, v128 row_ror:8 row_mask:0xf bank_mask:0xf
	v_mov_b32_e32 v121, v128
	s_nop 1
	v_permlane16_swap_b32_e32 v128, v121
	s_nop 0
	v_max_f32_e32 v128, v128, v121
	v_mov_b32_e32 v121, v128
	s_nop 1
	v_permlane32_swap_b32_e32 v128, v121
	s_nop 0
	v_max_f32_e32 v128, v128, v121
	v_mov_b32_e32 v121, v128
	s_waitcnt lgkmcnt(0)
	v_max_f32_e32 v129, v129, v129
	s_waitcnt lgkmcnt(0)
	v_max_f32_e32 v121, v121, v121
	v_max_f32_e32 v121, v128, v121
	v_mov_b32_e32 v128, v3
	v_max_f32_e32 v127, v127, v129
	s_waitcnt lgkmcnt(0)
	v_max_f32_e32 v128, v128, v128
	v_max_f32_e32 v3, v3, v128
	v_mov_b32_e32 v128, v4
	s_waitcnt lgkmcnt(0)
	v_max_f32_e32 v128, v128, v128
	v_max_f32_e32 v4, v4, v128
	v_mov_b32_e32 v128, v5
	s_waitcnt lgkmcnt(0)
	v_max_f32_e32 v128, v128, v128
	v_max_f32_e32 v5, v5, v128
	v_mov_b32_e32 v128, v124
	s_waitcnt lgkmcnt(0)
	v_max_f32_e32 v128, v128, v128
	v_max_f32_e32 v124, v124, v128
	v_mov_b32_e32 v128, v125
	s_waitcnt lgkmcnt(0)
	v_max_f32_e32 v128, v128, v128
	v_max_f32_e32 v125, v125, v128
	v_mov_b32_e32 v128, v126
	s_waitcnt lgkmcnt(0)
	v_max_f32_e32 v128, v128, v128
	v_max_f32_e32 v126, v126, v128
	v_mov_b32_e32 v128, v127
	v_mov_b32_e32 v120, v121
	s_waitcnt lgkmcnt(0)
	v_max_f32_e32 v128, v128, v128
	s_waitcnt lgkmcnt(0)
	v_max_f32_e32 v120, v120, v120
	v_max_f32_e32 v120, v121, v120
	v_mov_b32_e32 v121, v3
	v_max_f32_e32 v127, v127, v128
	s_waitcnt lgkmcnt(0)
	v_max_f32_e32 v121, v121, v121
	v_max_f32_e32 v3, v3, v121
	v_mov_b32_e32 v121, v4
	s_waitcnt lgkmcnt(0)
	v_max_f32_e32 v121, v121, v121
	v_max_f32_e32 v4, v4, v121
	v_mov_b32_e32 v121, v5
	s_waitcnt lgkmcnt(0)
	v_max_f32_e32 v121, v121, v121
	v_max_f32_e32 v5, v5, v121
	v_mov_b32_e32 v121, v124
	s_waitcnt lgkmcnt(0)
	v_max_f32_e32 v121, v121, v121
	v_max_f32_e32 v121, v124, v121
	v_mov_b32_e32 v124, v125
	s_waitcnt lgkmcnt(0)
	v_max_f32_e32 v124, v124, v124
	v_max_f32_e32 v124, v125, v124
	v_mov_b32_e32 v125, v126
	s_waitcnt lgkmcnt(0)
	v_max_f32_e32 v125, v125, v125
	v_max_f32_e32 v125, v126, v125
	v_mov_b32_e32 v126, v127
	v_mov_b32_e32 v119, v120
	s_waitcnt lgkmcnt(0)
	v_max_f32_e32 v126, v126, v126
	s_waitcnt lgkmcnt(0)
	v_max_f32_e32 v119, v119, v119
	v_max_f32_e32 v119, v120, v119
	v_mov_b32_e32 v120, v3
	v_max_f32_e32 v126, v127, v126
	s_waitcnt lgkmcnt(0)
	v_max_f32_e32 v120, v120, v120
	v_max_f32_e32 v3, v3, v120
	v_mov_b32_e32 v120, v4
	s_waitcnt lgkmcnt(0)
	v_max_f32_e32 v120, v120, v120
	v_max_f32_e32 v4, v4, v120
	v_mov_b32_e32 v120, v5
	s_waitcnt lgkmcnt(0)
	v_max_f32_e32 v120, v120, v120
	v_max_f32_e32 v5, v5, v120
	v_mov_b32_e32 v120, v121
	s_waitcnt lgkmcnt(0)
	v_max_f32_e32 v120, v120, v120
	v_max_f32_e32 v120, v121, v120
	v_mov_b32_e32 v121, v124
	s_waitcnt lgkmcnt(0)
	v_max_f32_e32 v121, v121, v121
	v_max_f32_e32 v121, v124, v121
	v_mov_b32_e32 v124, v125
	s_waitcnt lgkmcnt(0)
	v_max_f32_e32 v124, v124, v124
	v_max_f32_e32 v128, v125, v124
	v_mov_b32_e32 v124, v126
	v_mov_b32_e32 v118, v119
	s_waitcnt lgkmcnt(0)
	v_max_f32_e32 v124, v124, v124
	s_waitcnt lgkmcnt(0)
	v_max_f32_e32 v118, v118, v118
	v_max_f32_e32 v119, v119, v118
	v_mov_b32_e32 v118, v3
	v_max_f32_e32 v126, v126, v124
	s_waitcnt lgkmcnt(0)
	v_max_f32_e32 v118, v118, v118
	v_max_f32_e32 v132, v3, v118
	v_mov_b32_e32 v3, v4
	v_mov_b32_e32 v133, v132
	s_waitcnt lgkmcnt(0)
	v_max_f32_e32 v3, v3, v3
	v_max_f32_e32 v129, v4, v3
	v_mov_b32_e32 v3, v5
	v_mov_b32_e32 v131, v129
	s_waitcnt lgkmcnt(0)
	v_max3_f32 v132, v132, v133, s72
	s_waitcnt lgkmcnt(0)
	v_max_f32_e32 v3, v3, v3
	v_max_f32_e32 v127, v5, v3
	v_mov_b32_e32 v3, v120
	v_mov_b32_e32 v130, v127
	s_waitcnt lgkmcnt(0)
	v_max_f32_e32 v3, v3, v3
	v_max_f32_e32 v125, v120, v3
	v_mov_b32_e32 v3, v121
	s_waitcnt lgkmcnt(0)
	v_max_f32_e32 v3, v3, v3
	v_max_f32_e32 v124, v121, v3
	v_mov_b32_e32 v3, v128
	s_waitcnt lgkmcnt(0)
	v_max_f32_e32 v3, v3, v3
	v_max_f32_e32 v120, v128, v3
	v_mov_b32_e32 v3, v126
	v_mov_b32_e32 v128, v125
	v_mov_b32_e32 v121, v120
	s_waitcnt lgkmcnt(0)
	v_max_f32_e32 v3, v3, v3
	v_max_f32_e32 v118, v126, v3
	v_mov_b32_e32 v3, v119
	v_mov_b32_e32 v126, v124
	s_waitcnt lgkmcnt(0)
	v_max_f32_e32 v3, v3, v3
	v_max_f32_e32 v116, v119, v3
	v_mov_b32_e32 v119, v118
	v_mov_b32_e32 v117, v116
	v_ashrrev_i32_e32 v3, 31, v2
	v_lshl_add_u64 v[4:5], s[36:37], 0, v[2:3]
	s_and_saveexec_b64 s[12:13], s[6:7]
	s_cbranch_execz .LBB0_601
	v_lshl_add_u64 v[2:3], v[4:5], 2, s[8:9]
	v_mul_f32_e32 v133, 0x3c010204, v132
	global_store_dword v[2:3], v133, off
